# final-norm rewrite + nt on pool/PLE/Wo epilogue stores + start stagger of Wo phase by blockIdx bit 3
# baseline (speedup 1.0000x reference)
.LBB0_498:
	v_mov_b32_e32 v188, v0
	s_lshl_b32 s34, s34, 8
	v_readfirstlane_b32 s36, v188
	s_ashr_i32 s29, s36, 6
	s_ashr_i32 s36, s36, 2
	s_mul_i32 s27, s29, 0xb00
	s_and_b32 s29, s29, 3
	s_andn2_b32 s36, s36, 63
	s_lshl_b32 s37, s35, 8
	s_lshl_b32 s38, s29, 6
	s_add_i32 s46, s36, s34
	s_add_i32 s27, s27, 0
	s_or_b32 s38, s38, s37
	s_ashr_i32 s47, s46, 31
	s_add_i32 s27, s27, 0x20000
	s_ashr_i32 s39, s38, 31
	s_lshl_b64 s[40:41], s[46:47], 12
	s_add_u32 s37, s10, s40
	s_addc_u32 s41, s11, s41
	s_lshl_b64 s[44:45], s[38:39], 2
	v_and_b32_e32 v196, 63, v188
	s_add_u32 s40, s37, s44
	v_bfe_u32 v189, v188, 3, 3
	s_addc_u32 s41, s41, s45
	v_lshlrev_b32_e32 v138, 12, v189
	v_lshlrev_b32_e32 v197, 4, v196
	v_or_b32_e32 v190, 8, v189
	v_and_b32_e32 v144, 0x70, v197
	v_mov_b32_e32 v145, v139
	v_lshlrev_b32_e32 v146, 12, v190
	v_mov_b32_e32 v147, v139
	v_lshl_add_u64 v[148:149], s[40:41], 0, v[138:139]
	v_lshl_add_u64 v[164:165], v[148:149], 0, v[144:145]
	v_lshl_add_u64 v[152:153], s[40:41], 0, v[146:147]
	global_load_dwordx4 v[148:151], v[164:165], off
	v_lshl_add_u64 v[168:169], v[152:153], 0, v[144:145]
	global_load_dwordx4 v[152:155], v[168:169], off
	v_bfe_u32 v198, v188, 4, 2
	s_add_u32 s42, s12, s44
	s_addc_u32 s43, s13, s45
	v_lshlrev_b32_e32 v201, 5, v198
	global_load_dwordx4 v[156:159], v201, s[42:43]
	global_load_dwordx4 v[160:163], v201, s[42:43] offset:16
	s_nop 0
	global_load_dwordx4 v[164:167], v[164:165], off offset:128
	s_nop 0
	global_load_dwordx4 v[168:171], v[168:169], off offset:128
	s_nop 0
	global_load_dwordx4 v[172:175], v201, s[42:43] offset:128
	global_load_dwordx4 v[176:179], v201, s[42:43] offset:144
	v_mul_u32_u24_e32 v180, 0x90, v189
	v_and_b32_e32 v199, 15, v188
	v_add3_u32 v200, s27, v180, v144
	v_mov_b32_e32 v180, s27
	v_mad_u32_u24 v203, v199, s67, v180
	v_add_u32_e32 v206, v203, v201
	v_mov_b32_e32 v184, v139
	v_mov_b32_e32 v185, v139
	v_mov_b32_e32 v186, v139
	v_mov_b32_e32 v187, v139
	v_and_b32_e32 v191, 48, v188
	s_lshl_b64 s[40:41], s[46:47], 11
	s_add_u32 s37, s56, s40
	v_add_u32_e32 v203, v203, v191
	s_addc_u32 s49, s57, s41
	s_lshl_b64 s[40:41], s[38:39], 1
	s_add_u32 s48, s37, s40
	s_addc_u32 s49, s49, s41
	v_lshlrev_b32_e32 v204, 3, v198
	v_mov_b32_e32 v191, v139
	v_mov_b32_e32 v208, v139
	v_mov_b32_e32 v209, v139
	s_waitcnt vmcnt(0)
	ds_write_b128 v200, v[148:151]
	ds_write_b128 v200, v[152:155] offset:1152
	ds_read_b128 v[148:151], v206
	ds_read_b128 v[180:183], v206 offset:16
	s_waitcnt lgkmcnt(1)
	v_pk_fma_f32 v[152:153], v[124:125], v[158:159], v[150:151]
	v_pk_fma_f32 v[154:155], v[122:123], v[156:157], v[148:149]
	s_waitcnt lgkmcnt(0)
	v_pk_fma_f32 v[150:151], v[126:127], v[160:161], v[180:181]
	v_pk_fma_f32 v[148:149], v[128:129], v[162:163], v[182:183]
	v_cvt_pk_bf16_f32 v156, v154, v155
	v_cvt_pk_bf16_f32 v157, v152, v153
	v_cvt_pk_bf16_f32 v158, v150, v151
	v_med3_f32 v122, v154, s68, v195
	v_cvt_pk_bf16_f32 v159, v148, v149
	v_med3_f32 v123, v150, s68, v195
	v_med3_f32 v124, v155, s68, v195
	v_med3_f32 v125, v151, s68, v195
	ds_write_b128 v200, v[164:167]
	ds_write_b128 v200, v[168:171] offset:1152
	v_cvt_pk_fp8_f32 v184, v122, v124
	v_cvt_pk_fp8_f32 v185, v123, v125
	ds_read_b128 v[124:127], v206
	ds_read_b128 v[160:163], v206 offset:16
	v_med3_f32 v128, v152, s68, v195
	v_med3_f32 v129, v148, s68, v195
	v_med3_f32 v180, v153, s68, v195
	v_med3_f32 v122, v149, s68, v195
	v_cvt_pk_fp8_f32 v184, v128, v180 op_sel:[0,0,1]
	v_cvt_pk_fp8_f32 v185, v129, v122 op_sel:[0,0,1]
	s_waitcnt lgkmcnt(1)
	v_pk_fma_f32 v[122:123], v[116:117], v[174:175], v[126:127]
	v_pk_fma_f32 v[126:127], v[114:115], v[172:173], v[124:125]
	s_waitcnt lgkmcnt(0)
	v_pk_fma_f32 v[128:129], v[118:119], v[176:177], v[160:161]
	v_pk_fma_f32 v[124:125], v[120:121], v[178:179], v[162:163]
	v_med3_f32 v118, v126, s68, v195
	v_med3_f32 v119, v128, s68, v195
	v_med3_f32 v120, v127, s68, v195
	v_med3_f32 v121, v129, s68, v195
	v_cvt_pk_fp8_f32 v186, v118, v120
	v_cvt_pk_fp8_f32 v187, v119, v121
	v_cvt_pk_bf16_f32 v114, v126, v127
	v_cvt_pk_bf16_f32 v115, v122, v123
	v_cvt_pk_bf16_f32 v116, v128, v129
	v_cvt_pk_bf16_f32 v117, v124, v125
	v_med3_f32 v160, v122, s68, v195
	v_med3_f32 v161, v124, s68, v195
	v_med3_f32 v118, v123, s68, v195
	v_med3_f32 v119, v125, s68, v195
	ds_write_b128 v203, v[156:159]
	ds_write_b128 v203, v[114:117] offset:64
	v_cvt_pk_fp8_f32 v186, v160, v118 op_sel:[0,0,1]
	v_cvt_pk_fp8_f32 v187, v161, v119 op_sel:[0,0,1]
	ds_read_b128 v[116:119], v200
	ds_read_b128 v[156:159], v200 offset:1152
	v_lshlrev_b32_e32 v114, 11, v189
	v_mov_b32_e32 v115, v139
	v_lshl_add_u64 v[120:121], s[48:49], 0, v[114:115]
	v_lshl_add_u64 v[120:121], v[120:121], 0, v[144:145]
	s_waitcnt lgkmcnt(1)
	global_store_dwordx4 v[120:121], v[116:119], off nt
	v_mov_b32_e32 v121, v139
	v_mov_b32_e32 v189, v139
	v_lshlrev_b32_e32 v116, 11, v190
	v_mov_b32_e32 v117, v139
	v_lshl_add_u64 v[118:119], s[48:49], 0, v[116:117]
	s_lshl_b64 s[48:49], s[46:47], 10
	v_lshl_add_u64 v[118:119], v[118:119], 0, v[144:145]
	s_add_u32 s37, s60, s48
	s_waitcnt lgkmcnt(0)
	global_store_dwordx4 v[118:119], v[156:159], off nt
	s_addc_u32 s47, s61, s49
	v_mul_u32_u24_e32 v118, 0x50, v199
	v_bfe_u32 v119, v188, 2, 4
	s_add_u32 s48, s37, s38
	v_add3_u32 v204, s27, v118, v204
	v_mul_u32_u24_e32 v120, 0x50, v119
	v_and_b32_e32 v118, 48, v197
	s_addc_u32 s49, s47, s39
	v_add3_u32 v205, s27, v120, v118
	v_lshlrev_b32_e32 v120, 10, v119
	v_lshl_add_u64 v[160:161], s[48:49], 0, v[120:121]
	s_or_b32 s48, s46, 16
	ds_write2_b64 v204, v[184:185], v[186:187] offset1:4
	s_ashr_i32 s49, s48, 31
	ds_read_b128 v[156:159], v205
	s_lshl_b64 s[70:71], s[48:49], 12
	s_add_u32 s37, s10, s70
	s_addc_u32 s47, s11, s71
	v_mov_b32_e32 v119, v139
	s_add_u32 s70, s37, s44
	v_lshl_add_u64 v[160:161], v[160:161], 0, v[118:119]
	s_addc_u32 s71, s47, s45
	s_waitcnt lgkmcnt(0)
	global_store_dwordx4 v[160:161], v[156:159], off nt
	v_lshl_add_u64 v[160:161], s[70:71], 0, v[146:147]
	v_lshl_add_u64 v[176:177], v[160:161], 0, v[144:145]
	v_lshl_add_u64 v[156:157], s[70:71], 0, v[138:139]
	v_lshl_add_u64 v[172:173], v[156:157], 0, v[144:145]
	global_load_dwordx4 v[156:159], v[172:173], off
	global_load_dwordx4 v[160:163], v[176:177], off
	global_load_dwordx4 v[164:167], v201, s[42:43]
	global_load_dwordx4 v[168:171], v201, s[42:43] offset:16
	s_nop 0
	global_load_dwordx4 v[172:175], v[172:173], off offset:128
	s_nop 0
	global_load_dwordx4 v[176:179], v[176:177], off offset:128
	s_nop 0
	global_load_dwordx4 v[180:183], v201, s[42:43] offset:128
	global_load_dwordx4 v[184:187], v201, s[42:43] offset:144
	s_waitcnt vmcnt(7)
	ds_write_b128 v200, v[156:159]
	s_waitcnt vmcnt(6)
	ds_write_b128 v200, v[160:163] offset:1152
	ds_read_b128 v[156:159], v206
	ds_read_b128 v[160:163], v206 offset:16
	v_mov_b32_e32 v188, v139
	s_lshl_b64 s[70:71], s[48:49], 11
	v_mov_b32_e32 v190, v139
	s_waitcnt vmcnt(5) lgkmcnt(1)
	v_pk_fma_f32 v[156:157], v[106:107], v[164:165], v[156:157]
	s_waitcnt vmcnt(4) lgkmcnt(0)
	v_pk_fma_f32 v[110:111], v[110:111], v[168:169], v[160:161]
	v_pk_fma_f32 v[108:109], v[108:109], v[166:167], v[158:159]
	v_pk_fma_f32 v[106:107], v[112:113], v[170:171], v[162:163]
	v_cvt_pk_bf16_f32 v158, v156, v157
	v_cvt_pk_bf16_f32 v159, v108, v109
	v_cvt_pk_bf16_f32 v160, v110, v111
	v_med3_f32 v112, v156, s68, v195
	v_cvt_pk_bf16_f32 v161, v106, v107
	v_med3_f32 v113, v110, s68, v195
	v_med3_f32 v162, v157, s68, v195
	v_med3_f32 v163, v111, s68, v195
	s_waitcnt vmcnt(3)
	ds_write_b128 v200, v[172:175]
	s_waitcnt vmcnt(2)
	ds_write_b128 v200, v[176:179] offset:1152
	v_cvt_pk_fp8_f32 v188, v112, v162
	v_cvt_pk_fp8_f32 v189, v113, v163
	ds_read_b128 v[162:165], v206
	ds_read_b128 v[166:169], v206 offset:16
	v_med3_f32 v171, v106, s68, v195
	v_med3_f32 v112, v107, s68, v195
	v_cvt_pk_fp8_f32 v189, v171, v112 op_sel:[0,0,1]
	s_waitcnt vmcnt(1) lgkmcnt(1)
	v_pk_fma_f32 v[112:113], v[98:99], v[180:181], v[162:163]
	s_waitcnt vmcnt(0) lgkmcnt(0)
	v_pk_fma_f32 v[102:103], v[102:103], v[184:185], v[166:167]
	v_pk_fma_f32 v[98:99], v[104:105], v[186:187], v[168:169]
	v_med3_f32 v105, v102, s68, v195
	v_med3_f32 v167, v103, s68, v195
	s_add_u32 s37, s56, s70
	v_pk_fma_f32 v[100:101], v[100:101], v[182:183], v[164:165]
	v_cvt_pk_bf16_f32 v162, v112, v113
	v_med3_f32 v104, v112, s68, v195
	v_cvt_pk_bf16_f32 v163, v100, v101
	v_cvt_pk_bf16_f32 v164, v102, v103
	v_cvt_pk_bf16_f32 v165, v98, v99
	v_med3_f32 v166, v113, s68, v195
	v_cvt_pk_fp8_f32 v191, v105, v167
	ds_write_b128 v203, v[158:161]
	ds_write_b128 v203, v[162:165] offset:64
	s_addc_u32 s47, s57, s71
	v_cvt_pk_fp8_f32 v190, v104, v166
	ds_read_b128 v[158:161], v200
	ds_read_b128 v[162:165], v200 offset:1152
	s_add_u32 s70, s37, s40
	v_med3_f32 v170, v108, s68, v195
	v_med3_f32 v207, v109, s68, v195
	v_med3_f32 v169, v98, s68, v195
	v_med3_f32 v104, v99, s68, v195
	s_addc_u32 s71, s47, s41
	s_lshl_b64 s[48:49], s[48:49], 10
	v_cvt_pk_fp8_f32 v188, v170, v207 op_sel:[0,0,1]
	v_med3_f32 v168, v100, s68, v195
	v_med3_f32 v170, v101, s68, v195
	v_cvt_pk_fp8_f32 v191, v169, v104 op_sel:[0,0,1]
	v_lshl_add_u64 v[104:105], s[70:71], 0, v[114:115]
	s_add_u32 s37, s60, s48
	v_cvt_pk_fp8_f32 v190, v168, v170 op_sel:[0,0,1]
	v_lshl_add_u64 v[104:105], v[104:105], 0, v[144:145]
	s_addc_u32 s47, s61, s49
	s_waitcnt lgkmcnt(1)
	global_store_dwordx4 v[104:105], v[158:161], off nt
	v_lshl_add_u64 v[104:105], s[70:71], 0, v[116:117]
	s_add_u32 s48, s37, s38
	v_lshl_add_u64 v[104:105], v[104:105], 0, v[144:145]
	s_addc_u32 s49, s47, s39
	s_waitcnt lgkmcnt(0)
	global_store_dwordx4 v[104:105], v[162:165], off nt
	v_lshl_add_u64 v[104:105], s[48:49], 0, v[120:121]
	s_or_b32 s48, s46, 32
	ds_write2_b64 v204, v[188:189], v[190:191] offset1:4
	s_ashr_i32 s49, s48, 31
	ds_read_b128 v[158:161], v205
	s_lshl_b64 s[70:71], s[48:49], 12
	s_add_u32 s37, s10, s70
	s_addc_u32 s47, s11, s71
	s_add_u32 s70, s37, s44
	v_lshl_add_u64 v[104:105], v[104:105], 0, v[118:119]
	s_addc_u32 s71, s47, s45
	s_waitcnt lgkmcnt(0)
	global_store_dwordx4 v[104:105], v[158:161], off nt
	v_lshl_add_u64 v[104:105], s[70:71], 0, v[138:139]
	v_lshl_add_u64 v[104:105], v[104:105], 0, v[144:145]
	global_load_dwordx4 v[158:161], v[104:105], off
	v_lshl_add_u64 v[162:163], s[70:71], 0, v[146:147]
	v_lshl_add_u64 v[178:179], v[162:163], 0, v[144:145]
	global_load_dwordx4 v[162:165], v[178:179], off
	global_load_dwordx4 v[166:169], v201, s[42:43]
	global_load_dwordx4 v[170:173], v201, s[42:43] offset:16
	global_load_dwordx4 v[174:177], v[104:105], off offset:128
	s_nop 0
	global_load_dwordx4 v[178:181], v[178:179], off offset:128
	s_nop 0
	global_load_dwordx4 v[182:185], v201, s[42:43] offset:128
	global_load_dwordx4 v[186:189], v201, s[42:43] offset:144
	s_lshl_b64 s[70:71], s[48:49], 11
	s_add_u32 s37, s56, s70
	s_addc_u32 s47, s57, s71
	s_add_u32 s70, s37, s40
	s_addc_u32 s71, s47, s41
	s_lshl_b64 s[48:49], s[48:49], 10
	s_waitcnt vmcnt(7)
	ds_write_b128 v200, v[158:161]
	s_waitcnt vmcnt(6)
	ds_write_b128 v200, v[162:165] offset:1152
	s_add_u32 s37, s60, s48
	ds_read_b128 v[158:161], v206
	ds_read_b128 v[162:165], v206 offset:16
	s_addc_u32 s47, s61, s49
	v_lshl_add_u64 v[104:105], s[70:71], 0, v[114:115]
	v_lshl_add_u64 v[210:211], s[70:71], 0, v[116:117]
	s_add_u32 s70, s37, s38
	s_addc_u32 s71, s47, s39
	v_lshl_add_u64 v[212:213], v[104:105], 0, v[144:145]
	v_lshl_add_u64 v[104:105], s[70:71], 0, v[120:121]
	v_lshl_add_u64 v[214:215], v[104:105], 0, v[118:119]
	s_waitcnt vmcnt(5) lgkmcnt(1)
	v_pk_fma_f32 v[104:105], v[90:91], v[166:167], v[158:159]
	s_waitcnt vmcnt(4) lgkmcnt(0)
	v_pk_fma_f32 v[94:95], v[94:95], v[170:171], v[162:163]
	v_mov_b32_e32 v190, v139
	v_mov_b32_e32 v191, v139
	v_pk_fma_f32 v[92:93], v[92:93], v[168:169], v[160:161]
	v_pk_fma_f32 v[90:91], v[96:97], v[172:173], v[164:165]
	v_cvt_pk_bf16_f32 v158, v104, v105
	v_cvt_pk_bf16_f32 v159, v92, v93
	v_cvt_pk_bf16_f32 v160, v94, v95
	v_med3_f32 v96, v104, s68, v195
	v_cvt_pk_bf16_f32 v161, v90, v91
	v_med3_f32 v97, v94, s68, v195
	v_med3_f32 v162, v105, s68, v195
	v_med3_f32 v163, v95, s68, v195
	s_waitcnt vmcnt(3)
	ds_write_b128 v200, v[174:177]
	s_waitcnt vmcnt(2)
	ds_write_b128 v200, v[178:181] offset:1152
	v_cvt_pk_fp8_f32 v190, v96, v162
	v_cvt_pk_fp8_f32 v191, v97, v163
	ds_read_b128 v[162:165], v206
	ds_read_b128 v[166:169], v206 offset:16
	v_med3_f32 v171, v90, s68, v195
	v_med3_f32 v96, v91, s68, v195
	v_cvt_pk_fp8_f32 v191, v171, v96 op_sel:[0,0,1]
	s_waitcnt vmcnt(1) lgkmcnt(1)
	v_pk_fma_f32 v[96:97], v[82:83], v[182:183], v[162:163]
	s_waitcnt vmcnt(0) lgkmcnt(0)
	v_pk_fma_f32 v[86:87], v[86:87], v[186:187], v[166:167]
	v_pk_fma_f32 v[82:83], v[88:89], v[188:189], v[168:169]
	v_med3_f32 v88, v96, s68, v195
	v_med3_f32 v89, v86, s68, v195
	v_med3_f32 v166, v97, s68, v195
	v_med3_f32 v167, v87, s68, v195
	v_cvt_pk_fp8_f32 v208, v88, v166
	v_cvt_pk_fp8_f32 v209, v89, v167
	v_med3_f32 v170, v92, s68, v195
	v_med3_f32 v172, v93, s68, v195
	v_pk_fma_f32 v[84:85], v[84:85], v[184:185], v[164:165]
	v_cvt_pk_fp8_f32 v190, v170, v172 op_sel:[0,0,1]
	v_med3_f32 v168, v84, s68, v195
	v_med3_f32 v169, v82, s68, v195
	v_med3_f32 v170, v85, s68, v195
	v_med3_f32 v88, v83, s68, v195
	v_cvt_pk_fp8_f32 v208, v168, v170 op_sel:[0,0,1]
	v_cvt_pk_fp8_f32 v209, v169, v88 op_sel:[0,0,1]
	s_or_b32 s48, s46, 48
	s_ashr_i32 s49, s48, 31
	v_cvt_pk_bf16_f32 v162, v96, v97
	v_cvt_pk_bf16_f32 v163, v84, v85
	v_cvt_pk_bf16_f32 v164, v86, v87
	v_cvt_pk_bf16_f32 v165, v82, v83
	ds_write_b128 v203, v[158:161]
	ds_write_b128 v203, v[162:165] offset:64
	ds_read_b128 v[158:161], v200
	ds_read_b128 v[162:165], v200 offset:1152
	s_lshl_b64 s[70:71], s[48:49], 12
	ds_write2_b64 v204, v[190:191], v[208:209] offset1:4
	s_add_u32 s37, s10, s70
	ds_read_b128 v[166:169], v205
	s_addc_u32 s47, s11, s71
	s_add_u32 s70, s37, s44
	s_addc_u32 s71, s47, s45
	v_lshl_add_u64 v[210:211], v[210:211], 0, v[144:145]
	s_waitcnt lgkmcnt(3)
	global_store_dwordx4 v[212:213], v[158:161], off nt
	s_waitcnt lgkmcnt(2)
	global_store_dwordx4 v[210:211], v[162:165], off nt
	s_waitcnt lgkmcnt(0)
	global_store_dwordx4 v[214:215], v[166:169], off nt
	v_lshl_add_u64 v[88:89], s[70:71], 0, v[138:139]
	v_lshl_add_u64 v[88:89], v[88:89], 0, v[144:145]
	global_load_dwordx4 v[158:161], v[88:89], off
	v_lshl_add_u64 v[162:163], s[70:71], 0, v[146:147]
	v_lshl_add_u64 v[178:179], v[162:163], 0, v[144:145]
	global_load_dwordx4 v[162:165], v[178:179], off
	global_load_dwordx4 v[166:169], v201, s[42:43]
	global_load_dwordx4 v[170:173], v201, s[42:43] offset:16
	global_load_dwordx4 v[174:177], v[88:89], off offset:128
	s_nop 0
	global_load_dwordx4 v[178:181], v[178:179], off offset:128
	s_nop 0
	global_load_dwordx4 v[182:185], v201, s[42:43] offset:128
	global_load_dwordx4 v[186:189], v201, s[42:43] offset:144
	s_lshl_b64 s[70:71], s[48:49], 11
	s_add_u32 s37, s56, s70
	s_addc_u32 s47, s57, s71
	s_add_u32 s70, s37, s40
	s_addc_u32 s71, s47, s41
	v_lshl_add_u64 v[208:209], s[70:71], 0, v[116:117]
	s_waitcnt vmcnt(7)
	ds_write_b128 v200, v[158:161]
	s_waitcnt vmcnt(6)
	ds_write_b128 v200, v[162:165] offset:1152
	v_lshl_add_u64 v[216:217], v[208:209], 0, v[144:145]
	ds_read_b128 v[158:161], v206
	ds_read_b128 v[208:211], v206 offset:16
	s_lshl_b64 s[48:49], s[48:49], 10
	v_mov_b32_e32 v190, v139
	v_mov_b32_e32 v191, v139
	s_waitcnt vmcnt(5) lgkmcnt(1)
	v_pk_fma_f32 v[164:165], v[74:75], v[166:167], v[158:159]
	s_waitcnt vmcnt(4) lgkmcnt(0)
	v_pk_fma_f32 v[166:167], v[78:79], v[170:171], v[208:209]
	s_add_u32 s37, s60, s48
	v_pk_fma_f32 v[160:161], v[76:77], v[168:169], v[160:161]
	v_pk_fma_f32 v[162:163], v[80:81], v[172:173], v[210:211]
	v_cvt_pk_bf16_f32 v74, v164, v165
	v_cvt_pk_bf16_f32 v75, v160, v161
	v_cvt_pk_bf16_f32 v76, v166, v167
	v_med3_f32 v78, v164, s68, v195
	v_cvt_pk_bf16_f32 v77, v162, v163
	v_med3_f32 v79, v166, s68, v195
	v_med3_f32 v80, v165, s68, v195
	v_med3_f32 v81, v167, s68, v195
	s_waitcnt vmcnt(3)
	ds_write_b128 v200, v[174:177]
	s_waitcnt vmcnt(2)
	ds_write_b128 v200, v[178:181] offset:1152
	s_addc_u32 s47, s61, s49
	v_cvt_pk_fp8_f32 v190, v78, v80
	v_cvt_pk_fp8_f32 v191, v79, v81
	ds_read_b128 v[78:81], v206
	ds_read_b128 v[172:175], v206 offset:16
	v_lshl_add_u64 v[88:89], s[70:71], 0, v[114:115]
	s_add_u32 s70, s37, s38
	s_addc_u32 s71, s47, s39
	v_lshl_add_u64 v[214:215], v[88:89], 0, v[144:145]
	v_lshl_add_u64 v[88:89], s[70:71], 0, v[120:121]
	v_lshl_add_u64 v[218:219], v[88:89], 0, v[118:119]
	v_med3_f32 v88, v160, s68, v195
	v_med3_f32 v89, v162, s68, v195
	v_med3_f32 v158, v161, s68, v195
	v_med3_f32 v159, v163, s68, v195
	v_cvt_pk_fp8_f32 v190, v88, v158 op_sel:[0,0,1]
	v_cvt_pk_fp8_f32 v191, v89, v159 op_sel:[0,0,1]
	s_waitcnt vmcnt(1) lgkmcnt(1)
	v_pk_fma_f32 v[170:171], v[66:67], v[182:183], v[78:79]
	s_waitcnt vmcnt(0) lgkmcnt(0)
	v_pk_fma_f32 v[158:159], v[70:71], v[186:187], v[172:173]
	v_mov_b32_e32 v212, v139
	v_mov_b32_e32 v213, v139
	v_pk_fma_f32 v[88:89], v[72:73], v[188:189], v[174:175]
	v_med3_f32 v70, v170, s68, v195
	v_med3_f32 v71, v158, s68, v195
	v_med3_f32 v72, v171, s68, v195
	v_med3_f32 v73, v159, s68, v195
	v_cvt_pk_fp8_f32 v212, v70, v72
	v_cvt_pk_fp8_f32 v213, v71, v73
	v_pk_fma_f32 v[168:169], v[68:69], v[184:185], v[80:81]
	v_med3_f32 v79, v88, s68, v195
	v_med3_f32 v78, v168, s68, v195
	v_med3_f32 v80, v169, s68, v195
	v_med3_f32 v70, v89, s68, v195
	v_cvt_pk_fp8_f32 v212, v78, v80 op_sel:[0,0,1]
	v_cvt_pk_fp8_f32 v213, v79, v70 op_sel:[0,0,1]
	s_add_i32 s48, s46, 0x80
	s_ashr_i32 s49, s48, 31
	v_cvt_pk_bf16_f32 v66, v170, v171
	v_cvt_pk_bf16_f32 v67, v168, v169
	v_cvt_pk_bf16_f32 v68, v158, v159
	v_cvt_pk_bf16_f32 v69, v88, v89
	ds_write_b128 v203, v[74:77]
	ds_write_b128 v203, v[66:69] offset:64
	s_lshl_b64 s[70:71], s[48:49], 12
	ds_read_b128 v[66:69], v200
	ds_read_b128 v[70:73], v200 offset:1152
	s_add_u32 s37, s10, s70
	ds_write2_b64 v204, v[190:191], v[212:213] offset1:4
	s_addc_u32 s47, s11, s71
	ds_read_b128 v[74:77], v205
	s_add_u32 s70, s37, s44
	s_addc_u32 s71, s47, s45
	v_lshl_add_u64 v[220:221], s[70:71], 0, v[138:139]
	s_waitcnt lgkmcnt(3)
	global_store_dwordx4 v[214:215], v[66:69], off nt
	s_waitcnt lgkmcnt(2)
	global_store_dwordx4 v[216:217], v[70:73], off nt
	s_waitcnt lgkmcnt(0)
	global_store_dwordx4 v[218:219], v[74:77], off nt
	v_lshl_add_u64 v[222:223], s[70:71], 0, v[146:147]
	v_lshl_add_u64 v[172:173], v[220:221], 0, v[144:145]
	v_lshl_add_u64 v[174:175], v[222:223], 0, v[144:145]
	global_load_dwordx4 v[66:69], v[172:173], off
	global_load_dwordx4 v[70:73], v[174:175], off
	global_load_dwordx4 v[74:77], v201, s[42:43]
	global_load_dwordx4 v[78:81], v201, s[42:43] offset:16
	global_load_dwordx4 v[180:183], v[172:173], off offset:128
	global_load_dwordx4 v[184:187], v[174:175], off offset:128
	global_load_dwordx4 v[188:191], v201, s[42:43] offset:128
	global_load_dwordx4 v[208:211], v201, s[42:43] offset:144
	s_lshl_b64 s[70:71], s[48:49], 11
	s_add_u32 s37, s56, s70
	s_addc_u32 s47, s57, s71
	s_add_u32 s70, s37, s40
	s_waitcnt vmcnt(7)
	ds_write_b128 v200, v[66:69]
	s_waitcnt vmcnt(6)
	ds_write_b128 v200, v[70:73] offset:1152
	s_addc_u32 s71, s47, s41
	s_lshl_b64 s[48:49], s[48:49], 10
	ds_read_b128 v[66:69], v206
	ds_read_b128 v[70:73], v206 offset:16
	s_add_u32 s37, s60, s48
	s_addc_u32 s47, s61, s49
	v_lshl_add_u64 v[172:173], s[70:71], 0, v[114:115]
	v_lshl_add_u64 v[174:175], s[70:71], 0, v[116:117]
	s_add_u32 s70, s37, s38
	s_addc_u32 s71, s47, s39
	v_lshl_add_u64 v[216:217], v[172:173], 0, v[144:145]
	v_lshl_add_u64 v[172:173], s[70:71], 0, v[120:121]
	s_waitcnt vmcnt(5) lgkmcnt(1)
	v_pk_fma_f32 v[178:179], v[58:59], v[74:75], v[66:67]
	s_waitcnt vmcnt(4) lgkmcnt(0)
	v_pk_fma_f32 v[176:177], v[62:63], v[78:79], v[70:71]
	v_mov_b32_e32 v212, v139
	v_mov_b32_e32 v213, v139
	v_lshl_add_u64 v[218:219], v[174:175], 0, v[144:145]
	v_lshl_add_u64 v[220:221], v[172:173], 0, v[118:119]
	v_pk_fma_f32 v[174:175], v[60:61], v[76:77], v[68:69]
	v_pk_fma_f32 v[172:173], v[64:65], v[80:81], v[72:73]
	v_cvt_pk_bf16_f32 v58, v178, v179
	v_cvt_pk_bf16_f32 v59, v174, v175
	v_cvt_pk_bf16_f32 v60, v176, v177
	v_med3_f32 v62, v178, s68, v195
	v_cvt_pk_bf16_f32 v61, v172, v173
	v_med3_f32 v63, v176, s68, v195
	v_med3_f32 v64, v179, s68, v195
	v_med3_f32 v65, v177, s68, v195
	s_waitcnt vmcnt(3)
	ds_write_b128 v200, v[180:183]
	s_waitcnt vmcnt(2)
	ds_write_b128 v200, v[184:187] offset:1152
	v_cvt_pk_fp8_f32 v212, v62, v64
	v_cvt_pk_fp8_f32 v213, v63, v65
	ds_read_b128 v[62:65], v206
	ds_read_b128 v[66:69], v206 offset:16
	v_mov_b32_e32 v214, v139
	v_mov_b32_e32 v215, v139
	v_med3_f32 v70, v174, s68, v195
	s_waitcnt vmcnt(1) lgkmcnt(1)
	v_pk_fma_f32 v[186:187], v[50:51], v[188:189], v[62:63]
	s_waitcnt vmcnt(0) lgkmcnt(0)
	v_pk_fma_f32 v[184:185], v[54:55], v[208:209], v[66:67]
	v_pk_fma_f32 v[180:181], v[56:57], v[210:211], v[68:69]
	v_med3_f32 v54, v186, s68, v195
	v_med3_f32 v55, v184, s68, v195
	v_med3_f32 v56, v187, s68, v195
	v_med3_f32 v57, v185, s68, v195
	v_cvt_pk_fp8_f32 v214, v54, v56
	v_cvt_pk_fp8_f32 v215, v55, v57
	v_pk_fma_f32 v[182:183], v[52:53], v[190:191], v[64:65]
	v_med3_f32 v71, v172, s68, v195
	v_med3_f32 v72, v175, s68, v195
	v_med3_f32 v73, v173, s68, v195
	v_med3_f32 v62, v182, s68, v195
	v_med3_f32 v63, v180, s68, v195
	v_med3_f32 v64, v183, s68, v195
	v_med3_f32 v54, v181, s68, v195
	v_cvt_pk_fp8_f32 v212, v70, v72 op_sel:[0,0,1]
	v_cvt_pk_fp8_f32 v213, v71, v73 op_sel:[0,0,1]
	v_cvt_pk_fp8_f32 v214, v62, v64 op_sel:[0,0,1]
	v_cvt_pk_fp8_f32 v215, v63, v54 op_sel:[0,0,1]
	s_add_i32 s48, s46, 0x90
	s_ashr_i32 s49, s48, 31
	v_cvt_pk_bf16_f32 v50, v186, v187
	v_cvt_pk_bf16_f32 v51, v182, v183
	v_cvt_pk_bf16_f32 v52, v184, v185
	v_cvt_pk_bf16_f32 v53, v180, v181
	ds_write_b128 v203, v[58:61]
	ds_write_b128 v203, v[50:53] offset:64
	s_lshl_b64 s[70:71], s[48:49], 12
	ds_read_b128 v[50:53], v200
	ds_read_b128 v[54:57], v200 offset:1152
	s_add_u32 s37, s10, s70
	ds_write2_b64 v204, v[212:213], v[214:215] offset1:4
	s_addc_u32 s47, s11, s71
	ds_read_b128 v[58:61], v205
	s_add_u32 s70, s37, s44
	s_addc_u32 s71, s47, s45
	v_lshl_add_u64 v[222:223], s[70:71], 0, v[138:139]
	v_lshl_add_u64 v[224:225], s[70:71], 0, v[146:147]
	s_waitcnt lgkmcnt(3)
	global_store_dwordx4 v[216:217], v[50:53], off nt
	s_waitcnt lgkmcnt(2)
	global_store_dwordx4 v[218:219], v[54:57], off nt
	s_waitcnt lgkmcnt(0)
	global_store_dwordx4 v[220:221], v[58:61], off nt
	v_lshl_add_u64 v[62:63], v[222:223], 0, v[144:145]
	v_lshl_add_u64 v[64:65], v[224:225], 0, v[144:145]
	global_load_dwordx4 v[74:77], v[62:63], off
	global_load_dwordx4 v[78:81], v[64:65], off
	global_load_dwordx4 v[70:73], v201, s[42:43]
	global_load_dwordx4 v[66:69], v201, s[42:43] offset:16
	global_load_dwordx4 v[58:61], v[62:63], off offset:128
	s_nop 0
	global_load_dwordx4 v[62:65], v[64:65], off offset:128
	s_nop 0
	global_load_dwordx4 v[54:57], v201, s[42:43] offset:128
	global_load_dwordx4 v[50:53], v201, s[42:43] offset:144
	s_waitcnt vmcnt(7)
	ds_write_b128 v200, v[74:77]
	s_waitcnt vmcnt(6)
	ds_write_b128 v200, v[78:81] offset:1152
	ds_read_b128 v[74:77], v206
	ds_read_b128 v[78:81], v206 offset:16
	v_mov_b32_e32 v190, v139
	v_mov_b32_e32 v191, v139
	s_lshl_b64 s[70:71], s[48:49], 11
	s_waitcnt vmcnt(5) lgkmcnt(1)
	v_pk_fma_f32 v[72:73], v[44:45], v[72:73], v[76:77]
	v_pk_fma_f32 v[70:71], v[42:43], v[70:71], v[74:75]
	s_waitcnt vmcnt(4) lgkmcnt(0)
	v_pk_fma_f32 v[44:45], v[46:47], v[66:67], v[78:79]
	v_pk_fma_f32 v[42:43], v[48:49], v[68:69], v[80:81]
	v_cvt_pk_bf16_f32 v66, v70, v71
	v_cvt_pk_bf16_f32 v67, v72, v73
	v_cvt_pk_bf16_f32 v68, v44, v45
	v_med3_f32 v46, v70, s68, v195
	v_cvt_pk_bf16_f32 v69, v42, v43
	v_med3_f32 v47, v44, s68, v195
	v_med3_f32 v48, v71, s68, v195
	v_med3_f32 v49, v45, s68, v195
	s_waitcnt vmcnt(3)
	ds_write_b128 v200, v[58:61]
	s_waitcnt vmcnt(2)
	ds_write_b128 v200, v[62:65] offset:1152
	v_cvt_pk_fp8_f32 v190, v46, v48
	v_cvt_pk_fp8_f32 v191, v47, v49
	ds_read_b128 v[46:49], v206
	ds_read_b128 v[58:61], v206 offset:16
	s_add_u32 s37, s56, s70
	v_mov_b32_e32 v208, v139
	v_mov_b32_e32 v209, v139
	s_waitcnt vmcnt(1) lgkmcnt(1)
	v_pk_fma_f32 v[46:47], v[34:35], v[54:55], v[46:47]
	s_waitcnt vmcnt(0) lgkmcnt(0)
	v_pk_fma_f32 v[38:39], v[38:39], v[50:51], v[58:59]
	s_addc_u32 s47, s57, s71
	v_pk_fma_f32 v[34:35], v[40:41], v[52:53], v[60:61]
	v_med3_f32 v40, v46, s68, v195
	v_med3_f32 v41, v38, s68, v195
	v_med3_f32 v52, v47, s68, v195
	v_med3_f32 v53, v39, s68, v195
	s_add_u32 s70, s37, s40
	v_cvt_pk_fp8_f32 v208, v40, v52
	v_cvt_pk_fp8_f32 v209, v41, v53
	s_addc_u32 s71, s47, s41
	s_lshl_b64 s[48:49], s[48:49], 10
	s_add_u32 s37, s60, s48
	v_pk_fma_f32 v[36:37], v[36:37], v[56:57], v[48:49]
	s_addc_u32 s47, s61, s49
	v_med3_f32 v74, v72, s68, v195
	v_med3_f32 v75, v42, s68, v195
	v_med3_f32 v76, v73, s68, v195
	v_med3_f32 v62, v43, s68, v195
	v_med3_f32 v54, v36, s68, v195
	v_med3_f32 v55, v34, s68, v195
	v_med3_f32 v56, v37, s68, v195
	v_med3_f32 v40, v35, s68, v195
	v_lshl_add_u64 v[210:211], s[70:71], 0, v[114:115]
	v_lshl_add_u64 v[212:213], s[70:71], 0, v[116:117]
	s_add_u32 s70, s37, s38
	v_cvt_pk_fp8_f32 v190, v74, v76 op_sel:[0,0,1]
	v_cvt_pk_fp8_f32 v191, v75, v62 op_sel:[0,0,1]
	v_cvt_pk_fp8_f32 v208, v54, v56 op_sel:[0,0,1]
	v_cvt_pk_fp8_f32 v209, v55, v40 op_sel:[0,0,1]
	s_addc_u32 s71, s47, s39
	s_add_i32 s48, s46, 0xa0
	s_ashr_i32 s49, s48, 31
	v_cvt_pk_bf16_f32 v48, v46, v47
	v_cvt_pk_bf16_f32 v49, v36, v37
	v_cvt_pk_bf16_f32 v50, v38, v39
	v_cvt_pk_bf16_f32 v51, v34, v35
	ds_write_b128 v203, v[66:69]
	ds_write_b128 v203, v[48:51] offset:64
	v_lshl_add_u64 v[214:215], s[70:71], 0, v[120:121]
	s_lshl_b64 s[70:71], s[48:49], 12
	ds_read_b128 v[48:51], v200
	ds_read_b128 v[52:55], v200 offset:1152
	s_add_u32 s37, s10, s70
	ds_write2_b64 v204, v[190:191], v[208:209] offset1:4
	s_addc_u32 s47, s11, s71
	ds_read_b128 v[56:59], v205
	s_add_u32 s70, s37, s44
	v_lshl_add_u64 v[210:211], v[210:211], 0, v[144:145]
	s_addc_u32 s71, s47, s45
	v_lshl_add_u64 v[212:213], v[212:213], 0, v[144:145]
	v_lshl_add_u64 v[214:215], v[214:215], 0, v[118:119]
	v_lshl_add_u64 v[216:217], s[70:71], 0, v[138:139]
	s_waitcnt lgkmcnt(3)
	global_store_dwordx4 v[210:211], v[48:51], off nt
	s_waitcnt lgkmcnt(2)
	global_store_dwordx4 v[212:213], v[52:55], off nt
	s_waitcnt lgkmcnt(0)
	global_store_dwordx4 v[214:215], v[56:59], off nt
	v_lshl_add_u64 v[218:219], s[70:71], 0, v[146:147]
	v_lshl_add_u64 v[216:217], v[216:217], 0, v[144:145]
	v_lshl_add_u64 v[218:219], v[218:219], 0, v[144:145]
	global_load_dwordx4 v[48:51], v[216:217], off
	global_load_dwordx4 v[52:55], v[218:219], off
	v_mul_f32_e32 v41, v127, v127
	v_mul_f32_e32 v64, v123, v123
	v_mul_f32_e32 v65, v129, v129
	v_mul_f32_e32 v66, v125, v125
	v_fmac_f32_e32 v41, v126, v126
	v_fmac_f32_e32 v64, v122, v122
	v_fmac_f32_e32 v65, v128, v128
	v_fmac_f32_e32 v66, v124, v124
	global_load_dwordx4 v[56:59], v201, s[42:43] offset:16
	global_load_dwordx4 v[60:63], v201, s[42:43]
	v_add_f32_e32 v41, v41, v64
	v_add_f32_e32 v64, v65, v66
	v_add_f32_e32 v41, v41, v64
	global_load_dwordx4 v[64:67], v[216:217], off offset:128
	global_load_dwordx4 v[74:77], v[218:219], off offset:128
	v_mul_f32_e32 v155, v155, v155
	v_mul_f32_e32 v153, v153, v153
	v_mul_f32_e32 v151, v151, v151
	v_mul_f32_e32 v149, v149, v149
	v_fmac_f32_e32 v155, v154, v154
	v_fmac_f32_e32 v153, v152, v152
	v_fmac_f32_e32 v151, v150, v150
	v_fmac_f32_e32 v149, v148, v148
	v_add_f32_e32 v148, v155, v153
	v_add_f32_e32 v40, v151, v149
	v_add_f32_e32 v40, v148, v40
	v_add_f32_e32 v122, v40, v41
	v_mul_f32_e32 v41, v109, v109
	v_mul_f32_e32 v69, v107, v107
	v_fmac_f32_e32 v41, v108, v108
	v_fmac_f32_e32 v69, v106, v106
	global_load_dwordx4 v[78:81], v201, s[42:43] offset:144
	global_load_dwordx4 v[106:109], v201, s[42:43] offset:128
	v_mul_f32_e32 v40, v157, v157
	v_mul_f32_e32 v68, v111, v111
	v_fmac_f32_e32 v40, v156, v156
	v_fmac_f32_e32 v68, v110, v110
	v_add_f32_e32 v40, v40, v41
	v_add_f32_e32 v41, v68, v69
	v_add_f32_e32 v40, v40, v41
	v_mul_f32_e32 v41, v113, v113
	v_mul_f32_e32 v68, v101, v101
	v_mul_f32_e32 v69, v103, v103
	v_mul_f32_e32 v99, v99, v99
	v_fmac_f32_e32 v41, v112, v112
	v_fmac_f32_e32 v68, v100, v100
	v_fmac_f32_e32 v69, v102, v102
	v_fmac_f32_e32 v99, v98, v98
	v_add_f32_e32 v41, v41, v68
	v_add_f32_e32 v68, v69, v99
	v_add_f32_e32 v41, v41, v68
	v_add_f32_e32 v98, v40, v41
	v_mul_f32_e32 v40, v105, v105
	v_mul_f32_e32 v41, v93, v93
	v_mul_f32_e32 v68, v95, v95
	v_mul_f32_e32 v69, v91, v91
	v_fmac_f32_e32 v40, v104, v104
	v_fmac_f32_e32 v41, v92, v92
	v_fmac_f32_e32 v68, v94, v94
	v_fmac_f32_e32 v69, v90, v90
	v_add_f32_e32 v40, v40, v41
	v_add_f32_e32 v41, v68, v69
	v_add_f32_e32 v40, v40, v41
	v_mul_f32_e32 v41, v97, v97
	v_mul_f32_e32 v68, v85, v85
	v_mul_f32_e32 v69, v87, v87
	v_mul_f32_e32 v83, v83, v83
	v_fmac_f32_e32 v41, v96, v96
	v_fmac_f32_e32 v68, v84, v84
	v_fmac_f32_e32 v69, v86, v86
	v_fmac_f32_e32 v83, v82, v82
	v_add_f32_e32 v41, v41, v68
	v_add_f32_e32 v68, v69, v83
	s_waitcnt vmcnt(7)
	ds_write_b128 v200, v[48:51]
	s_waitcnt vmcnt(6)
	ds_write_b128 v200, v[52:55] offset:1152
	v_add_f32_e32 v41, v41, v68
	ds_read_b128 v[48:51], v206
	ds_read_b128 v[52:55], v206 offset:16
	v_add_f32_e32 v86, v40, v41
	v_mul_f32_e32 v40, v165, v165
	v_mul_f32_e32 v41, v161, v161
	v_mul_f32_e32 v68, v167, v167
	v_mul_f32_e32 v69, v163, v163
	v_fmac_f32_e32 v40, v164, v164
	v_fmac_f32_e32 v41, v160, v160
	v_fmac_f32_e32 v68, v166, v166
	v_fmac_f32_e32 v69, v162, v162
	v_add_f32_e32 v40, v40, v41
	v_add_f32_e32 v41, v68, v69
	v_add_f32_e32 v87, v40, v41
	v_mul_f32_e32 v40, v171, v171
	v_mul_f32_e32 v41, v169, v169
	v_fmac_f32_e32 v40, v170, v170
	v_fmac_f32_e32 v41, v168, v168
	s_waitcnt vmcnt(4) lgkmcnt(1)
	v_pk_fma_f32 v[68:69], v[26:27], v[60:61], v[48:49]
	s_waitcnt lgkmcnt(0)
	v_pk_fma_f32 v[84:85], v[30:31], v[56:57], v[52:53]
	v_mov_b32_e32 v188, v139
	v_mov_b32_e32 v189, v139
	v_add_f32_e32 v91, v40, v41
	v_pk_fma_f32 v[40:41], v[28:29], v[62:63], v[50:51]
	v_pk_fma_f32 v[82:83], v[32:33], v[58:59], v[54:55]
	v_cvt_pk_bf16_f32 v26, v68, v69
	v_cvt_pk_bf16_f32 v27, v40, v41
	v_cvt_pk_bf16_f32 v28, v84, v85
	v_med3_f32 v30, v68, s68, v195
	v_cvt_pk_bf16_f32 v29, v82, v83
	v_med3_f32 v31, v84, s68, v195
	v_med3_f32 v32, v69, s68, v195
	v_med3_f32 v33, v85, s68, v195
	s_waitcnt vmcnt(3)
	ds_write_b128 v200, v[64:67]
	s_waitcnt vmcnt(2)
	ds_write_b128 v200, v[74:77] offset:1152
	v_cvt_pk_fp8_f32 v188, v30, v32
	v_cvt_pk_fp8_f32 v189, v31, v33
	ds_read_b128 v[30:33], v206
	ds_read_b128 v[48:51], v206 offset:16
	s_lshl_b64 s[70:71], s[48:49], 11
	s_add_u32 s37, s56, s70
	s_addc_u32 s47, s57, s71
	s_waitcnt vmcnt(0) lgkmcnt(1)
	v_pk_fma_f32 v[66:67], v[22:23], v[106:107], v[30:31]
	s_waitcnt lgkmcnt(0)
	v_pk_fma_f32 v[76:77], v[18:19], v[78:79], v[48:49]
	v_pk_fma_f32 v[64:65], v[24:25], v[108:109], v[32:33]
	v_med3_f32 v22, v66, s68, v195
	v_med3_f32 v23, v76, s68, v195
	v_med3_f32 v24, v67, s68, v195
	v_med3_f32 v25, v77, s68, v195
	v_mov_b32_e32 v30, v139
	v_mov_b32_e32 v31, v139
	v_cvt_pk_fp8_f32 v30, v22, v24
	v_cvt_pk_fp8_f32 v31, v23, v25
	v_pk_fma_f32 v[74:75], v[20:21], v[80:81], v[50:51]
	v_cvt_pk_bf16_f32 v18, v66, v67
	v_cvt_pk_bf16_f32 v19, v64, v65
	v_cvt_pk_bf16_f32 v20, v76, v77
	s_add_u32 s70, s37, s40
	v_cvt_pk_bf16_f32 v21, v74, v75
	ds_write_b128 v203, v[26:29]
	ds_write_b128 v203, v[18:21] offset:64
	ds_read_b128 v[18:21], v200
	v_med3_f32 v52, v40, s68, v195
	v_med3_f32 v53, v82, s68, v195
	v_med3_f32 v54, v41, s68, v195
	v_med3_f32 v55, v83, s68, v195
	v_med3_f32 v32, v64, s68, v195
	v_med3_f32 v33, v74, s68, v195
	v_med3_f32 v22, v65, s68, v195
	v_med3_f32 v23, v75, s68, v195
	s_addc_u32 s71, s47, s41
	s_lshl_b64 s[48:49], s[48:49], 10
	v_cvt_pk_fp8_f32 v188, v52, v54 op_sel:[0,0,1]
	v_cvt_pk_fp8_f32 v189, v53, v55 op_sel:[0,0,1]
	v_cvt_pk_fp8_f32 v30, v32, v22 op_sel:[0,0,1]
	v_cvt_pk_fp8_f32 v31, v33, v23 op_sel:[0,0,1]
	ds_read_b128 v[22:25], v200 offset:1152
	s_add_u32 s37, s60, s48
	v_lshl_add_u64 v[26:27], s[70:71], 0, v[114:115]
	s_addc_u32 s47, s61, s49
	v_lshl_add_u64 v[26:27], v[26:27], 0, v[144:145]
	s_add_u32 s48, s37, s38
	s_waitcnt lgkmcnt(1)
	global_store_dwordx4 v[26:27], v[18:21], off nt
	s_addc_u32 s49, s47, s39
	s_addk_i32 s46, 0xb0
	v_lshl_add_u64 v[18:19], s[70:71], 0, v[116:117]
	v_lshl_add_u64 v[18:19], v[18:19], 0, v[144:145]
	ds_write2_b64 v204, v[188:189], v[30:31] offset1:4
	s_ashr_i32 s47, s46, 31
	s_waitcnt lgkmcnt(1)
	global_store_dwordx4 v[18:19], v[22:25], off nt
	ds_read_b128 v[18:21], v205
	v_mul_f32_e32 v90, v159, v159
	v_lshl_add_u64 v[22:23], s[48:49], 0, v[120:121]
	s_lshl_b64 s[48:49], s[46:47], 12
	s_add_u32 s37, s10, s48
	s_addc_u32 s48, s11, s49
	s_add_u32 s44, s37, s44
	v_lshl_add_u64 v[22:23], v[22:23], 0, v[118:119]
	s_addc_u32 s45, s48, s45
	v_mul_f32_e32 v26, v89, v89
	s_waitcnt lgkmcnt(0)
	global_store_dwordx4 v[22:23], v[18:21], off nt
	v_fmac_f32_e32 v90, v158, v158
	v_fmac_f32_e32 v26, v88, v88
	v_lshl_add_u64 v[18:19], s[44:45], 0, v[138:139]
	v_lshl_add_u64 v[48:49], v[18:19], 0, v[144:145]
	v_lshl_add_u64 v[22:23], s[44:45], 0, v[146:147]
	v_add_f32_e32 v50, v90, v26
	global_load_dwordx4 v[18:21], v[48:49], off
	v_lshl_add_u64 v[52:53], v[22:23], 0, v[144:145]
	v_add_f32_e32 v50, v91, v50
	global_load_dwordx4 v[22:25], v[52:53], off
	v_add_f32_e32 v78, v87, v50
	v_mul_f32_e32 v50, v179, v179
	v_mul_f32_e32 v51, v175, v175
	v_fmac_f32_e32 v50, v178, v178
	v_fmac_f32_e32 v51, v174, v174
	v_add_f32_e32 v50, v50, v51
	v_mul_f32_e32 v51, v177, v177
	v_mul_f32_e32 v54, v173, v173
	v_fmac_f32_e32 v51, v176, v176
	v_fmac_f32_e32 v54, v172, v172
	v_add_f32_e32 v51, v51, v54
	global_load_dwordx4 v[26:29], v201, s[42:43] offset:16
	global_load_dwordx4 v[30:33], v201, s[42:43]
	v_add_f32_e32 v50, v50, v51
	v_mul_f32_e32 v51, v187, v187
	v_mul_f32_e32 v54, v183, v183
	v_fmac_f32_e32 v51, v186, v186
	v_fmac_f32_e32 v54, v182, v182
	v_add_f32_e32 v51, v51, v54
	v_mul_f32_e32 v54, v185, v185
	v_mul_f32_e32 v55, v181, v181
	v_fmac_f32_e32 v54, v184, v184
	v_fmac_f32_e32 v55, v180, v180
	v_add_f32_e32 v54, v54, v55
	v_add_f32_e32 v51, v51, v54
	v_add_f32_e32 v79, v50, v51
	global_load_dwordx4 v[48:51], v[48:49], off offset:128
	s_nop 0
	global_load_dwordx4 v[52:55], v[52:53], off offset:128
	v_mul_f32_e32 v56, v71, v71
	v_mul_f32_e32 v57, v73, v73
	v_fmac_f32_e32 v56, v70, v70
	v_fmac_f32_e32 v57, v72, v72
	v_add_f32_e32 v70, v56, v57
	global_load_dwordx4 v[56:59], v201, s[42:43] offset:144
	global_load_dwordx4 v[60:63], v201, s[42:43] offset:128
	s_waitcnt vmcnt(7)
	ds_write_b128 v200, v[18:21]
	s_waitcnt vmcnt(6)
	ds_write_b128 v200, v[22:25] offset:1152
	ds_read_b128 v[18:21], v206
	ds_read_b128 v[22:25], v206 offset:16
	v_mul_f32_e32 v45, v45, v45
	v_mul_f32_e32 v43, v43, v43
	v_fmac_f32_e32 v45, v44, v44
	v_fmac_f32_e32 v43, v42, v42
	v_add_f32_e32 v42, v45, v43
	v_mul_f32_e32 v43, v47, v47
	v_mul_f32_e32 v37, v37, v37
	s_lshl_b64 s[42:43], s[46:47], 11
	v_fmac_f32_e32 v43, v46, v46
	v_fmac_f32_e32 v37, v36, v36
	s_waitcnt vmcnt(4) lgkmcnt(1)
	v_pk_fma_f32 v[16:17], v[16:17], v[32:33], v[20:21]
	v_pk_fma_f32 v[14:15], v[14:15], v[30:31], v[18:19]
	s_waitcnt lgkmcnt(0)
	v_pk_fma_f32 v[20:21], v[10:11], v[26:27], v[22:23]
	v_mul_f32_e32 v10, v15, v15
	v_mul_f32_e32 v11, v17, v17
	v_pk_fma_f32 v[18:19], v[12:13], v[28:29], v[24:25]
	v_fmac_f32_e32 v10, v14, v14
	v_fmac_f32_e32 v11, v16, v16
	v_add_f32_e32 v10, v10, v11
	v_mul_f32_e32 v11, v21, v21
	v_mul_f32_e32 v12, v19, v19
	v_fmac_f32_e32 v11, v20, v20
	v_fmac_f32_e32 v12, v18, v18
	v_add_f32_e32 v11, v11, v12
	v_add_f32_e32 v24, v10, v11
	v_cvt_pk_bf16_f32 v10, v14, v15
	v_cvt_pk_bf16_f32 v11, v16, v17
	v_cvt_pk_bf16_f32 v12, v20, v21
	v_cvt_pk_bf16_f32 v13, v18, v19
	v_med3_f32 v14, v14, s68, v195
	v_med3_f32 v15, v15, s68, v195
	v_mov_b32_e32 v22, v139
	s_waitcnt vmcnt(3)
	ds_write_b128 v200, v[48:51]
	s_waitcnt vmcnt(2)
	ds_write_b128 v200, v[52:55] offset:1152
	v_med3_f32 v20, v20, s68, v195
	v_med3_f32 v21, v21, s68, v195
	v_med3_f32 v25, v16, s68, v195
	v_med3_f32 v27, v17, s68, v195
	v_cvt_pk_fp8_f32 v22, v14, v15
	v_mov_b32_e32 v23, v139
	ds_read_b128 v[14:17], v206
	v_med3_f32 v26, v18, s68, v195
	v_cvt_pk_fp8_f32 v23, v20, v21
	v_med3_f32 v28, v19, s68, v195
	ds_read_b128 v[18:21], v206 offset:16
	s_waitcnt vmcnt(0) lgkmcnt(1)
	v_pk_fma_f32 v[8:9], v[8:9], v[62:63], v[16:17]
	v_pk_fma_f32 v[6:7], v[6:7], v[60:61], v[14:15]
	s_add_u32 s37, s56, s42
	v_add_f32_e32 v36, v43, v37
	s_waitcnt lgkmcnt(0)
	v_pk_fma_f32 v[16:17], v[2:3], v[56:57], v[18:19]
	v_mul_f32_e32 v2, v7, v7
	v_mul_f32_e32 v3, v9, v9
	v_pk_fma_f32 v[14:15], v[4:5], v[58:59], v[20:21]
	v_fmac_f32_e32 v2, v6, v6
	v_fmac_f32_e32 v3, v8, v8
	v_add_f32_e32 v2, v2, v3
	v_mul_f32_e32 v3, v17, v17
	v_mul_f32_e32 v4, v15, v15
	v_fmac_f32_e32 v3, v16, v16
	v_fmac_f32_e32 v4, v14, v14
	v_add_f32_e32 v3, v3, v4
	v_add_f32_e32 v2, v2, v3
	v_add_f32_e32 v18, v24, v2
	v_cvt_pk_bf16_f32 v2, v6, v7
	v_cvt_pk_bf16_f32 v3, v8, v9
	v_cvt_pk_bf16_f32 v4, v16, v17
	v_med3_f32 v6, v6, s68, v195
	v_med3_f32 v19, v16, s68, v195
	v_med3_f32 v7, v7, s68, v195
	v_med3_f32 v20, v17, s68, v195
	v_mov_b32_e32 v16, v139
	v_mov_b32_e32 v17, v139
	v_cvt_pk_fp8_f32 v16, v6, v7
	v_cvt_pk_fp8_f32 v17, v19, v20
	v_cvt_pk_bf16_f32 v5, v14, v15
	ds_write_b128 v203, v[10:13]
	ds_write_b128 v203, v[2:5] offset:64
	v_mul_f32_e32 v37, v39, v39
	v_mul_f32_e32 v35, v35, v35
	s_addc_u32 s42, s57, s43
	ds_read_b128 v[2:5], v200
	v_fmac_f32_e32 v37, v38, v38
	v_fmac_f32_e32 v35, v34, v34
	v_med3_f32 v8, v8, s68, v195
	v_med3_f32 v14, v14, s68, v195
	v_med3_f32 v6, v9, s68, v195
	v_med3_f32 v7, v15, s68, v195
	s_add_u32 s40, s37, s40
	v_add_f32_e32 v34, v37, v35
	v_cvt_pk_fp8_f32 v22, v25, v27 op_sel:[0,0,1]
	v_cvt_pk_fp8_f32 v23, v26, v28 op_sel:[0,0,1]
	v_cvt_pk_fp8_f32 v16, v8, v6 op_sel:[0,0,1]
	v_cvt_pk_fp8_f32 v17, v14, v7 op_sel:[0,0,1]
	s_addc_u32 s41, s42, s41
	ds_read_b128 v[6:9], v200 offset:1152
	v_add_f32_e32 v34, v36, v34
	v_mul_f32_e32 v35, v69, v69
	v_mul_f32_e32 v36, v41, v41
	v_lshl_add_u64 v[10:11], s[40:41], 0, v[114:115]
	v_fmac_f32_e32 v35, v68, v68
	v_fmac_f32_e32 v36, v40, v40
	v_lshl_add_u64 v[10:11], v[10:11], 0, v[144:145]
	v_add_f32_e32 v35, v35, v36
	v_mul_f32_e32 v36, v85, v85
	v_mul_f32_e32 v37, v83, v83
	s_waitcnt lgkmcnt(1)
	global_store_dwordx4 v[10:11], v[2:5], off nt
	v_fmac_f32_e32 v36, v84, v84
	v_fmac_f32_e32 v37, v82, v82
	v_lshl_add_u64 v[2:3], s[40:41], 0, v[116:117]
	s_lshl_b64 s[40:41], s[46:47], 10
	v_lshl_add_u64 v[2:3], v[2:3], 0, v[144:145]
	s_add_u32 s37, s60, s40
	ds_write2_b64 v204, v[22:23], v[16:17] offset1:4
	v_add_f32_e32 v36, v36, v37
	s_waitcnt lgkmcnt(1)
	global_store_dwordx4 v[2:3], v[6:9], off nt
	s_addc_u32 s40, s61, s41
	ds_read_b128 v[2:5], v205
	v_add_f32_e32 v35, v35, v36
	v_mul_f32_e32 v36, v67, v67
	v_mul_f32_e32 v37, v65, v65
	s_add_u32 s38, s37, s38
	v_fmac_f32_e32 v36, v66, v66
	v_fmac_f32_e32 v37, v64, v64
	s_addc_u32 s39, s40, s39
	v_add_f32_e32 v36, v36, v37
	v_mul_f32_e32 v37, v77, v77
	v_mul_f32_e32 v38, v75, v75
	v_lshl_add_u64 v[6:7], s[38:39], 0, v[120:121]
	v_fmac_f32_e32 v37, v76, v76
	v_fmac_f32_e32 v38, v74, v74
	v_lshl_add_u64 v[6:7], v[6:7], 0, v[118:119]
	v_add_f32_e32 v37, v37, v38
	s_waitcnt lgkmcnt(0)
	global_store_dwordx4 v[6:7], v[2:5], off nt
	s_lshl_b32 s35, s35, 2
	v_add_f32_e32 v42, v70, v42
	v_lshlrev_b32_e32 v2, 2, v198
	v_lshlrev_b32_e32 v3, 4, v199
	v_add_f32_e32 v36, v36, v37
	s_or_b32 s38, s29, s35
	v_add3_u32 v2, s27, v2, v3
	v_add_f32_e32 v34, v42, v34
	v_add_f32_e32 v35, v35, v36
	ds_write2st64_b32 v2, v122, v98 offset1:1
	ds_write2st64_b32 v2, v86, v78 offset0:2 offset1:3
	ds_write2st64_b32 v2, v79, v34 offset0:4 offset1:5
	ds_write2st64_b32 v2, v35, v18 offset0:6 offset1:7
	v_add_u32_e32 v6, s27, v197
	s_ashr_i32 s39, s38, 31
	s_ashr_i32 s35, s34, 31
	s_ashr_i32 s37, s36, 31
	s_lshl_b64 s[38:39], s[38:39], 18
	ds_read_b128 v[2:5], v6
	s_add_u32 s27, s58, s38
	s_addc_u32 s29, s59, s39
	s_lshl_b64 s[34:35], s[34:35], 2
	ds_read_b128 v[6:9], v6 offset:1024
	s_add_u32 s27, s27, s34
	s_addc_u32 s29, s29, s35
	s_lshl_b64 s[34:35], s[36:37], 2
	s_add_u32 s34, s27, s34
	s_waitcnt lgkmcnt(1)
	v_add_f32_e32 v2, v2, v3
	v_add_f32_e32 v3, v4, v5
	s_addc_u32 s35, s29, s35
	v_lshlrev_b32_e32 v10, 2, v196
	v_add_f32_e32 v2, v2, v3
	global_store_dword v10, v2, s[34:35]
	s_waitcnt lgkmcnt(0)
	v_add_f32_e32 v2, v6, v7
	v_add_f32_e32 v3, v8, v9
	v_add_f32_e32 v2, v2, v3
	s_andn2_b64 vcc, exec, s[6:7]
	s_mov_b64 s[6:7], -1
	global_store_dword v10, v2, s[34:35] offset:512
	s_cbranch_vccnz .LBB0_487
	v_mov_b32_e32 v2, v0
	s_andn2_b64 vcc, exec, s[14:15]
	s_cbranch_vccnz .LBB0_486
	s_barrier
	s_branch .LBB0_486

.LBB0_1756:
	v_pk_mul_f32 v[126:127], v[126:127], s[22:23] op_sel_hi:[1,0]
	v_pk_mul_f32 v[128:129], v[128:129], s[22:23] op_sel_hi:[1,0]
	v_med3_f32 v150, v126, s50, v149
	v_med3_f32 v127, v127, s50, v149
	v_mov_b32_e32 v126, v139
	v_pk_mul_f32 v[114:115], v[114:115], s[22:23] op_sel_hi:[1,0]
	v_cvt_pk_fp8_f32 v126, v150, v127
	v_med3_f32 v127, v128, s50, v149
	v_med3_f32 v128, v129, s50, v149
	v_med3_f32 v114, v114, s50, v149
	v_med3_f32 v115, v115, s50, v149
	v_mov_b32_e32 v129, v139
	v_cvt_pk_fp8_f32 v129, v114, v115
	v_pk_mul_f32 v[114:115], v[116:117], s[22:23] op_sel_hi:[1,0]
	v_pk_mul_f32 v[110:111], v[110:111], s[22:23] op_sel_hi:[1,0]
	v_med3_f32 v114, v114, s50, v149
	v_med3_f32 v115, v115, s50, v149
	v_cvt_pk_fp8_f32 v129, v114, v115 op_sel:[0,0,1]
	v_med3_f32 v114, v110, s50, v149
	v_med3_f32 v111, v111, s50, v149
	v_mov_b32_e32 v110, v139
	v_pk_mul_f32 v[112:113], v[112:113], s[22:23] op_sel_hi:[1,0]
	v_pk_mul_f32 v[98:99], v[98:99], s[22:23] op_sel_hi:[1,0]
	v_cvt_pk_fp8_f32 v110, v114, v111
	v_med3_f32 v111, v112, s50, v149
	v_med3_f32 v112, v113, s50, v149
	v_med3_f32 v98, v98, s50, v149
	v_med3_f32 v99, v99, s50, v149
	v_mov_b32_e32 v113, v139
	v_cvt_pk_fp8_f32 v113, v98, v99
	v_pk_mul_f32 v[98:99], v[100:101], s[22:23] op_sel_hi:[1,0]
	v_pk_mul_f32 v[94:95], v[94:95], s[22:23] op_sel_hi:[1,0]
	v_med3_f32 v98, v98, s50, v149
	v_med3_f32 v99, v99, s50, v149
	v_cvt_pk_fp8_f32 v113, v98, v99 op_sel:[0,0,1]
	v_med3_f32 v98, v94, s50, v149
	v_med3_f32 v95, v95, s50, v149
	v_mov_b32_e32 v94, v139
	v_pk_mul_f32 v[96:97], v[96:97], s[22:23] op_sel_hi:[1,0]
	v_pk_mul_f32 v[82:83], v[82:83], s[22:23] op_sel_hi:[1,0]
	v_cvt_pk_fp8_f32 v94, v98, v95
	v_med3_f32 v95, v96, s50, v149
	v_med3_f32 v96, v97, s50, v149
	v_med3_f32 v82, v82, s50, v149
	v_med3_f32 v83, v83, s50, v149
	v_mov_b32_e32 v97, v139
	v_cvt_pk_fp8_f32 v97, v82, v83
	v_pk_mul_f32 v[82:83], v[84:85], s[22:23] op_sel_hi:[1,0]
	v_pk_mul_f32 v[78:79], v[78:79], s[22:23] op_sel_hi:[1,0]
	v_med3_f32 v82, v82, s50, v149
	v_med3_f32 v83, v83, s50, v149
	v_cvt_pk_fp8_f32 v97, v82, v83 op_sel:[0,0,1]
	v_med3_f32 v82, v78, s50, v149
	v_med3_f32 v79, v79, s50, v149
	v_mov_b32_e32 v78, v139
	v_pk_mul_f32 v[80:81], v[80:81], s[22:23] op_sel_hi:[1,0]
	v_pk_mul_f32 v[54:55], v[54:55], s[22:23] op_sel_hi:[1,0]
	v_cvt_pk_fp8_f32 v78, v82, v79
	v_med3_f32 v79, v80, s50, v149
	v_med3_f32 v80, v81, s50, v149
	v_med3_f32 v54, v54, s50, v149
	v_med3_f32 v55, v55, s50, v149
	v_mov_b32_e32 v81, v139
	v_cvt_pk_fp8_f32 v81, v54, v55
	v_pk_mul_f32 v[54:55], v[56:57], s[22:23] op_sel_hi:[1,0]
	v_pk_mul_f32 v[50:51], v[50:51], s[22:23] op_sel_hi:[1,0]
	v_med3_f32 v54, v54, s50, v149
	v_med3_f32 v55, v55, s50, v149
	v_cvt_pk_fp8_f32 v81, v54, v55 op_sel:[0,0,1]
	v_pk_mul_f32 v[54:55], v[74:75], s[22:23] op_sel_hi:[1,0]
	v_med3_f32 v50, v50, s50, v149
	v_med3_f32 v56, v54, s50, v149
	v_med3_f32 v55, v55, s50, v149
	v_mov_b32_e32 v54, v139
	v_cvt_pk_fp8_f32 v54, v56, v55
	v_pk_mul_f32 v[56:57], v[76:77], s[22:23] op_sel_hi:[1,0]
	v_med3_f32 v51, v51, s50, v149
	v_med3_f32 v55, v56, s50, v149
	v_med3_f32 v56, v57, s50, v149
	v_cvt_pk_fp8_f32 v54, v55, v56 op_sel:[0,0,1]
	v_pk_mul_f32 v[56:57], v[58:59], s[22:23] op_sel_hi:[1,0]
	v_mov_b32_e32 v55, v139
	v_med3_f32 v56, v56, s50, v149
	v_med3_f32 v57, v57, s50, v149
	v_cvt_pk_fp8_f32 v55, v56, v57
	v_pk_mul_f32 v[56:57], v[60:61], s[22:23] op_sel_hi:[1,0]
	v_pk_mul_f32 v[46:47], v[46:47], s[22:23] op_sel_hi:[1,0]
	v_med3_f32 v56, v56, s50, v149
	v_med3_f32 v57, v57, s50, v149
	v_cvt_pk_fp8_f32 v55, v56, v57 op_sel:[0,0,1]
	v_pk_mul_f32 v[56:57], v[62:63], s[22:23] op_sel_hi:[1,0]
	v_med3_f32 v47, v47, s50, v149
	v_med3_f32 v58, v56, s50, v149
	v_med3_f32 v57, v57, s50, v149
	v_mov_b32_e32 v56, v139
	v_cvt_pk_fp8_f32 v56, v58, v57
	v_pk_mul_f32 v[58:59], v[64:65], s[22:23] op_sel_hi:[1,0]
	v_pk_mul_f32 v[48:49], v[48:49], s[22:23] op_sel_hi:[1,0]
	v_med3_f32 v57, v58, s50, v149
	v_med3_f32 v58, v59, s50, v149
	v_cvt_pk_fp8_f32 v56, v57, v58 op_sel:[0,0,1]
	v_mov_b32_e32 v57, v139
	v_cvt_pk_fp8_f32 v57, v50, v51
	v_pk_mul_f32 v[50:51], v[52:53], s[22:23] op_sel_hi:[1,0]
	v_med3_f32 v52, v46, s50, v149
	v_mov_b32_e32 v46, v139
	v_pk_mul_f32 v[34:35], v[34:35], s[22:23] op_sel_hi:[1,0]
	v_cvt_pk_fp8_f32 v46, v52, v47
	v_med3_f32 v47, v48, s50, v149
	v_med3_f32 v48, v49, s50, v149
	v_med3_f32 v34, v34, s50, v149
	v_med3_f32 v35, v35, s50, v149
	v_mov_b32_e32 v49, v139
	v_cvt_pk_fp8_f32 v49, v34, v35
	v_pk_mul_f32 v[34:35], v[36:37], s[22:23] op_sel_hi:[1,0]
	v_pk_mul_f32 v[30:31], v[30:31], s[22:23] op_sel_hi:[1,0]
	v_med3_f32 v34, v34, s50, v149
	v_med3_f32 v35, v35, s50, v149
	v_cvt_pk_fp8_f32 v49, v34, v35 op_sel:[0,0,1]
	v_med3_f32 v34, v30, s50, v149
	v_med3_f32 v31, v31, s50, v149
	v_mov_b32_e32 v30, v139
	v_pk_mul_f32 v[32:33], v[32:33], s[22:23] op_sel_hi:[1,0]
	v_pk_mul_f32 v[18:19], v[18:19], s[22:23] op_sel_hi:[1,0]
	v_cvt_pk_fp8_f32 v30, v34, v31
	v_med3_f32 v31, v32, s50, v149
	v_med3_f32 v32, v33, s50, v149
	v_med3_f32 v18, v18, s50, v149
	v_med3_f32 v19, v19, s50, v149
	v_mov_b32_e32 v33, v139
	v_cvt_pk_fp8_f32 v33, v18, v19
	v_pk_mul_f32 v[18:19], v[20:21], s[22:23] op_sel_hi:[1,0]
	v_pk_mul_f32 v[14:15], v[14:15], s[22:23] op_sel_hi:[1,0]
	v_med3_f32 v18, v18, s50, v149
	v_med3_f32 v19, v19, s50, v149
	v_cvt_pk_fp8_f32 v33, v18, v19 op_sel:[0,0,1]
	v_med3_f32 v18, v14, s50, v149
	v_med3_f32 v15, v15, s50, v149
	v_mov_b32_e32 v14, v139
	v_pk_mul_f32 v[118:119], v[118:119], s[22:23] op_sel_hi:[1,0]
	v_cvt_pk_fp8_f32 v14, v18, v15
	v_mov_b32_e32 v138, v0
	v_cvt_pk_fp8_f32 v126, v127, v128 op_sel:[0,0,1]
	v_med3_f32 v118, v118, s50, v149
	v_med3_f32 v119, v119, s50, v149
	v_mov_b32_e32 v127, v139
	v_pk_mul_f32 v[102:103], v[102:103], s[22:23] op_sel_hi:[1,0]
	v_pk_mul_f32 v[38:39], v[38:39], s[22:23] op_sel_hi:[1,0]
	v_cvt_pk_fp8_f32 v127, v118, v119
	v_readfirstlane_b32 s25, v138
	v_cvt_pk_fp8_f32 v110, v111, v112 op_sel:[0,0,1]
	v_med3_f32 v102, v102, s50, v149
	v_med3_f32 v103, v103, s50, v149
	v_mov_b32_e32 v111, v139
	v_pk_mul_f32 v[86:87], v[86:87], s[22:23] op_sel_hi:[1,0]
	v_cvt_pk_fp8_f32 v46, v47, v48 op_sel:[0,0,1]
	v_med3_f32 v38, v38, s50, v149
	v_med3_f32 v39, v39, s50, v149
	v_mov_b32_e32 v47, v139
	v_pk_mul_f32 v[22:23], v[22:23], s[22:23] op_sel_hi:[1,0]
	v_pk_mul_f32 v[16:17], v[16:17], s[22:23] op_sel_hi:[1,0]
	s_bfe_u32 s27, s25, 0x20006
	s_ashr_i32 s25, s25, 6
	v_cvt_pk_fp8_f32 v111, v102, v103
	v_cvt_pk_fp8_f32 v94, v95, v96 op_sel:[0,0,1]
	v_med3_f32 v86, v86, s50, v149
	v_med3_f32 v87, v87, s50, v149
	v_mov_b32_e32 v95, v139
	v_pk_mul_f32 v[66:67], v[66:67], s[22:23] op_sel_hi:[1,0]
	v_cvt_pk_fp8_f32 v47, v38, v39
	v_cvt_pk_fp8_f32 v30, v31, v32 op_sel:[0,0,1]
	v_med3_f32 v22, v22, s50, v149
	v_med3_f32 v23, v23, s50, v149
	v_mov_b32_e32 v31, v139
	v_med3_f32 v15, v16, s50, v149
	v_med3_f32 v16, v17, s50, v149
	v_pk_mul_f32 v[6:7], v[6:7], s[22:23] op_sel_hi:[1,0]
	s_lshl_b32 s34, s34, 2
	s_and_b32 s25, s25, -4
	v_pk_mul_f32 v[118:119], v[120:121], s[22:23] op_sel_hi:[1,0]
	v_cvt_pk_fp8_f32 v95, v86, v87
	v_cvt_pk_fp8_f32 v78, v79, v80 op_sel:[0,0,1]
	v_med3_f32 v66, v66, s50, v149
	v_med3_f32 v67, v67, s50, v149
	v_mov_b32_e32 v79, v139
	v_cvt_pk_fp8_f32 v31, v22, v23
	v_cvt_pk_fp8_f32 v14, v15, v16 op_sel:[0,0,1]
	v_med3_f32 v6, v6, s50, v149
	v_med3_f32 v7, v7, s50, v149
	v_mov_b32_e32 v15, v139
	s_add_i32 s34, s34, s35
	s_or_b32 s36, s25, s27
	v_med3_f32 v118, v118, s50, v149
	v_med3_f32 v119, v119, s50, v149
	v_pk_mul_f32 v[102:103], v[104:105], s[22:23] op_sel_hi:[1,0]
	v_cvt_pk_fp8_f32 v79, v66, v67
	v_pk_mul_f32 v[38:39], v[40:41], s[22:23] op_sel_hi:[1,0]
	v_cvt_pk_fp8_f32 v15, v6, v7
	s_ashr_i32 s35, s34, 31
	s_ashr_i32 s37, s36, 31
	v_cvt_pk_fp8_f32 v127, v118, v119 op_sel:[0,0,1]
	v_pk_mul_f32 v[118:119], v[122:123], s[22:23] op_sel_hi:[1,0]
	v_med3_f32 v102, v102, s50, v149
	v_med3_f32 v103, v103, s50, v149
	v_pk_mul_f32 v[86:87], v[88:89], s[22:23] op_sel_hi:[1,0]
	v_med3_f32 v38, v38, s50, v149
	v_med3_f32 v39, v39, s50, v149
	v_pk_mul_f32 v[22:23], v[24:25], s[22:23] op_sel_hi:[1,0]
	s_lshl_b64 s[34:35], s[34:35], 16
	s_lshl_b64 s[36:37], s[36:37], 13
	v_med3_f32 v118, v118, s50, v149
	v_med3_f32 v119, v119, s50, v149
	v_mov_b32_e32 v128, v139
	v_cvt_pk_fp8_f32 v111, v102, v103 op_sel:[0,0,1]
	v_pk_mul_f32 v[102:103], v[106:107], s[22:23] op_sel_hi:[1,0]
	v_med3_f32 v86, v86, s50, v149
	v_med3_f32 v87, v87, s50, v149
	v_pk_mul_f32 v[66:67], v[68:69], s[22:23] op_sel_hi:[1,0]
	v_cvt_pk_fp8_f32 v47, v38, v39 op_sel:[0,0,1]
	v_pk_mul_f32 v[38:39], v[42:43], s[22:23] op_sel_hi:[1,0]
	v_med3_f32 v22, v22, s50, v149
	v_med3_f32 v23, v23, s50, v149
	v_pk_mul_f32 v[6:7], v[8:9], s[22:23] op_sel_hi:[1,0]
	s_add_u32 s25, s44, s34
	v_cvt_pk_fp8_f32 v128, v118, v119
	v_med3_f32 v102, v102, s50, v149
	v_med3_f32 v103, v103, s50, v149
	v_mov_b32_e32 v112, v139
	v_cvt_pk_fp8_f32 v95, v86, v87 op_sel:[0,0,1]
	v_pk_mul_f32 v[86:87], v[90:91], s[22:23] op_sel_hi:[1,0]
	v_med3_f32 v66, v66, s50, v149
	v_med3_f32 v67, v67, s50, v149
	v_med3_f32 v38, v38, s50, v149
	v_med3_f32 v39, v39, s50, v149
	v_mov_b32_e32 v48, v139
	v_cvt_pk_fp8_f32 v31, v22, v23 op_sel:[0,0,1]
	v_pk_mul_f32 v[22:23], v[26:27], s[22:23] op_sel_hi:[1,0]
	v_med3_f32 v6, v6, s50, v149
	v_med3_f32 v7, v7, s50, v149
	s_addc_u32 s27, s45, s35
	v_cvt_pk_fp8_f32 v112, v102, v103
	v_med3_f32 v86, v86, s50, v149
	v_med3_f32 v87, v87, s50, v149
	v_mov_b32_e32 v96, v139
	v_cvt_pk_fp8_f32 v79, v66, v67 op_sel:[0,0,1]
	v_pk_mul_f32 v[66:67], v[70:71], s[22:23] op_sel_hi:[1,0]
	v_cvt_pk_fp8_f32 v48, v38, v39
	v_med3_f32 v22, v22, s50, v149
	v_med3_f32 v23, v23, s50, v149
	v_mov_b32_e32 v32, v139
	v_cvt_pk_fp8_f32 v15, v6, v7 op_sel:[0,0,1]
	v_pk_mul_f32 v[6:7], v[10:11], s[22:23] op_sel_hi:[1,0]
	v_pk_mul_f32 v[2:3], v[2:3], s[22:23] op_sel_hi:[1,0]
	s_add_u32 s34, s25, s36
	v_lshlrev_b32_e32 v138, 4, v138
	v_pk_mul_f32 v[118:119], v[124:125], s[22:23] op_sel_hi:[1,0]
	v_cvt_pk_fp8_f32 v96, v86, v87
	v_med3_f32 v66, v66, s50, v149
	v_med3_f32 v67, v67, s50, v149
	v_mov_b32_e32 v80, v139
	v_cvt_pk_fp8_f32 v32, v22, v23
	v_med3_f32 v6, v6, s50, v149
	v_med3_f32 v7, v7, s50, v149
	v_mov_b32_e32 v16, v139
	v_med3_f32 v2, v2, s50, v149
	v_med3_f32 v3, v3, s50, v149
	v_mov_b32_e32 v17, v139
	s_addc_u32 s35, s27, s37
	v_and_b32_e32 v138, 0x3f0, v138
	v_med3_f32 v118, v118, s50, v149
	v_med3_f32 v119, v119, s50, v149
	v_pk_mul_f32 v[102:103], v[108:109], s[22:23] op_sel_hi:[1,0]
	v_cvt_pk_fp8_f32 v80, v66, v67
	v_med3_f32 v50, v50, s50, v149
	v_med3_f32 v51, v51, s50, v149
	v_pk_mul_f32 v[38:39], v[44:45], s[22:23] op_sel_hi:[1,0]
	v_cvt_pk_fp8_f32 v16, v6, v7
	v_cvt_pk_fp8_f32 v17, v2, v3
	v_lshl_add_u64 v[144:145], s[34:35], 0, v[138:139]
	v_cvt_pk_fp8_f32 v128, v118, v119 op_sel:[0,0,1]
	v_med3_f32 v102, v102, s50, v149
	v_med3_f32 v103, v103, s50, v149
	v_pk_mul_f32 v[86:87], v[92:93], s[22:23] op_sel_hi:[1,0]
	v_cvt_pk_fp8_f32 v57, v50, v51 op_sel:[0,0,1]
	v_med3_f32 v38, v38, s50, v149
	v_med3_f32 v39, v39, s50, v149
	v_pk_mul_f32 v[22:23], v[28:29], s[22:23] op_sel_hi:[1,0]
	v_cvt_pk_fp8_f32 v112, v102, v103 op_sel:[0,0,1]
	v_med3_f32 v86, v86, s50, v149
	v_med3_f32 v87, v87, s50, v149
	v_pk_mul_f32 v[66:67], v[72:73], s[22:23] op_sel_hi:[1,0]
	v_add_co_u32_e32 v50, vcc, s51, v144
	v_cvt_pk_fp8_f32 v48, v38, v39 op_sel:[0,0,1]
	v_med3_f32 v22, v22, s50, v149
	v_med3_f32 v23, v23, s50, v149
	v_pk_mul_f32 v[6:7], v[12:13], s[22:23] op_sel_hi:[1,0]
	v_pk_mul_f32 v[2:3], v[4:5], s[22:23] op_sel_hi:[1,0]
	v_cvt_pk_fp8_f32 v96, v86, v87 op_sel:[0,0,1]
	v_med3_f32 v66, v66, s50, v149
	v_med3_f32 v67, v67, s50, v149
	v_addc_co_u32_e32 v51, vcc, 0, v145, vcc
	v_cvt_pk_fp8_f32 v32, v22, v23 op_sel:[0,0,1]
	v_med3_f32 v6, v6, s50, v149
	v_med3_f32 v7, v7, s50, v149
	v_med3_f32 v2, v2, s50, v149
	v_med3_f32 v3, v3, s50, v149
	v_cvt_pk_fp8_f32 v80, v66, v67 op_sel:[0,0,1]
	v_cvt_pk_fp8_f32 v16, v6, v7 op_sel:[0,0,1]
	v_cvt_pk_fp8_f32 v17, v2, v3 op_sel:[0,0,1]
	s_andn2_b64 vcc, exec, s[8:9]
	s_mov_b64 s[8:9], -1
	global_store_dwordx4 v138, v[126:129], s[34:35] nt
	global_store_dwordx4 v138, v[110:113], s[34:35] offset:1024 nt
	global_store_dwordx4 v138, v[94:97], s[34:35] offset:2048 nt
	global_store_dwordx4 v138, v[78:81], s[34:35] offset:3072 nt
	global_store_dwordx4 v[50:51], v[54:57], off nt
	global_store_dwordx4 v[50:51], v[46:49], off offset:1024 nt
	global_store_dwordx4 v[50:51], v[30:33], off offset:2048 nt
	global_store_dwordx4 v[50:51], v[14:17], off offset:3072 nt
	s_cbranch_vccnz .LBB0_1747
	v_mov_b32_e32 v2, v0
	s_andn2_b64 vcc, exec, s[10:11]
	s_cbranch_vccnz .LBB0_1746
	s_barrier
	s_branch .LBB0_1746

.LBB0_1780:
	v_mov_b32_e32 v209, v0
	s_lshl_b32 s47, s64, 8
	v_readfirstlane_b32 s10, v209
	s_ashr_i32 s45, s10, 6
	s_mul_i32 s11, s45, 0xb00
	s_and_b32 s45, s45, 3
	s_lshl_b32 s68, s45, 6
	s_ashr_i32 s10, s10, 8
	s_or_b32 s74, s68, s47
	s_lshl_b32 s47, s72, 2
	s_add_i32 s68, s47, s64
	s_lshl_b32 s47, s10, 2
	s_or_b32 s70, s47, s45
	s_add_i32 s11, s11, 0
	s_ashr_i32 s69, s68, 31
	s_ashr_i32 s71, s70, 31
	s_add_i32 s11, s11, 0x20000
	s_lshl_b64 s[68:69], s[68:69], 16
	s_lshl_b64 s[70:71], s[70:71], 13
	s_add_u32 s47, s41, s68
	s_addc_u32 s68, s43, s69
	s_add_u32 s78, s47, s70
	s_addc_u32 s79, s68, s71
	s_lshl_b32 s72, s72, 8
	s_lshl_b32 s10, s10, 6
	s_add_i32 s80, s10, s72
	s_ashr_i32 s81, s80, 31
	s_ashr_i32 s75, s74, 31
	s_lshl_b64 s[82:83], s[80:81], 11
	s_add_u32 s47, s54, s82
	s_addc_u32 s69, s55, s83
	s_lshl_b64 s[76:77], s[74:75], 1
	v_and_b32_e32 v204, 63, v209
	s_add_u32 s68, s47, s76
	v_bfe_u32 v190, v209, 3, 3
	v_lshlrev_b32_e32 v174, 4, v204
	s_addc_u32 s69, s69, s77
	v_lshlrev_b32_e32 v182, 11, v190
	v_mov_b32_e32 v183, v175
	v_lshl_add_u64 v[146:147], s[68:69], 0, v[182:183]
	v_and_b32_e32 v180, 0x70, v174
	v_mov_b32_e32 v181, v175
	v_lshl_add_u64 v[146:147], v[146:147], 0, v[180:181]
	v_or_b32_e32 v184, 0x4000, v182
	v_mov_b32_e32 v185, v175
	global_load_dwordx4 v[162:165], v[146:147], off
	v_lshl_add_u64 v[146:147], s[68:69], 0, v[184:185]
	v_lshl_add_u64 v[146:147], v[146:147], 0, v[180:181]
	global_load_dwordx4 v[186:189], v[146:147], off
	global_load_dwordx4 v[158:161], v174, s[78:79]
	s_or_b32 s47, s72, 16
	s_add_i32 s68, s10, s47
	s_ashr_i32 s69, s68, 31
	s_lshl_b64 s[68:69], s[68:69], 11
	s_add_u32 s68, s54, s68
	s_addc_u32 s69, s55, s69
	s_add_u32 s68, s68, s76
	s_addc_u32 s69, s69, s77
	v_lshl_add_u64 v[150:151], s[68:69], 0, v[182:183]
	v_lshl_add_u64 v[150:151], v[150:151], 0, v[180:181]
	v_lshl_add_u64 v[154:155], s[68:69], 0, v[184:185]
	global_load_dwordx4 v[150:153], v[150:151], off
	v_lshl_add_u64 v[154:155], v[154:155], 0, v[180:181]
	global_load_dwordx4 v[146:149], v174, s[78:79] offset:1024
	v_mul_u32_u24_e32 v190, 0x90, v190
	global_load_dwordx4 v[154:157], v[154:155], off
	v_and_b32_e32 v205, 15, v209
	v_add3_u32 v207, s11, v190, v180
	v_pk_fma_f32 v[144:145], v[144:145], s[38:39], v[16:17] op_sel_hi:[1,0,1]
	v_pk_fma_f32 v[142:143], v[142:143], s[38:39], v[14:15] op_sel_hi:[1,0,1]
	v_pk_fma_f32 v[138:139], v[138:139], s[38:39], v[10:11] op_sel_hi:[1,0,1]
	v_pk_fma_f32 v[210:211], v[140:141], s[38:39], v[12:13] op_sel_hi:[1,0,1]
	v_pk_mul_f32 v[140:141], v[142:143], s[40:41] op_sel_hi:[1,0]
	v_pk_mul_f32 v[138:139], v[138:139], s[40:41] op_sel_hi:[1,0]
	v_pk_mul_f32 v[142:143], v[144:145], s[40:41] op_sel_hi:[1,0]
	v_exp_f32_e32 v138, v138
	v_exp_f32_e32 v139, v139
	v_exp_f32_e32 v142, v142
	v_exp_f32_e32 v143, v143
	v_pk_mul_f32 v[144:145], v[210:211], s[40:41] op_sel_hi:[1,0]
	s_waitcnt vmcnt(0)
	v_pk_fma_f32 v[136:137], v[136:137], s[38:39], v[8:9] op_sel_hi:[1,0,1]
	v_exp_f32_e32 v144, v144
	v_exp_f32_e32 v145, v145
	v_pk_fma_f32 v[134:135], v[134:135], s[38:39], v[6:7] op_sel_hi:[1,0,1]
	v_pk_fma_f32 v[132:133], v[132:133], s[38:39], v[4:5] op_sel_hi:[1,0,1]
	v_pk_fma_f32 v[130:131], v[130:131], s[38:39], v[2:3] op_sel_hi:[1,0,1]
	v_exp_f32_e32 v140, v140
	v_exp_f32_e32 v141, v141
	v_pk_add_f32 v[138:139], v[138:139], 1.0 op_sel_hi:[1,0]
	v_pk_add_f32 v[142:143], v[142:143], 1.0 op_sel_hi:[1,0]
	v_pk_mul_f32 v[134:135], v[134:135], s[40:41] op_sel_hi:[1,0]
	v_pk_mul_f32 v[130:131], v[130:131], s[40:41] op_sel_hi:[1,0]
	v_pk_mul_f32 v[136:137], v[136:137], s[40:41] op_sel_hi:[1,0]
	v_pk_mul_f32 v[132:133], v[132:133], s[40:41] op_sel_hi:[1,0]
	v_rcp_f32_e32 v138, v138
	v_rcp_f32_e32 v139, v139
	v_rcp_f32_e32 v142, v142
	v_rcp_f32_e32 v143, v143
	v_exp_f32_e32 v134, v134
	v_exp_f32_e32 v135, v135
	v_exp_f32_e32 v130, v130
	v_exp_f32_e32 v131, v131
	v_exp_f32_e32 v136, v136
	s_waitcnt vmcnt(0)
	ds_write_b128 v207, v[162:165]
	ds_write_b128 v207, v[186:189] offset:1152
	v_mul_u32_u24_e32 v162, 0x90, v205
	v_and_b32_e32 v163, 48, v209
	v_add3_u32 v208, s11, v162, v163
	ds_read_b128 v[194:197], v208
	ds_read_b128 v[162:165], v208 offset:64
	v_cvt_pk_f32_fp8_sdwa v[198:199], v158 src0_sel:WORD_1
	v_cvt_pk_f32_fp8_e32 v[200:201], v159
	v_exp_f32_e32 v137, v137
	s_waitcnt lgkmcnt(0)
	v_lshlrev_b32_e32 v186, 16, v196
	v_and_b32_e32 v187, 0xffff0000, v196
	v_lshlrev_b32_e32 v190, 16, v197
	v_and_b32_e32 v191, 0xffff0000, v197
	v_cvt_pk_f32_fp8_e32 v[196:197], v158
	v_exp_f32_e32 v132, v132
	v_exp_f32_e32 v133, v133
	v_pk_add_f32 v[144:145], v[144:145], 1.0 op_sel_hi:[1,0]
	v_lshlrev_b32_e32 v188, 16, v194
	v_and_b32_e32 v189, 0xffff0000, v194
	v_lshlrev_b32_e32 v194, 16, v195
	v_and_b32_e32 v195, 0xffff0000, v195
	v_cvt_pk_f32_fp8_sdwa v[158:159], v159 src0_sel:WORD_1
	v_pk_add_f32 v[140:141], v[140:141], 1.0 op_sel_hi:[1,0]
	v_rcp_f32_e32 v210, v144
	v_rcp_f32_e32 v211, v145
	v_pk_mul_f32 v[144:145], v[196:197], s[42:43] op_sel_hi:[1,0]
	v_pk_mul_f32 v[196:197], v[198:199], s[42:43] op_sel_hi:[1,0]
	v_pk_mul_f32 v[198:199], v[200:201], s[42:43] op_sel_hi:[1,0]
	v_rcp_f32_e32 v140, v140
	v_rcp_f32_e32 v141, v141
	v_pk_fma_f32 v[142:143], v[142:143], v[196:197], v[194:195]
	v_pk_fma_f32 v[186:187], v[138:139], v[198:199], v[186:187]
	v_cvt_pk_f32_fp8_e32 v[194:195], v160
	v_cvt_pk_f32_fp8_sdwa v[196:197], v160 src0_sel:WORD_1
	v_cvt_pk_f32_fp8_e32 v[198:199], v161
	v_cvt_pk_f32_fp8_sdwa v[160:161], v161 src0_sel:WORD_1
	v_pk_add_f32 v[134:135], v[134:135], 1.0 op_sel_hi:[1,0]
	v_pk_add_f32 v[130:131], v[130:131], 1.0 op_sel_hi:[1,0]
	v_pk_add_f32 v[136:137], v[136:137], 1.0 op_sel_hi:[1,0]
	v_pk_add_f32 v[132:133], v[132:133], 1.0 op_sel_hi:[1,0]
	v_rcp_f32_e32 v134, v134
	v_rcp_f32_e32 v135, v135
	v_rcp_f32_e32 v130, v130
	v_rcp_f32_e32 v131, v131
	v_rcp_f32_e32 v136, v136
	v_rcp_f32_e32 v137, v137
	v_rcp_f32_e32 v132, v132
	v_rcp_f32_e32 v133, v133
	v_pk_mul_f32 v[158:159], v[158:159], s[42:43] op_sel_hi:[1,0]
	v_pk_fma_f32 v[144:145], v[140:141], v[144:145], v[188:189]
	v_pk_fma_f32 v[158:159], v[210:211], v[158:159], v[190:191]
	v_cvt_pk_bf16_f32 v138, v144, v145
	v_cvt_pk_bf16_f32 v139, v142, v143
	v_cvt_pk_bf16_f32 v140, v186, v187
	v_lshlrev_b32_e32 v188, 16, v162
	v_cvt_pk_bf16_f32 v141, v158, v159
	v_and_b32_e32 v189, 0xffff0000, v162
	v_lshlrev_b32_e32 v162, 16, v163
	v_and_b32_e32 v163, 0xffff0000, v163
	v_lshlrev_b32_e32 v190, 16, v164
	v_and_b32_e32 v191, 0xffff0000, v164
	v_lshlrev_b32_e32 v164, 16, v165
	v_and_b32_e32 v165, 0xffff0000, v165
	v_pk_mul_f32 v[194:195], v[194:195], s[42:43] op_sel_hi:[1,0]
	v_pk_mul_f32 v[196:197], v[196:197], s[42:43] op_sel_hi:[1,0]
	v_pk_mul_f32 v[198:199], v[198:199], s[42:43] op_sel_hi:[1,0]
	v_pk_mul_f32 v[200:201], v[160:161], s[42:43] op_sel_hi:[1,0]
	s_add_u32 s68, s56, s82
	v_pk_fma_f32 v[160:161], v[136:137], v[196:197], v[162:163]
	v_pk_fma_f32 v[162:163], v[134:135], v[194:195], v[188:189]
	v_pk_fma_f32 v[164:165], v[132:133], v[200:201], v[164:165]
	v_pk_fma_f32 v[188:189], v[130:131], v[198:199], v[190:191]
	v_cvt_pk_bf16_f32 v130, v162, v163
	v_cvt_pk_bf16_f32 v131, v160, v161
	s_addc_u32 s69, s57, s83
	v_cvt_pk_bf16_f32 v132, v188, v189
	v_cvt_pk_bf16_f32 v133, v164, v165
	ds_write_b128 v208, v[138:141]
	ds_write_b128 v208, v[130:133] offset:64
	s_add_u32 s68, s68, s76
	ds_read_b128 v[130:133], v207
	ds_read_b128 v[134:137], v207 offset:1152
	s_addc_u32 s69, s69, s77
	v_lshl_add_u64 v[138:139], s[68:69], 0, v[182:183]
	v_lshl_add_u64 v[138:139], v[138:139], 0, v[180:181]
	s_waitcnt lgkmcnt(1)
	global_store_dwordx4 v[138:139], v[130:133], off nt
	v_bfe_u32 v206, v209, 4, 2
	v_bfe_u32 v195, v209, 2, 4
	v_lshl_add_u64 v[130:131], s[68:69], 0, v[184:185]
	v_lshl_add_u64 v[130:131], v[130:131], 0, v[180:181]
	s_waitcnt lgkmcnt(0)
	global_store_dwordx4 v[130:131], v[134:137], off nt
	v_mov_b32_e32 v131, v175
	v_mov_b32_e32 v130, v175
	v_mov_b32_e32 v133, v175
	v_mov_b32_e32 v132, v175
	v_cvt_pk_fp8_f32 v131, v188, v189
	v_cvt_pk_fp8_f32 v130, v162, v163
	v_cvt_pk_fp8_f32 v133, v186, v187
	v_cvt_pk_fp8_f32 v132, v144, v145
	v_cvt_pk_fp8_f32 v131, v164, v165 op_sel:[0,0,1]
	v_cvt_pk_fp8_f32 v130, v160, v161 op_sel:[0,0,1]
	v_cvt_pk_fp8_f32 v133, v158, v159 op_sel:[0,0,1]
	v_cvt_pk_fp8_f32 v132, v142, v143 op_sel:[0,0,1]
	v_mul_u32_u24_e32 v134, 0x50, v205
	v_lshlrev_b32_e32 v135, 3, v206
	v_add3_u32 v194, s11, v134, v135
	s_or_b32 s69, s72, 32
	ds_write2_b64 v194, v[132:133], v[130:131] offset1:4
	v_mul_u32_u24_e32 v130, 0x50, v195
	v_and_b32_e32 v190, 48, v174
	v_or_b32_e32 v134, s72, v195
	s_add_i32 s70, s10, s69
	v_pk_fma_f32 v[126:127], v[126:127], s[38:39], v[14:15] op_sel_hi:[1,0,1]
	v_add3_u32 v196, s11, v130, v190
	v_add_u32_e32 v134, s10, v134
	s_ashr_i32 s71, s70, 31
	v_pk_mul_f32 v[126:127], v[126:127], s[40:41] op_sel_hi:[1,0]
	ds_read_b128 v[130:133], v196
	v_ashrrev_i32_e32 v135, 31, v134
	s_lshl_b64 s[70:71], s[70:71], 11
	v_exp_f32_e32 v126, v126
	v_exp_f32_e32 v127, v127
	v_lshlrev_b64 v[134:135], 10, v[134:135]
	s_add_u32 s68, s54, s70
	v_lshl_add_u64 v[134:135], s[16:17], 0, v[134:135]
	s_addc_u32 s71, s55, s71
	v_lshl_add_u64 v[134:135], v[134:135], 0, s[74:75]
	v_mov_b32_e32 v191, v175
	s_add_u32 s70, s68, s76
	v_lshl_add_u64 v[134:135], v[134:135], 0, v[190:191]
	s_addc_u32 s71, s71, s77
	v_pk_fma_f32 v[128:129], v[128:129], s[38:39], v[16:17] op_sel_hi:[1,0,1]
	v_pk_fma_f32 v[122:123], v[122:123], s[38:39], v[10:11] op_sel_hi:[1,0,1]
	v_pk_add_f32 v[126:127], v[126:127], 1.0 op_sel_hi:[1,0]
	s_waitcnt lgkmcnt(0)
	global_store_dwordx4 v[134:135], v[130:133], off nt
	v_lshl_add_u64 v[134:135], s[70:71], 0, v[182:183]
	v_pk_mul_f32 v[122:123], v[122:123], s[40:41] op_sel_hi:[1,0]
	v_rcp_f32_e32 v216, v126
	v_rcp_f32_e32 v217, v127
	v_pk_mul_f32 v[126:127], v[128:129], s[40:41] op_sel_hi:[1,0]
	v_lshl_add_u64 v[134:135], v[134:135], 0, v[180:181]
	v_lshl_add_u64 v[138:139], s[70:71], 0, v[184:185]
	v_exp_f32_e32 v122, v122
	v_exp_f32_e32 v123, v123
	v_exp_f32_e32 v126, v126
	v_exp_f32_e32 v127, v127
	global_load_dwordx4 v[130:133], v174, s[78:79] offset:2048
	v_lshl_add_u64 v[138:139], v[138:139], 0, v[180:181]
	global_load_dwordx4 v[134:137], v[134:135], off
	v_pk_fma_f32 v[124:125], v[124:125], s[38:39], v[12:13] op_sel_hi:[1,0,1]
	global_load_dwordx4 v[138:141], v[138:139], off
	ds_write_b128 v207, v[150:153]
	ds_write_b128 v207, v[154:157] offset:1152
	v_pk_mul_f32 v[124:125], v[124:125], s[40:41] op_sel_hi:[1,0]
	v_pk_fma_f32 v[120:121], v[120:121], s[38:39], v[8:9] op_sel_hi:[1,0,1]
	v_pk_fma_f32 v[118:119], v[118:119], s[38:39], v[6:7] op_sel_hi:[1,0,1]
	v_pk_fma_f32 v[116:117], v[116:117], s[38:39], v[4:5] op_sel_hi:[1,0,1]
	v_pk_fma_f32 v[114:115], v[114:115], s[38:39], v[2:3] op_sel_hi:[1,0,1]
	ds_read_b128 v[150:153], v208
	ds_read_b128 v[154:157], v208 offset:64
	v_cvt_pk_f32_fp8_e32 v[210:211], v146
	v_cvt_pk_f32_fp8_sdwa v[212:213], v146 src0_sel:WORD_1
	v_cvt_pk_f32_fp8_e32 v[214:215], v147
	v_pk_add_f32 v[122:123], v[122:123], 1.0 op_sel_hi:[1,0]
	v_exp_f32_e32 v124, v124
	v_exp_f32_e32 v125, v125
	v_pk_add_f32 v[126:127], v[126:127], 1.0 op_sel_hi:[1,0]
	v_pk_mul_f32 v[118:119], v[118:119], s[40:41] op_sel_hi:[1,0]
	v_pk_mul_f32 v[114:115], v[114:115], s[40:41] op_sel_hi:[1,0]
	v_pk_mul_f32 v[120:121], v[120:121], s[40:41] op_sel_hi:[1,0]
	v_pk_mul_f32 v[116:117], v[116:117], s[40:41] op_sel_hi:[1,0]
	v_rcp_f32_e32 v122, v122
	v_rcp_f32_e32 v123, v123
	v_rcp_f32_e32 v126, v126
	v_rcp_f32_e32 v127, v127
	v_exp_f32_e32 v118, v118
	v_exp_f32_e32 v119, v119
	v_exp_f32_e32 v114, v114
	v_exp_f32_e32 v115, v115
	v_exp_f32_e32 v120, v120
	v_exp_f32_e32 v121, v121
	v_exp_f32_e32 v116, v116
	v_exp_f32_e32 v117, v117
	s_waitcnt lgkmcnt(1)
	v_lshlrev_b32_e32 v198, 16, v150
	v_and_b32_e32 v199, 0xffff0000, v150
	v_lshlrev_b32_e32 v150, 16, v151
	v_and_b32_e32 v151, 0xffff0000, v151
	v_lshlrev_b32_e32 v200, 16, v152
	v_and_b32_e32 v201, 0xffff0000, v152
	v_cvt_pk_f32_fp8_sdwa v[146:147], v147 src0_sel:WORD_1
	v_pk_add_f32 v[124:125], v[124:125], 1.0 op_sel_hi:[1,0]
	v_pk_mul_f32 v[128:129], v[210:211], s[42:43] op_sel_hi:[1,0]
	v_pk_mul_f32 v[210:211], v[212:213], s[42:43] op_sel_hi:[1,0]
	v_pk_mul_f32 v[212:213], v[214:215], s[42:43] op_sel_hi:[1,0]
	v_rcp_f32_e32 v124, v124
	v_rcp_f32_e32 v125, v125
	v_pk_fma_f32 v[126:127], v[126:127], v[210:211], v[150:151]
	v_pk_fma_f32 v[150:151], v[122:123], v[212:213], v[200:201]
	v_cvt_pk_f32_fp8_e32 v[200:201], v148
	v_cvt_pk_f32_fp8_sdwa v[210:211], v148 src0_sel:WORD_1
	v_cvt_pk_f32_fp8_e32 v[212:213], v149
	v_cvt_pk_f32_fp8_sdwa v[148:149], v149 src0_sel:WORD_1
	v_pk_add_f32 v[118:119], v[118:119], 1.0 op_sel_hi:[1,0]
	v_pk_add_f32 v[114:115], v[114:115], 1.0 op_sel_hi:[1,0]
	v_pk_add_f32 v[120:121], v[120:121], 1.0 op_sel_hi:[1,0]
	v_pk_add_f32 v[116:117], v[116:117], 1.0 op_sel_hi:[1,0]
	v_rcp_f32_e32 v118, v118
	v_rcp_f32_e32 v119, v119
	v_rcp_f32_e32 v114, v114
	v_rcp_f32_e32 v115, v115
	v_rcp_f32_e32 v120, v120
	v_rcp_f32_e32 v121, v121
	v_rcp_f32_e32 v116, v116
	v_rcp_f32_e32 v117, v117
	s_or_b32 s70, s80, 16
	s_ashr_i32 s71, s70, 31
	v_lshlrev_b32_e32 v152, 16, v153
	v_and_b32_e32 v153, 0xffff0000, v153
	v_pk_mul_f32 v[146:147], v[146:147], s[42:43] op_sel_hi:[1,0]
	s_lshl_b64 s[70:71], s[70:71], 11
	v_pk_fma_f32 v[128:129], v[216:217], v[128:129], v[198:199]
	v_pk_fma_f32 v[146:147], v[124:125], v[146:147], v[152:153]
	v_cvt_pk_bf16_f32 v122, v128, v129
	v_cvt_pk_bf16_f32 v123, v126, v127
	v_cvt_pk_bf16_f32 v124, v150, v151
	s_waitcnt lgkmcnt(0)
	v_lshlrev_b32_e32 v152, 16, v154
	v_cvt_pk_bf16_f32 v125, v146, v147
	v_and_b32_e32 v153, 0xffff0000, v154
	v_lshlrev_b32_e32 v154, 16, v155
	v_and_b32_e32 v155, 0xffff0000, v155
	v_lshlrev_b32_e32 v198, 16, v156
	v_and_b32_e32 v199, 0xffff0000, v156
	v_lshlrev_b32_e32 v156, 16, v157
	v_and_b32_e32 v157, 0xffff0000, v157
	v_pk_mul_f32 v[200:201], v[200:201], s[42:43] op_sel_hi:[1,0]
	v_pk_mul_f32 v[210:211], v[210:211], s[42:43] op_sel_hi:[1,0]
	v_pk_mul_f32 v[212:213], v[212:213], s[42:43] op_sel_hi:[1,0]
	v_pk_mul_f32 v[214:215], v[148:149], s[42:43] op_sel_hi:[1,0]
	s_add_u32 s68, s56, s70
	v_pk_fma_f32 v[148:149], v[120:121], v[210:211], v[154:155]
	v_pk_fma_f32 v[152:153], v[118:119], v[200:201], v[152:153]
	v_pk_fma_f32 v[154:155], v[116:117], v[214:215], v[156:157]
	v_pk_fma_f32 v[156:157], v[114:115], v[212:213], v[198:199]
	v_cvt_pk_bf16_f32 v114, v152, v153
	v_cvt_pk_bf16_f32 v115, v148, v149
	s_addc_u32 s71, s57, s71
	v_cvt_pk_bf16_f32 v116, v156, v157
	v_cvt_pk_bf16_f32 v117, v154, v155
	ds_write_b128 v208, v[122:125]
	ds_write_b128 v208, v[114:117] offset:64
	s_add_u32 s70, s68, s76
	ds_read_b128 v[114:117], v207
	ds_read_b128 v[118:121], v207 offset:1152
	s_addc_u32 s71, s71, s77
	v_lshl_add_u64 v[122:123], s[70:71], 0, v[182:183]
	v_lshl_add_u64 v[122:123], v[122:123], 0, v[180:181]
	s_waitcnt lgkmcnt(1)
	global_store_dwordx4 v[122:123], v[114:117], off nt
	s_or_b32 s68, s72, 48
	v_pk_fma_f32 v[110:111], v[110:111], s[38:39], v[14:15] op_sel_hi:[1,0,1]
	v_lshl_add_u64 v[114:115], s[70:71], 0, v[184:185]
	v_lshl_add_u64 v[114:115], v[114:115], 0, v[180:181]
	s_waitcnt lgkmcnt(0)
	global_store_dwordx4 v[114:115], v[118:121], off nt
	v_mov_b32_e32 v115, v175
	v_mov_b32_e32 v114, v175
	v_mov_b32_e32 v117, v175
	v_mov_b32_e32 v116, v175
	v_cvt_pk_fp8_f32 v115, v156, v157
	v_cvt_pk_fp8_f32 v114, v152, v153
	v_cvt_pk_fp8_f32 v117, v150, v151
	v_cvt_pk_fp8_f32 v116, v128, v129
	v_cvt_pk_fp8_f32 v115, v154, v155 op_sel:[0,0,1]
	v_cvt_pk_fp8_f32 v114, v148, v149 op_sel:[0,0,1]
	v_cvt_pk_fp8_f32 v117, v146, v147 op_sel:[0,0,1]
	v_cvt_pk_fp8_f32 v116, v126, v127 op_sel:[0,0,1]
	v_or_b32_e32 v118, s47, v195
	s_add_i32 s70, s10, s68
	v_add_u32_e32 v118, s10, v118
	ds_write2_b64 v194, v[116:117], v[114:115] offset1:4
	s_ashr_i32 s71, s70, 31
	ds_read_b128 v[114:117], v196
	v_ashrrev_i32_e32 v119, 31, v118
	s_lshl_b64 s[70:71], s[70:71], 11
	v_lshlrev_b64 v[118:119], 10, v[118:119]
	s_add_u32 s47, s54, s70
	v_lshl_add_u64 v[118:119], s[16:17], 0, v[118:119]
	s_addc_u32 s71, s55, s71
	v_lshl_add_u64 v[118:119], v[118:119], 0, s[74:75]
	s_add_u32 s70, s47, s76
	v_lshl_add_u64 v[118:119], v[118:119], 0, v[190:191]
	s_addc_u32 s71, s71, s77
	s_waitcnt lgkmcnt(0)
	global_store_dwordx4 v[118:119], v[114:117], off nt
	v_lshl_add_u64 v[118:119], s[70:71], 0, v[182:183]
	v_lshl_add_u64 v[118:119], v[118:119], 0, v[180:181]
	v_lshl_add_u64 v[122:123], s[70:71], 0, v[184:185]
	global_load_dwordx4 v[114:117], v174, s[78:79] offset:3072
	v_lshl_add_u64 v[122:123], v[122:123], 0, v[180:181]
	global_load_dwordx4 v[118:121], v[118:119], off
	v_pk_mul_f32 v[110:111], v[110:111], s[40:41] op_sel_hi:[1,0]
	global_load_dwordx4 v[122:125], v[122:123], off
	v_exp_f32_e32 v110, v110
	v_exp_f32_e32 v111, v111
	v_pk_fma_f32 v[112:113], v[112:113], s[38:39], v[16:17] op_sel_hi:[1,0,1]
	v_pk_fma_f32 v[106:107], v[106:107], s[38:39], v[10:11] op_sel_hi:[1,0,1]
	v_pk_fma_f32 v[108:109], v[108:109], s[38:39], v[12:13] op_sel_hi:[1,0,1]
	v_pk_add_f32 v[110:111], v[110:111], 1.0 op_sel_hi:[1,0]
	v_pk_mul_f32 v[106:107], v[106:107], s[40:41] op_sel_hi:[1,0]
	v_rcp_f32_e32 v216, v110
	v_rcp_f32_e32 v217, v111
	v_pk_mul_f32 v[110:111], v[112:113], s[40:41] op_sel_hi:[1,0]
	v_exp_f32_e32 v106, v106
	v_exp_f32_e32 v107, v107
	v_exp_f32_e32 v110, v110
	v_exp_f32_e32 v111, v111
	s_waitcnt vmcnt(7)
	ds_write_b128 v207, v[134:137]
	s_waitcnt vmcnt(6)
	ds_write_b128 v207, v[138:141] offset:1152
	v_pk_mul_f32 v[108:109], v[108:109], s[40:41] op_sel_hi:[1,0]
	v_pk_fma_f32 v[104:105], v[104:105], s[38:39], v[8:9] op_sel_hi:[1,0,1]
	v_pk_fma_f32 v[102:103], v[102:103], s[38:39], v[6:7] op_sel_hi:[1,0,1]
	v_pk_fma_f32 v[100:101], v[100:101], s[38:39], v[4:5] op_sel_hi:[1,0,1]
	v_pk_fma_f32 v[98:99], v[98:99], s[38:39], v[2:3] op_sel_hi:[1,0,1]
	ds_read_b128 v[134:137], v208
	ds_read_b128 v[138:141], v208 offset:64
	v_cvt_pk_f32_fp8_e32 v[210:211], v130
	v_cvt_pk_f32_fp8_sdwa v[212:213], v130 src0_sel:WORD_1
	v_cvt_pk_f32_fp8_e32 v[214:215], v131
	v_pk_add_f32 v[106:107], v[106:107], 1.0 op_sel_hi:[1,0]
	v_exp_f32_e32 v108, v108
	v_exp_f32_e32 v109, v109
	v_pk_add_f32 v[110:111], v[110:111], 1.0 op_sel_hi:[1,0]
	v_pk_mul_f32 v[102:103], v[102:103], s[40:41] op_sel_hi:[1,0]
	v_pk_mul_f32 v[98:99], v[98:99], s[40:41] op_sel_hi:[1,0]
	v_pk_mul_f32 v[104:105], v[104:105], s[40:41] op_sel_hi:[1,0]
	v_pk_mul_f32 v[100:101], v[100:101], s[40:41] op_sel_hi:[1,0]
	v_rcp_f32_e32 v106, v106
	v_rcp_f32_e32 v107, v107
	v_rcp_f32_e32 v110, v110
	v_rcp_f32_e32 v111, v111
	v_exp_f32_e32 v102, v102
	v_exp_f32_e32 v103, v103
	v_exp_f32_e32 v98, v98
	v_exp_f32_e32 v99, v99
	v_exp_f32_e32 v104, v104
	v_exp_f32_e32 v105, v105
	v_exp_f32_e32 v100, v100
	v_exp_f32_e32 v101, v101
	s_waitcnt lgkmcnt(1)
	v_lshlrev_b32_e32 v198, 16, v134
	v_and_b32_e32 v199, 0xffff0000, v134
	v_lshlrev_b32_e32 v134, 16, v135
	v_and_b32_e32 v135, 0xffff0000, v135
	v_lshlrev_b32_e32 v200, 16, v136
	v_and_b32_e32 v201, 0xffff0000, v136
	v_cvt_pk_f32_fp8_sdwa v[130:131], v131 src0_sel:WORD_1
	v_pk_add_f32 v[108:109], v[108:109], 1.0 op_sel_hi:[1,0]
	v_pk_mul_f32 v[112:113], v[210:211], s[42:43] op_sel_hi:[1,0]
	v_pk_mul_f32 v[210:211], v[212:213], s[42:43] op_sel_hi:[1,0]
	v_pk_mul_f32 v[212:213], v[214:215], s[42:43] op_sel_hi:[1,0]
	v_rcp_f32_e32 v108, v108
	v_rcp_f32_e32 v109, v109
	v_pk_fma_f32 v[110:111], v[110:111], v[210:211], v[134:135]
	v_pk_fma_f32 v[134:135], v[106:107], v[212:213], v[200:201]
	v_cvt_pk_f32_fp8_e32 v[200:201], v132
	v_cvt_pk_f32_fp8_sdwa v[210:211], v132 src0_sel:WORD_1
	v_cvt_pk_f32_fp8_e32 v[212:213], v133
	v_cvt_pk_f32_fp8_sdwa v[132:133], v133 src0_sel:WORD_1
	v_pk_add_f32 v[102:103], v[102:103], 1.0 op_sel_hi:[1,0]
	v_pk_add_f32 v[98:99], v[98:99], 1.0 op_sel_hi:[1,0]
	v_pk_add_f32 v[104:105], v[104:105], 1.0 op_sel_hi:[1,0]
	v_pk_add_f32 v[100:101], v[100:101], 1.0 op_sel_hi:[1,0]
	v_rcp_f32_e32 v102, v102
	v_rcp_f32_e32 v103, v103
	v_rcp_f32_e32 v98, v98
	v_rcp_f32_e32 v99, v99
	v_rcp_f32_e32 v104, v104
	v_rcp_f32_e32 v105, v105
	v_rcp_f32_e32 v100, v100
	v_rcp_f32_e32 v101, v101
	s_or_b32 s70, s80, 32
	s_ashr_i32 s71, s70, 31
	v_lshlrev_b32_e32 v136, 16, v137
	v_and_b32_e32 v137, 0xffff0000, v137
	v_pk_mul_f32 v[130:131], v[130:131], s[42:43] op_sel_hi:[1,0]
	s_lshl_b64 s[70:71], s[70:71], 11
	v_pk_fma_f32 v[112:113], v[216:217], v[112:113], v[198:199]
	v_pk_fma_f32 v[130:131], v[108:109], v[130:131], v[136:137]
	v_cvt_pk_bf16_f32 v106, v112, v113
	v_cvt_pk_bf16_f32 v107, v110, v111
	v_cvt_pk_bf16_f32 v108, v134, v135
	s_waitcnt lgkmcnt(0)
	v_lshlrev_b32_e32 v136, 16, v138
	v_cvt_pk_bf16_f32 v109, v130, v131
	v_and_b32_e32 v137, 0xffff0000, v138
	v_lshlrev_b32_e32 v138, 16, v139
	v_and_b32_e32 v139, 0xffff0000, v139
	v_lshlrev_b32_e32 v198, 16, v140
	v_and_b32_e32 v199, 0xffff0000, v140
	v_lshlrev_b32_e32 v140, 16, v141
	v_and_b32_e32 v141, 0xffff0000, v141
	v_pk_mul_f32 v[200:201], v[200:201], s[42:43] op_sel_hi:[1,0]
	v_pk_mul_f32 v[210:211], v[210:211], s[42:43] op_sel_hi:[1,0]
	v_pk_mul_f32 v[212:213], v[212:213], s[42:43] op_sel_hi:[1,0]
	v_pk_mul_f32 v[214:215], v[132:133], s[42:43] op_sel_hi:[1,0]
	s_add_u32 s47, s56, s70
	v_pk_fma_f32 v[132:133], v[104:105], v[210:211], v[138:139]
	v_pk_fma_f32 v[136:137], v[102:103], v[200:201], v[136:137]
	v_pk_fma_f32 v[138:139], v[100:101], v[214:215], v[140:141]
	v_pk_fma_f32 v[140:141], v[98:99], v[212:213], v[198:199]
	v_cvt_pk_bf16_f32 v98, v136, v137
	v_cvt_pk_bf16_f32 v99, v132, v133
	s_addc_u32 s71, s57, s71
	v_cvt_pk_bf16_f32 v100, v140, v141
	v_cvt_pk_bf16_f32 v101, v138, v139
	ds_write_b128 v208, v[106:109]
	ds_write_b128 v208, v[98:101] offset:64
	s_add_u32 s70, s47, s76
	ds_read_b128 v[98:101], v207
	ds_read_b128 v[102:105], v207 offset:1152
	s_addc_u32 s71, s71, s77
	v_lshl_add_u64 v[106:107], s[70:71], 0, v[182:183]
	v_lshl_add_u64 v[106:107], v[106:107], 0, v[180:181]
	s_waitcnt lgkmcnt(1)
	global_store_dwordx4 v[106:107], v[98:101], off nt
	s_or_b32 s47, s72, 0x80
	v_lshl_add_u64 v[192:193], s[78:79], 0, v[174:175]
	v_lshl_add_u64 v[98:99], s[70:71], 0, v[184:185]
	v_lshl_add_u64 v[98:99], v[98:99], 0, v[180:181]
	s_waitcnt lgkmcnt(0)
	global_store_dwordx4 v[98:99], v[102:105], off nt
	v_mov_b32_e32 v99, v175
	v_mov_b32_e32 v98, v175
	v_mov_b32_e32 v101, v175
	v_mov_b32_e32 v100, v175
	v_cvt_pk_fp8_f32 v99, v140, v141
	v_cvt_pk_fp8_f32 v98, v136, v137
	v_cvt_pk_fp8_f32 v101, v134, v135
	v_cvt_pk_fp8_f32 v100, v112, v113
	v_cvt_pk_fp8_f32 v99, v138, v139 op_sel:[0,0,1]
	v_cvt_pk_fp8_f32 v98, v132, v133 op_sel:[0,0,1]
	v_cvt_pk_fp8_f32 v101, v130, v131 op_sel:[0,0,1]
	v_cvt_pk_fp8_f32 v100, v110, v111 op_sel:[0,0,1]
	v_or_b32_e32 v102, s69, v195
	s_add_i32 s78, s10, s47
	v_pk_fma_f32 v[94:95], v[94:95], s[38:39], v[14:15] op_sel_hi:[1,0,1]
	ds_write2_b64 v194, v[100:101], v[98:99] offset1:4
	v_add_u32_e32 v102, s10, v102
	s_ashr_i32 s79, s78, 31
	v_pk_mul_f32 v[94:95], v[94:95], s[40:41] op_sel_hi:[1,0]
	ds_read_b128 v[98:101], v196
	v_ashrrev_i32_e32 v103, 31, v102
	s_movk_i32 s69, 0x1000
	s_lshl_b64 s[82:83], s[78:79], 11
	v_exp_f32_e32 v94, v94
	v_exp_f32_e32 v95, v95
	v_lshlrev_b64 v[102:103], 10, v[102:103]
	v_add_co_u32_e32 v192, vcc, s69, v192
	s_add_u32 s69, s54, s82
	v_lshl_add_u64 v[102:103], s[16:17], 0, v[102:103]
	s_addc_u32 s71, s55, s83
	v_lshl_add_u64 v[102:103], v[102:103], 0, s[74:75]
	s_add_u32 s70, s69, s76
	v_lshl_add_u64 v[102:103], v[102:103], 0, v[190:191]
	s_addc_u32 s71, s71, s77
	v_pk_fma_f32 v[96:97], v[96:97], s[38:39], v[16:17] op_sel_hi:[1,0,1]
	v_pk_fma_f32 v[90:91], v[90:91], s[38:39], v[10:11] op_sel_hi:[1,0,1]
	v_pk_add_f32 v[94:95], v[94:95], 1.0 op_sel_hi:[1,0]
	s_waitcnt lgkmcnt(0)
	global_store_dwordx4 v[102:103], v[98:101], off nt
	v_lshl_add_u64 v[102:103], s[70:71], 0, v[182:183]
	v_pk_mul_f32 v[90:91], v[90:91], s[40:41] op_sel_hi:[1,0]
	v_rcp_f32_e32 v216, v94
	v_rcp_f32_e32 v217, v95
	v_pk_mul_f32 v[94:95], v[96:97], s[40:41] op_sel_hi:[1,0]
	v_lshl_add_u64 v[102:103], v[102:103], 0, v[180:181]
	v_lshl_add_u64 v[106:107], s[70:71], 0, v[184:185]
	v_exp_f32_e32 v90, v90
	v_exp_f32_e32 v91, v91
	v_exp_f32_e32 v94, v94
	v_exp_f32_e32 v95, v95
	v_addc_co_u32_e32 v193, vcc, 0, v193, vcc
	global_load_dwordx4 v[102:105], v[102:103], off
	v_lshl_add_u64 v[106:107], v[106:107], 0, v[180:181]
	global_load_dwordx4 v[98:101], v[192:193], off
	v_pk_fma_f32 v[92:93], v[92:93], s[38:39], v[12:13] op_sel_hi:[1,0,1]
	global_load_dwordx4 v[106:109], v[106:107], off
	s_waitcnt vmcnt(7)
	ds_write_b128 v207, v[118:121]
	s_waitcnt vmcnt(6)
	ds_write_b128 v207, v[122:125] offset:1152
	v_pk_mul_f32 v[92:93], v[92:93], s[40:41] op_sel_hi:[1,0]
	v_pk_fma_f32 v[88:89], v[88:89], s[38:39], v[8:9] op_sel_hi:[1,0,1]
	v_pk_fma_f32 v[86:87], v[86:87], s[38:39], v[6:7] op_sel_hi:[1,0,1]
	v_pk_fma_f32 v[84:85], v[84:85], s[38:39], v[4:5] op_sel_hi:[1,0,1]
	v_pk_fma_f32 v[82:83], v[82:83], s[38:39], v[2:3] op_sel_hi:[1,0,1]
	ds_read_b128 v[118:121], v208
	ds_read_b128 v[122:125], v208 offset:64
	v_cvt_pk_f32_fp8_e32 v[210:211], v114
	v_cvt_pk_f32_fp8_sdwa v[212:213], v114 src0_sel:WORD_1
	v_cvt_pk_f32_fp8_e32 v[214:215], v115
	v_pk_add_f32 v[90:91], v[90:91], 1.0 op_sel_hi:[1,0]
	v_exp_f32_e32 v92, v92
	v_exp_f32_e32 v93, v93
	v_pk_add_f32 v[94:95], v[94:95], 1.0 op_sel_hi:[1,0]
	v_pk_mul_f32 v[86:87], v[86:87], s[40:41] op_sel_hi:[1,0]
	v_pk_mul_f32 v[82:83], v[82:83], s[40:41] op_sel_hi:[1,0]
	v_pk_mul_f32 v[88:89], v[88:89], s[40:41] op_sel_hi:[1,0]
	v_pk_mul_f32 v[84:85], v[84:85], s[40:41] op_sel_hi:[1,0]
	v_rcp_f32_e32 v90, v90
	v_rcp_f32_e32 v91, v91
	v_rcp_f32_e32 v94, v94
	v_rcp_f32_e32 v95, v95
	v_exp_f32_e32 v86, v86
	v_exp_f32_e32 v87, v87
	v_exp_f32_e32 v82, v82
	v_exp_f32_e32 v83, v83
	v_exp_f32_e32 v88, v88
	v_exp_f32_e32 v89, v89
	v_exp_f32_e32 v84, v84
	v_exp_f32_e32 v85, v85
	s_waitcnt lgkmcnt(1)
	v_lshlrev_b32_e32 v198, 16, v118
	v_and_b32_e32 v199, 0xffff0000, v118
	v_lshlrev_b32_e32 v118, 16, v119
	v_and_b32_e32 v119, 0xffff0000, v119
	v_lshlrev_b32_e32 v200, 16, v120
	v_and_b32_e32 v201, 0xffff0000, v120
	v_cvt_pk_f32_fp8_sdwa v[114:115], v115 src0_sel:WORD_1
	v_pk_add_f32 v[92:93], v[92:93], 1.0 op_sel_hi:[1,0]
	v_pk_mul_f32 v[96:97], v[210:211], s[42:43] op_sel_hi:[1,0]
	v_pk_mul_f32 v[210:211], v[212:213], s[42:43] op_sel_hi:[1,0]
	v_pk_mul_f32 v[212:213], v[214:215], s[42:43] op_sel_hi:[1,0]
	v_rcp_f32_e32 v92, v92
	v_rcp_f32_e32 v93, v93
	v_pk_fma_f32 v[94:95], v[94:95], v[210:211], v[118:119]
	v_pk_fma_f32 v[118:119], v[90:91], v[212:213], v[200:201]
	v_cvt_pk_f32_fp8_e32 v[200:201], v116
	v_cvt_pk_f32_fp8_sdwa v[210:211], v116 src0_sel:WORD_1
	v_cvt_pk_f32_fp8_e32 v[212:213], v117
	v_cvt_pk_f32_fp8_sdwa v[116:117], v117 src0_sel:WORD_1
	v_pk_add_f32 v[86:87], v[86:87], 1.0 op_sel_hi:[1,0]
	v_pk_add_f32 v[82:83], v[82:83], 1.0 op_sel_hi:[1,0]
	v_pk_add_f32 v[88:89], v[88:89], 1.0 op_sel_hi:[1,0]
	v_pk_add_f32 v[84:85], v[84:85], 1.0 op_sel_hi:[1,0]
	v_rcp_f32_e32 v86, v86
	v_rcp_f32_e32 v87, v87
	v_rcp_f32_e32 v82, v82
	v_rcp_f32_e32 v83, v83
	v_rcp_f32_e32 v88, v88
	v_rcp_f32_e32 v89, v89
	v_rcp_f32_e32 v84, v84
	v_rcp_f32_e32 v85, v85
	s_or_b32 s70, s80, 48
	s_ashr_i32 s71, s70, 31
	v_lshlrev_b32_e32 v120, 16, v121
	v_and_b32_e32 v121, 0xffff0000, v121
	v_pk_mul_f32 v[114:115], v[114:115], s[42:43] op_sel_hi:[1,0]
	s_lshl_b64 s[70:71], s[70:71], 11
	v_pk_fma_f32 v[96:97], v[216:217], v[96:97], v[198:199]
	v_pk_fma_f32 v[114:115], v[92:93], v[114:115], v[120:121]
	v_cvt_pk_bf16_f32 v90, v96, v97
	v_cvt_pk_bf16_f32 v91, v94, v95
	v_cvt_pk_bf16_f32 v92, v118, v119
	s_waitcnt lgkmcnt(0)
	v_lshlrev_b32_e32 v120, 16, v122
	v_cvt_pk_bf16_f32 v93, v114, v115
	v_and_b32_e32 v121, 0xffff0000, v122
	v_lshlrev_b32_e32 v122, 16, v123
	v_and_b32_e32 v123, 0xffff0000, v123
	v_lshlrev_b32_e32 v198, 16, v124
	v_and_b32_e32 v199, 0xffff0000, v124
	v_lshlrev_b32_e32 v124, 16, v125
	v_and_b32_e32 v125, 0xffff0000, v125
	v_pk_mul_f32 v[200:201], v[200:201], s[42:43] op_sel_hi:[1,0]
	v_pk_mul_f32 v[210:211], v[210:211], s[42:43] op_sel_hi:[1,0]
	v_pk_mul_f32 v[212:213], v[212:213], s[42:43] op_sel_hi:[1,0]
	v_pk_mul_f32 v[214:215], v[116:117], s[42:43] op_sel_hi:[1,0]
	s_add_u32 s69, s56, s70
	v_pk_fma_f32 v[116:117], v[88:89], v[210:211], v[122:123]
	v_pk_fma_f32 v[120:121], v[86:87], v[200:201], v[120:121]
	v_pk_fma_f32 v[122:123], v[84:85], v[214:215], v[124:125]
	v_pk_fma_f32 v[124:125], v[82:83], v[212:213], v[198:199]
	v_cvt_pk_bf16_f32 v82, v120, v121
	v_cvt_pk_bf16_f32 v83, v116, v117
	s_addc_u32 s71, s57, s71
	v_cvt_pk_bf16_f32 v84, v124, v125
	v_cvt_pk_bf16_f32 v85, v122, v123
	ds_write_b128 v208, v[90:93]
	ds_write_b128 v208, v[82:85] offset:64
	s_add_u32 s70, s69, s76
	ds_read_b128 v[82:85], v207
	ds_read_b128 v[86:89], v207 offset:1152
	s_addc_u32 s71, s71, s77
	v_lshl_add_u64 v[90:91], s[70:71], 0, v[182:183]
	v_lshl_add_u64 v[90:91], v[90:91], 0, v[180:181]
	s_waitcnt lgkmcnt(1)
	global_store_dwordx4 v[90:91], v[82:85], off nt
	v_pk_fma_f32 v[80:81], v[80:81], s[38:39], v[16:17] op_sel_hi:[1,0,1]
	v_pk_fma_f32 v[78:79], v[78:79], s[38:39], v[14:15] op_sel_hi:[1,0,1]
	v_lshl_add_u64 v[82:83], s[70:71], 0, v[184:185]
	v_lshl_add_u64 v[82:83], v[82:83], 0, v[180:181]
	s_waitcnt lgkmcnt(0)
	global_store_dwordx4 v[82:83], v[86:89], off nt
	v_mov_b32_e32 v83, v175
	v_mov_b32_e32 v82, v175
	v_mov_b32_e32 v85, v175
	v_mov_b32_e32 v84, v175
	v_cvt_pk_fp8_f32 v83, v124, v125
	v_cvt_pk_fp8_f32 v82, v120, v121
	v_cvt_pk_fp8_f32 v85, v118, v119
	v_cvt_pk_fp8_f32 v84, v96, v97
	v_cvt_pk_fp8_f32 v83, v122, v123 op_sel:[0,0,1]
	v_cvt_pk_fp8_f32 v82, v116, v117 op_sel:[0,0,1]
	v_cvt_pk_fp8_f32 v85, v114, v115 op_sel:[0,0,1]
	v_cvt_pk_fp8_f32 v84, v94, v95 op_sel:[0,0,1]
	v_or_b32_e32 v86, s68, v195
	s_or_b32 s68, s72, 0x90
	s_add_i32 s70, s10, s68
	ds_write2_b64 v194, v[84:85], v[82:83] offset1:4
	v_add_u32_e32 v86, s10, v86
	s_ashr_i32 s71, s70, 31
	ds_read_b128 v[82:85], v196
	v_ashrrev_i32_e32 v87, 31, v86
	s_lshl_b64 s[70:71], s[70:71], 11
	v_lshlrev_b64 v[86:87], 10, v[86:87]
	s_add_u32 s69, s54, s70
	v_lshl_add_u64 v[86:87], s[16:17], 0, v[86:87]
	s_addc_u32 s71, s55, s71
	v_lshl_add_u64 v[86:87], v[86:87], 0, s[74:75]
	s_add_u32 s70, s69, s76
	v_lshl_add_u64 v[86:87], v[86:87], 0, v[190:191]
	s_addc_u32 s71, s71, s77
	s_waitcnt lgkmcnt(0)
	global_store_dwordx4 v[86:87], v[82:85], off nt
	v_lshl_add_u64 v[86:87], s[70:71], 0, v[182:183]
	v_lshl_add_u64 v[86:87], v[86:87], 0, v[180:181]
	v_lshl_add_u64 v[90:91], s[70:71], 0, v[184:185]
	global_load_dwordx4 v[86:89], v[86:87], off
	v_lshl_add_u64 v[90:91], v[90:91], 0, v[180:181]
	global_load_dwordx4 v[82:85], v[192:193], off offset:1024
	v_pk_fma_f32 v[74:75], v[74:75], s[38:39], v[10:11] op_sel_hi:[1,0,1]
	global_load_dwordx4 v[90:93], v[90:91], off
	v_pk_mul_f32 v[78:79], v[78:79], s[40:41] op_sel_hi:[1,0]
	v_pk_mul_f32 v[74:75], v[74:75], s[40:41] op_sel_hi:[1,0]
	v_pk_mul_f32 v[80:81], v[80:81], s[40:41] op_sel_hi:[1,0]
	v_exp_f32_e32 v78, v78
	v_exp_f32_e32 v79, v79
	v_exp_f32_e32 v74, v74
	v_exp_f32_e32 v75, v75
	v_exp_f32_e32 v80, v80
	v_exp_f32_e32 v81, v81
	v_pk_fma_f32 v[76:77], v[76:77], s[38:39], v[12:13] op_sel_hi:[1,0,1]
	s_waitcnt vmcnt(8)
	ds_write_b128 v207, v[102:105]
	s_waitcnt vmcnt(6)
	ds_write_b128 v207, v[106:109] offset:1152
	v_pk_mul_f32 v[76:77], v[76:77], s[40:41] op_sel_hi:[1,0]
	v_pk_fma_f32 v[72:73], v[72:73], s[38:39], v[8:9] op_sel_hi:[1,0,1]
	v_pk_fma_f32 v[70:71], v[70:71], s[38:39], v[6:7] op_sel_hi:[1,0,1]
	v_pk_fma_f32 v[68:69], v[68:69], s[38:39], v[4:5] op_sel_hi:[1,0,1]
	v_pk_fma_f32 v[66:67], v[66:67], s[38:39], v[2:3] op_sel_hi:[1,0,1]
	ds_read_b128 v[102:105], v208
	ds_read_b128 v[106:109], v208 offset:64
	v_cvt_pk_f32_fp8_e32 v[210:211], v98
	v_cvt_pk_f32_fp8_sdwa v[212:213], v98 src0_sel:WORD_1
	v_cvt_pk_f32_fp8_e32 v[214:215], v99
	v_cvt_pk_f32_fp8_sdwa v[98:99], v99 src0_sel:WORD_1
	v_pk_add_f32 v[78:79], v[78:79], 1.0 op_sel_hi:[1,0]
	v_pk_add_f32 v[74:75], v[74:75], 1.0 op_sel_hi:[1,0]
	v_exp_f32_e32 v76, v76
	v_exp_f32_e32 v77, v77
	v_pk_add_f32 v[80:81], v[80:81], 1.0 op_sel_hi:[1,0]
	v_pk_mul_f32 v[70:71], v[70:71], s[40:41] op_sel_hi:[1,0]
	v_pk_mul_f32 v[66:67], v[66:67], s[40:41] op_sel_hi:[1,0]
	v_pk_mul_f32 v[72:73], v[72:73], s[40:41] op_sel_hi:[1,0]
	v_pk_mul_f32 v[68:69], v[68:69], s[40:41] op_sel_hi:[1,0]
	v_rcp_f32_e32 v78, v78
	v_rcp_f32_e32 v79, v79
	v_rcp_f32_e32 v74, v74
	v_rcp_f32_e32 v75, v75
	v_rcp_f32_e32 v80, v80
	v_rcp_f32_e32 v81, v81
	v_exp_f32_e32 v70, v70
	v_exp_f32_e32 v71, v71
	v_exp_f32_e32 v66, v66
	v_exp_f32_e32 v67, v67
	v_exp_f32_e32 v72, v72
	v_exp_f32_e32 v73, v73
	v_exp_f32_e32 v68, v68
	v_exp_f32_e32 v69, v69
	s_waitcnt lgkmcnt(1)
	v_lshlrev_b32_e32 v198, 16, v102
	v_and_b32_e32 v199, 0xffff0000, v102
	v_lshlrev_b32_e32 v102, 16, v103
	v_and_b32_e32 v103, 0xffff0000, v103
	v_lshlrev_b32_e32 v200, 16, v104
	v_and_b32_e32 v201, 0xffff0000, v104
	v_pk_add_f32 v[76:77], v[76:77], 1.0 op_sel_hi:[1,0]
	v_pk_mul_f32 v[212:213], v[212:213], s[42:43] op_sel_hi:[1,0]
	v_pk_mul_f32 v[210:211], v[210:211], s[42:43] op_sel_hi:[1,0]
	v_pk_mul_f32 v[216:217], v[98:99], s[42:43] op_sel_hi:[1,0]
	v_pk_mul_f32 v[98:99], v[214:215], s[42:43] op_sel_hi:[1,0]
	v_rcp_f32_e32 v76, v76
	v_rcp_f32_e32 v77, v77
	v_pk_fma_f32 v[78:79], v[78:79], v[210:211], v[198:199]
	v_pk_fma_f32 v[80:81], v[80:81], v[212:213], v[102:103]
	v_pk_fma_f32 v[98:99], v[74:75], v[98:99], v[200:201]
	v_cvt_pk_f32_fp8_e32 v[200:201], v100
	v_cvt_pk_f32_fp8_sdwa v[210:211], v100 src0_sel:WORD_1
	v_cvt_pk_f32_fp8_e32 v[212:213], v101
	v_cvt_pk_f32_fp8_sdwa v[100:101], v101 src0_sel:WORD_1
	v_pk_add_f32 v[70:71], v[70:71], 1.0 op_sel_hi:[1,0]
	v_pk_add_f32 v[66:67], v[66:67], 1.0 op_sel_hi:[1,0]
	v_pk_add_f32 v[72:73], v[72:73], 1.0 op_sel_hi:[1,0]
	v_pk_add_f32 v[68:69], v[68:69], 1.0 op_sel_hi:[1,0]
	v_rcp_f32_e32 v70, v70
	v_rcp_f32_e32 v71, v71
	v_rcp_f32_e32 v66, v66
	v_rcp_f32_e32 v67, v67
	v_rcp_f32_e32 v72, v72
	v_rcp_f32_e32 v73, v73
	v_rcp_f32_e32 v68, v68
	v_rcp_f32_e32 v69, v69
	v_lshlrev_b32_e32 v104, 16, v105
	v_and_b32_e32 v105, 0xffff0000, v105
	v_pk_fma_f32 v[102:103], v[76:77], v[216:217], v[104:105]
	v_cvt_pk_bf16_f32 v74, v78, v79
	v_cvt_pk_bf16_f32 v75, v80, v81
	v_cvt_pk_bf16_f32 v76, v98, v99
	s_waitcnt lgkmcnt(0)
	v_lshlrev_b32_e32 v104, 16, v106
	v_cvt_pk_bf16_f32 v77, v102, v103
	v_and_b32_e32 v105, 0xffff0000, v106
	v_lshlrev_b32_e32 v106, 16, v107
	v_and_b32_e32 v107, 0xffff0000, v107
	v_lshlrev_b32_e32 v198, 16, v108
	v_and_b32_e32 v199, 0xffff0000, v108
	v_lshlrev_b32_e32 v108, 16, v109
	v_and_b32_e32 v109, 0xffff0000, v109
	v_pk_mul_f32 v[210:211], v[210:211], s[42:43] op_sel_hi:[1,0]
	v_pk_mul_f32 v[200:201], v[200:201], s[42:43] op_sel_hi:[1,0]
	v_pk_mul_f32 v[214:215], v[100:101], s[42:43] op_sel_hi:[1,0]
	v_pk_mul_f32 v[212:213], v[212:213], s[42:43] op_sel_hi:[1,0]
	s_add_u32 s69, s56, s82
	v_pk_fma_f32 v[100:101], v[70:71], v[200:201], v[104:105]
	v_pk_fma_f32 v[104:105], v[72:73], v[210:211], v[106:107]
	v_pk_fma_f32 v[106:107], v[66:67], v[212:213], v[198:199]
	v_pk_fma_f32 v[108:109], v[68:69], v[214:215], v[108:109]
	v_cvt_pk_bf16_f32 v66, v100, v101
	v_cvt_pk_bf16_f32 v67, v104, v105
	v_cvt_pk_bf16_f32 v68, v106, v107
	s_addc_u32 s71, s57, s83
	v_cvt_pk_bf16_f32 v69, v108, v109
	ds_write_b128 v208, v[74:77]
	ds_write_b128 v208, v[66:69] offset:64
	s_add_u32 s70, s69, s76
	ds_read_b128 v[66:69], v207
	ds_read_b128 v[70:73], v207 offset:1152
	s_addc_u32 s71, s71, s77
	v_lshl_add_u64 v[74:75], s[70:71], 0, v[182:183]
	v_lshl_add_u64 v[74:75], v[74:75], 0, v[180:181]
	s_waitcnt lgkmcnt(1)
	global_store_dwordx4 v[74:75], v[66:69], off nt
	v_pk_fma_f32 v[64:65], v[64:65], s[38:39], v[16:17] op_sel_hi:[1,0,1]
	v_pk_fma_f32 v[62:63], v[62:63], s[38:39], v[14:15] op_sel_hi:[1,0,1]
	v_lshl_add_u64 v[66:67], s[70:71], 0, v[184:185]
	v_lshl_add_u64 v[66:67], v[66:67], 0, v[180:181]
	s_waitcnt lgkmcnt(0)
	global_store_dwordx4 v[66:67], v[70:73], off nt
	v_mov_b32_e32 v67, v175
	v_mov_b32_e32 v66, v175
	v_mov_b32_e32 v69, v175
	v_mov_b32_e32 v68, v175
	v_cvt_pk_fp8_f32 v67, v106, v107
	v_cvt_pk_fp8_f32 v66, v100, v101
	v_cvt_pk_fp8_f32 v69, v98, v99
	v_cvt_pk_fp8_f32 v68, v78, v79
	v_cvt_pk_fp8_f32 v67, v108, v109 op_sel:[0,0,1]
	v_cvt_pk_fp8_f32 v66, v104, v105 op_sel:[0,0,1]
	v_cvt_pk_fp8_f32 v69, v102, v103 op_sel:[0,0,1]
	v_cvt_pk_fp8_f32 v68, v80, v81 op_sel:[0,0,1]
	v_or_b32_e32 v70, s47, v195
	v_add_u32_e32 v70, s10, v70
	s_or_b32 s47, s72, 0xa0
	ds_write2_b64 v194, v[68:69], v[66:67] offset1:4
	ds_read_b128 v[66:69], v196
	v_ashrrev_i32_e32 v71, 31, v70
	s_add_i32 s70, s10, s47
	v_lshlrev_b64 v[70:71], 10, v[70:71]
	s_ashr_i32 s71, s70, 31
	v_lshl_add_u64 v[70:71], s[16:17], 0, v[70:71]
	s_lshl_b64 s[70:71], s[70:71], 11
	v_lshl_add_u64 v[70:71], v[70:71], 0, s[74:75]
	s_add_u32 s69, s54, s70
	v_lshl_add_u64 v[70:71], v[70:71], 0, v[190:191]
	s_addc_u32 s71, s55, s71
	v_pk_fma_f32 v[58:59], v[58:59], s[38:39], v[10:11] op_sel_hi:[1,0,1]
	s_waitcnt lgkmcnt(0)
	global_store_dwordx4 v[70:71], v[66:69], off nt
	s_add_u32 s70, s69, s76
	v_pk_mul_f32 v[62:63], v[62:63], s[40:41] op_sel_hi:[1,0]
	v_pk_mul_f32 v[58:59], v[58:59], s[40:41] op_sel_hi:[1,0]
	v_pk_mul_f32 v[64:65], v[64:65], s[40:41] op_sel_hi:[1,0]
	s_addc_u32 s71, s71, s77
	v_exp_f32_e32 v62, v62
	v_exp_f32_e32 v63, v63
	v_exp_f32_e32 v58, v58
	v_exp_f32_e32 v59, v59
	v_exp_f32_e32 v64, v64
	v_exp_f32_e32 v65, v65
	global_load_dwordx4 v[66:69], v[192:193], off offset:2048
	v_lshl_add_u64 v[70:71], s[70:71], 0, v[182:183]
	v_lshl_add_u64 v[74:75], s[70:71], 0, v[184:185]
	v_lshl_add_u64 v[70:71], v[70:71], 0, v[180:181]
	v_lshl_add_u64 v[74:75], v[74:75], 0, v[180:181]
	v_pk_fma_f32 v[60:61], v[60:61], s[38:39], v[12:13] op_sel_hi:[1,0,1]
	global_load_dwordx4 v[70:73], v[70:71], off
	v_pk_mul_f32 v[60:61], v[60:61], s[40:41] op_sel_hi:[1,0]
	global_load_dwordx4 v[74:77], v[74:75], off
	s_waitcnt vmcnt(8)
	ds_write_b128 v207, v[86:89]
	s_waitcnt vmcnt(6)
	ds_write_b128 v207, v[90:93] offset:1152
	v_pk_fma_f32 v[56:57], v[56:57], s[38:39], v[8:9] op_sel_hi:[1,0,1]
	v_pk_fma_f32 v[54:55], v[54:55], s[38:39], v[6:7] op_sel_hi:[1,0,1]
	v_pk_fma_f32 v[52:53], v[52:53], s[38:39], v[4:5] op_sel_hi:[1,0,1]
	v_pk_fma_f32 v[50:51], v[50:51], s[38:39], v[2:3] op_sel_hi:[1,0,1]
	ds_read_b128 v[86:89], v208
	ds_read_b128 v[90:93], v208 offset:64
	v_cvt_pk_f32_fp8_e32 v[210:211], v82
	v_cvt_pk_f32_fp8_sdwa v[212:213], v82 src0_sel:WORD_1
	v_cvt_pk_f32_fp8_e32 v[214:215], v83
	v_cvt_pk_f32_fp8_sdwa v[82:83], v83 src0_sel:WORD_1
	v_pk_add_f32 v[62:63], v[62:63], 1.0 op_sel_hi:[1,0]
	v_pk_add_f32 v[58:59], v[58:59], 1.0 op_sel_hi:[1,0]
	v_exp_f32_e32 v60, v60
	v_exp_f32_e32 v61, v61
	v_pk_add_f32 v[64:65], v[64:65], 1.0 op_sel_hi:[1,0]
	v_pk_mul_f32 v[54:55], v[54:55], s[40:41] op_sel_hi:[1,0]
	v_pk_mul_f32 v[50:51], v[50:51], s[40:41] op_sel_hi:[1,0]
	v_pk_mul_f32 v[56:57], v[56:57], s[40:41] op_sel_hi:[1,0]
	v_pk_mul_f32 v[52:53], v[52:53], s[40:41] op_sel_hi:[1,0]
	v_rcp_f32_e32 v62, v62
	v_rcp_f32_e32 v63, v63
	v_rcp_f32_e32 v58, v58
	v_rcp_f32_e32 v59, v59
	v_rcp_f32_e32 v64, v64
	v_rcp_f32_e32 v65, v65
	v_exp_f32_e32 v54, v54
	v_exp_f32_e32 v55, v55
	v_exp_f32_e32 v50, v50
	v_exp_f32_e32 v51, v51
	v_exp_f32_e32 v56, v56
	v_exp_f32_e32 v57, v57
	v_exp_f32_e32 v52, v52
	v_exp_f32_e32 v53, v53
	s_waitcnt lgkmcnt(1)
	v_lshlrev_b32_e32 v198, 16, v86
	v_and_b32_e32 v199, 0xffff0000, v86
	v_lshlrev_b32_e32 v86, 16, v87
	v_and_b32_e32 v87, 0xffff0000, v87
	v_lshlrev_b32_e32 v200, 16, v88
	v_and_b32_e32 v201, 0xffff0000, v88
	v_pk_add_f32 v[60:61], v[60:61], 1.0 op_sel_hi:[1,0]
	v_pk_mul_f32 v[212:213], v[212:213], s[42:43] op_sel_hi:[1,0]
	v_pk_mul_f32 v[210:211], v[210:211], s[42:43] op_sel_hi:[1,0]
	v_pk_mul_f32 v[216:217], v[82:83], s[42:43] op_sel_hi:[1,0]
	v_pk_mul_f32 v[82:83], v[214:215], s[42:43] op_sel_hi:[1,0]
	v_rcp_f32_e32 v60, v60
	v_rcp_f32_e32 v61, v61
	v_pk_fma_f32 v[62:63], v[62:63], v[210:211], v[198:199]
	v_pk_fma_f32 v[64:65], v[64:65], v[212:213], v[86:87]
	v_pk_fma_f32 v[82:83], v[58:59], v[82:83], v[200:201]
	v_cvt_pk_f32_fp8_e32 v[200:201], v84
	v_cvt_pk_f32_fp8_sdwa v[210:211], v84 src0_sel:WORD_1
	v_cvt_pk_f32_fp8_e32 v[212:213], v85
	v_cvt_pk_f32_fp8_sdwa v[84:85], v85 src0_sel:WORD_1
	v_pk_add_f32 v[54:55], v[54:55], 1.0 op_sel_hi:[1,0]
	v_pk_add_f32 v[50:51], v[50:51], 1.0 op_sel_hi:[1,0]
	v_pk_add_f32 v[56:57], v[56:57], 1.0 op_sel_hi:[1,0]
	v_pk_add_f32 v[52:53], v[52:53], 1.0 op_sel_hi:[1,0]
	v_rcp_f32_e32 v54, v54
	v_rcp_f32_e32 v55, v55
	v_rcp_f32_e32 v50, v50
	v_rcp_f32_e32 v51, v51
	v_rcp_f32_e32 v56, v56
	v_rcp_f32_e32 v57, v57
	v_rcp_f32_e32 v52, v52
	v_rcp_f32_e32 v53, v53
	s_or_b32 s70, s78, 16
	s_ashr_i32 s71, s70, 31
	v_lshlrev_b32_e32 v88, 16, v89
	v_and_b32_e32 v89, 0xffff0000, v89
	s_lshl_b64 s[70:71], s[70:71], 11
	v_pk_fma_f32 v[86:87], v[60:61], v[216:217], v[88:89]
	v_cvt_pk_bf16_f32 v58, v62, v63
	v_cvt_pk_bf16_f32 v59, v64, v65
	v_cvt_pk_bf16_f32 v60, v82, v83
	s_waitcnt lgkmcnt(0)
	v_lshlrev_b32_e32 v88, 16, v90
	v_cvt_pk_bf16_f32 v61, v86, v87
	v_and_b32_e32 v89, 0xffff0000, v90
	v_lshlrev_b32_e32 v90, 16, v91
	v_and_b32_e32 v91, 0xffff0000, v91
	v_lshlrev_b32_e32 v198, 16, v92
	v_and_b32_e32 v199, 0xffff0000, v92
	v_lshlrev_b32_e32 v92, 16, v93
	v_and_b32_e32 v93, 0xffff0000, v93
	v_pk_mul_f32 v[210:211], v[210:211], s[42:43] op_sel_hi:[1,0]
	v_pk_mul_f32 v[200:201], v[200:201], s[42:43] op_sel_hi:[1,0]
	v_pk_mul_f32 v[214:215], v[84:85], s[42:43] op_sel_hi:[1,0]
	v_pk_mul_f32 v[212:213], v[212:213], s[42:43] op_sel_hi:[1,0]
	s_add_u32 s69, s56, s70
	v_pk_fma_f32 v[84:85], v[54:55], v[200:201], v[88:89]
	v_pk_fma_f32 v[88:89], v[56:57], v[210:211], v[90:91]
	v_pk_fma_f32 v[90:91], v[50:51], v[212:213], v[198:199]
	v_pk_fma_f32 v[92:93], v[52:53], v[214:215], v[92:93]
	v_cvt_pk_bf16_f32 v50, v84, v85
	v_cvt_pk_bf16_f32 v51, v88, v89
	v_cvt_pk_bf16_f32 v52, v90, v91
	s_addc_u32 s71, s57, s71
	v_cvt_pk_bf16_f32 v53, v92, v93
	ds_write_b128 v208, v[58:61]
	ds_write_b128 v208, v[50:53] offset:64
	s_add_u32 s70, s69, s76
	ds_read_b128 v[50:53], v207
	ds_read_b128 v[54:57], v207 offset:1152
	s_addc_u32 s71, s71, s77
	v_lshl_add_u64 v[58:59], s[70:71], 0, v[182:183]
	v_lshl_add_u64 v[58:59], v[58:59], 0, v[180:181]
	s_waitcnt lgkmcnt(1)
	global_store_dwordx4 v[58:59], v[50:53], off nt
	v_pk_fma_f32 v[42:43], v[42:43], s[38:39], v[10:11] op_sel_hi:[1,0,1]
	v_pk_fma_f32 v[48:49], v[48:49], s[38:39], v[16:17] op_sel_hi:[1,0,1]
	v_lshl_add_u64 v[50:51], s[70:71], 0, v[184:185]
	v_lshl_add_u64 v[50:51], v[50:51], 0, v[180:181]
	s_waitcnt lgkmcnt(0)
	global_store_dwordx4 v[50:51], v[54:57], off nt
	v_mov_b32_e32 v51, v175
	v_mov_b32_e32 v50, v175
	v_mov_b32_e32 v53, v175
	v_mov_b32_e32 v52, v175
	v_cvt_pk_fp8_f32 v51, v90, v91
	v_cvt_pk_fp8_f32 v50, v84, v85
	v_cvt_pk_fp8_f32 v53, v82, v83
	v_cvt_pk_fp8_f32 v52, v62, v63
	v_cvt_pk_fp8_f32 v51, v92, v93 op_sel:[0,0,1]
	v_cvt_pk_fp8_f32 v50, v88, v89 op_sel:[0,0,1]
	v_cvt_pk_fp8_f32 v53, v86, v87 op_sel:[0,0,1]
	v_cvt_pk_fp8_f32 v52, v64, v65 op_sel:[0,0,1]
	v_or_b32_e32 v54, s68, v195
	s_or_b32 s68, s72, 0xb0
	s_add_i32 s70, s10, s68
	ds_write2_b64 v194, v[52:53], v[50:51] offset1:4
	v_add_u32_e32 v54, s10, v54
	s_ashr_i32 s71, s70, 31
	ds_read_b128 v[50:53], v196
	v_ashrrev_i32_e32 v55, 31, v54
	s_lshl_b64 s[70:71], s[70:71], 11
	v_lshlrev_b64 v[54:55], 10, v[54:55]
	s_add_u32 s69, s54, s70
	v_lshl_add_u64 v[54:55], s[16:17], 0, v[54:55]
	s_addc_u32 s71, s55, s71
	v_lshl_add_u64 v[54:55], v[54:55], 0, s[74:75]
	s_add_u32 s70, s69, s76
	v_lshl_add_u64 v[54:55], v[54:55], 0, v[190:191]
	s_addc_u32 s71, s71, s77
	s_waitcnt lgkmcnt(0)
	global_store_dwordx4 v[54:55], v[50:53], off nt
	v_lshl_add_u64 v[54:55], s[70:71], 0, v[182:183]
	v_lshl_add_u64 v[54:55], v[54:55], 0, v[180:181]
	v_lshl_add_u64 v[58:59], s[70:71], 0, v[184:185]
	global_load_dwordx4 v[54:57], v[54:55], off
	v_lshl_add_u64 v[58:59], v[58:59], 0, v[180:181]
	global_load_dwordx4 v[50:53], v[192:193], off offset:3072
	v_pk_mul_f32 v[42:43], v[42:43], s[40:41] op_sel_hi:[1,0]
	global_load_dwordx4 v[58:61], v[58:59], off
	v_exp_f32_e32 v42, v42
	v_exp_f32_e32 v43, v43
	v_pk_fma_f32 v[34:35], v[34:35], s[38:39], v[2:3] op_sel_hi:[1,0,1]
	v_pk_fma_f32 v[46:47], v[46:47], s[38:39], v[14:15] op_sel_hi:[1,0,1]
	v_pk_mul_f32 v[34:35], v[34:35], s[40:41] op_sel_hi:[1,0]
	v_pk_add_f32 v[42:43], v[42:43], 1.0 op_sel_hi:[1,0]
	v_pk_mul_f32 v[46:47], v[46:47], s[40:41] op_sel_hi:[1,0]
	v_rcp_f32_e32 v214, v42
	v_rcp_f32_e32 v215, v43
	v_pk_mul_f32 v[42:43], v[48:49], s[40:41] op_sel_hi:[1,0]
	v_exp_f32_e32 v34, v34
	v_exp_f32_e32 v42, v42
	v_exp_f32_e32 v43, v43
	v_exp_f32_e32 v35, v35
	s_waitcnt vmcnt(8)
	v_cvt_pk_f32_fp8_e32 v[200:201], v66
	v_cvt_pk_f32_fp8_e32 v[212:213], v67
	v_exp_f32_e32 v46, v46
	v_exp_f32_e32 v47, v47
	v_pk_fma_f32 v[44:45], v[44:45], s[38:39], v[12:13] op_sel_hi:[1,0,1]
	s_waitcnt vmcnt(7)
	ds_write_b128 v207, v[70:73]
	s_waitcnt vmcnt(6)
	ds_write_b128 v207, v[74:77] offset:1152
	v_pk_mul_f32 v[44:45], v[44:45], s[40:41] op_sel_hi:[1,0]
	v_pk_add_f32 v[42:43], v[42:43], 1.0 op_sel_hi:[1,0]
	v_pk_fma_f32 v[40:41], v[40:41], s[38:39], v[8:9] op_sel_hi:[1,0,1]
	v_pk_fma_f32 v[38:39], v[38:39], s[38:39], v[6:7] op_sel_hi:[1,0,1]
	v_pk_fma_f32 v[36:37], v[36:37], s[38:39], v[4:5] op_sel_hi:[1,0,1]
	v_pk_add_f32 v[34:35], v[34:35], 1.0 op_sel_hi:[1,0]
	ds_read_b128 v[70:73], v208
	ds_read_b128 v[74:77], v208 offset:64
	v_pk_add_f32 v[46:47], v[46:47], 1.0 op_sel_hi:[1,0]
	v_exp_f32_e32 v44, v44
	v_exp_f32_e32 v45, v45
	v_rcp_f32_e32 v48, v42
	v_rcp_f32_e32 v49, v43
	v_pk_mul_f32 v[42:43], v[200:201], s[42:43] op_sel_hi:[1,0]
	v_pk_mul_f32 v[200:201], v[212:213], s[42:43] op_sel_hi:[1,0]
	v_pk_mul_f32 v[38:39], v[38:39], s[40:41] op_sel_hi:[1,0]
	v_rcp_f32_e32 v212, v34
	v_rcp_f32_e32 v213, v35
	v_pk_mul_f32 v[34:35], v[40:41], s[40:41] op_sel_hi:[1,0]
	v_pk_mul_f32 v[36:37], v[36:37], s[40:41] op_sel_hi:[1,0]
	v_cvt_pk_f32_fp8_sdwa v[210:211], v66 src0_sel:WORD_1
	v_rcp_f32_e32 v46, v46
	v_rcp_f32_e32 v47, v47
	v_exp_f32_e32 v38, v38
	v_exp_f32_e32 v39, v39
	v_exp_f32_e32 v34, v34
	v_exp_f32_e32 v35, v35
	v_exp_f32_e32 v36, v36
	v_exp_f32_e32 v37, v37
	s_waitcnt lgkmcnt(1)
	v_lshlrev_b32_e32 v192, 16, v70
	v_and_b32_e32 v193, 0xffff0000, v70
	v_lshlrev_b32_e32 v198, 16, v72
	v_and_b32_e32 v199, 0xffff0000, v72
	v_cvt_pk_f32_fp8_sdwa v[66:67], v67 src0_sel:WORD_1
	v_pk_add_f32 v[44:45], v[44:45], 1.0 op_sel_hi:[1,0]
	v_pk_fma_f32 v[42:43], v[46:47], v[42:43], v[192:193]
	v_rcp_f32_e32 v216, v44
	v_rcp_f32_e32 v217, v45
	v_pk_mul_f32 v[44:45], v[210:211], s[42:43] op_sel_hi:[1,0]
	v_pk_fma_f32 v[46:47], v[214:215], v[200:201], v[198:199]
	v_cvt_pk_f32_fp8_e32 v[198:199], v68
	v_cvt_pk_f32_fp8_sdwa v[200:201], v68 src0_sel:WORD_1
	v_cvt_pk_f32_fp8_e32 v[210:211], v69
	v_cvt_pk_f32_fp8_sdwa v[68:69], v69 src0_sel:WORD_1
	v_pk_add_f32 v[38:39], v[38:39], 1.0 op_sel_hi:[1,0]
	v_pk_add_f32 v[34:35], v[34:35], 1.0 op_sel_hi:[1,0]
	v_pk_add_f32 v[36:37], v[36:37], 1.0 op_sel_hi:[1,0]
	v_rcp_f32_e32 v38, v38
	v_rcp_f32_e32 v39, v39
	v_rcp_f32_e32 v40, v34
	v_rcp_f32_e32 v41, v35
	v_rcp_f32_e32 v214, v36
	v_rcp_f32_e32 v215, v37
	s_or_b32 s70, s78, 32
	s_ashr_i32 s71, s70, 31
	v_lshlrev_b32_e32 v70, 16, v71
	v_and_b32_e32 v71, 0xffff0000, v71
	v_lshlrev_b32_e32 v72, 16, v73
	v_and_b32_e32 v73, 0xffff0000, v73
	v_pk_mul_f32 v[66:67], v[66:67], s[42:43] op_sel_hi:[1,0]
	s_lshl_b64 s[70:71], s[70:71], 11
	v_pk_fma_f32 v[44:45], v[48:49], v[44:45], v[70:71]
	v_pk_fma_f32 v[48:49], v[216:217], v[66:67], v[72:73]
	v_cvt_pk_bf16_f32 v70, v42, v43
	v_cvt_pk_bf16_f32 v71, v44, v45
	v_cvt_pk_bf16_f32 v72, v46, v47
	s_waitcnt lgkmcnt(0)
	v_lshlrev_b32_e32 v66, 16, v74
	v_cvt_pk_bf16_f32 v73, v48, v49
	v_and_b32_e32 v67, 0xffff0000, v74
	v_lshlrev_b32_e32 v74, 16, v75
	v_and_b32_e32 v75, 0xffff0000, v75
	v_lshlrev_b32_e32 v192, 16, v76
	v_and_b32_e32 v193, 0xffff0000, v76
	v_lshlrev_b32_e32 v76, 16, v77
	v_and_b32_e32 v77, 0xffff0000, v77
	v_pk_mul_f32 v[36:37], v[200:201], s[42:43] op_sel_hi:[1,0]
	v_pk_mul_f32 v[34:35], v[198:199], s[42:43] op_sel_hi:[1,0]
	v_pk_mul_f32 v[68:69], v[68:69], s[42:43] op_sel_hi:[1,0]
	v_pk_mul_f32 v[198:199], v[210:211], s[42:43] op_sel_hi:[1,0]
	s_add_u32 s69, s56, s70
	v_pk_fma_f32 v[34:35], v[38:39], v[34:35], v[66:67]
	v_pk_fma_f32 v[36:37], v[40:41], v[36:37], v[74:75]
	v_pk_fma_f32 v[38:39], v[212:213], v[198:199], v[192:193]
	v_pk_fma_f32 v[40:41], v[214:215], v[68:69], v[76:77]
	v_cvt_pk_bf16_f32 v66, v34, v35
	v_cvt_pk_bf16_f32 v67, v36, v37
	v_cvt_pk_bf16_f32 v68, v38, v39
	s_addc_u32 s71, s57, s71
	v_cvt_pk_bf16_f32 v69, v40, v41
	ds_write_b128 v208, v[70:73]
	ds_write_b128 v208, v[66:69] offset:64
	s_add_u32 s70, s69, s76
	ds_read_b128 v[66:69], v207
	ds_read_b128 v[70:73], v207 offset:1152
	s_addc_u32 s71, s71, s77
	v_lshl_add_u64 v[74:75], s[70:71], 0, v[182:183]
	v_lshl_add_u64 v[74:75], v[74:75], 0, v[180:181]
	s_waitcnt lgkmcnt(1)
	global_store_dwordx4 v[74:75], v[66:69], off nt
	v_pk_fma_f32 v[10:11], v[26:27], s[38:39], v[10:11] op_sel_hi:[1,0,1]
	v_pk_fma_f32 v[16:17], v[32:33], s[38:39], v[16:17] op_sel_hi:[1,0,1]
	v_lshl_add_u64 v[66:67], s[70:71], 0, v[184:185]
	v_lshl_add_u64 v[66:67], v[66:67], 0, v[180:181]
	s_waitcnt lgkmcnt(0)
	global_store_dwordx4 v[66:67], v[70:73], off nt
	v_mov_b32_e32 v67, v175
	v_mov_b32_e32 v66, v175
	v_mov_b32_e32 v69, v175
	v_mov_b32_e32 v68, v175
	v_cvt_pk_fp8_f32 v67, v38, v39
	v_cvt_pk_fp8_f32 v66, v34, v35
	v_cvt_pk_fp8_f32 v69, v46, v47
	v_cvt_pk_fp8_f32 v68, v42, v43
	v_cvt_pk_fp8_f32 v67, v40, v41 op_sel:[0,0,1]
	v_cvt_pk_fp8_f32 v66, v36, v37 op_sel:[0,0,1]
	v_cvt_pk_fp8_f32 v69, v48, v49 op_sel:[0,0,1]
	v_cvt_pk_fp8_f32 v68, v44, v45 op_sel:[0,0,1]
	v_pk_mul_f32 v[10:11], v[10:11], s[40:41] op_sel_hi:[1,0]
	v_or_b32_e32 v70, s47, v195
	v_exp_f32_e32 v10, v10
	v_exp_f32_e32 v11, v11
	ds_write2_b64 v194, v[68:69], v[66:67] offset1:4
	v_add_u32_e32 v70, s10, v70
	ds_read_b128 v[66:69], v196
	v_ashrrev_i32_e32 v71, 31, v70
	v_lshlrev_b64 v[70:71], 10, v[70:71]
	v_pk_fma_f32 v[14:15], v[30:31], s[38:39], v[14:15] op_sel_hi:[1,0,1]
	v_pk_fma_f32 v[12:13], v[28:29], s[38:39], v[12:13] op_sel_hi:[1,0,1]
	v_pk_add_f32 v[10:11], v[10:11], 1.0 op_sel_hi:[1,0]
	v_lshl_add_u64 v[70:71], s[16:17], 0, v[70:71]
	v_pk_mul_f32 v[14:15], v[14:15], s[40:41] op_sel_hi:[1,0]
	v_rcp_f32_e32 v26, v10
	v_rcp_f32_e32 v27, v11
	v_pk_mul_f32 v[10:11], v[16:17], s[40:41] op_sel_hi:[1,0]
	v_pk_mul_f32 v[12:13], v[12:13], s[40:41] op_sel_hi:[1,0]
	v_lshl_add_u64 v[70:71], v[70:71], 0, s[74:75]
	v_exp_f32_e32 v14, v14
	v_exp_f32_e32 v15, v15
	v_exp_f32_e32 v10, v10
	v_exp_f32_e32 v11, v11
	v_exp_f32_e32 v12, v12
	v_exp_f32_e32 v13, v13
	v_lshl_add_u64 v[70:71], v[70:71], 0, v[190:191]
	s_waitcnt lgkmcnt(0)
	global_store_dwordx4 v[70:71], v[66:69], off nt
	s_waitcnt vmcnt(5)
	ds_write_b128 v207, v[54:57]
	s_waitcnt vmcnt(3)
	ds_write_b128 v207, v[58:61] offset:1152
	v_pk_fma_f32 v[8:9], v[24:25], s[38:39], v[8:9] op_sel_hi:[1,0,1]
	v_pk_fma_f32 v[6:7], v[22:23], s[38:39], v[6:7] op_sel_hi:[1,0,1]
	v_pk_fma_f32 v[4:5], v[20:21], s[38:39], v[4:5] op_sel_hi:[1,0,1]
	v_pk_fma_f32 v[2:3], v[18:19], s[38:39], v[2:3] op_sel_hi:[1,0,1]
	ds_read_b128 v[54:57], v208
	ds_read_b128 v[58:61], v208 offset:64
	v_cvt_pk_f32_fp8_e32 v[70:71], v50
	v_cvt_pk_f32_fp8_sdwa v[72:73], v50 src0_sel:WORD_1
	v_cvt_pk_f32_fp8_e32 v[74:75], v51
	v_cvt_pk_f32_fp8_sdwa v[50:51], v51 src0_sel:WORD_1
	v_pk_add_f32 v[14:15], v[14:15], 1.0 op_sel_hi:[1,0]
	v_pk_add_f32 v[10:11], v[10:11], 1.0 op_sel_hi:[1,0]
	v_pk_add_f32 v[12:13], v[12:13], 1.0 op_sel_hi:[1,0]
	v_pk_mul_f32 v[6:7], v[6:7], s[40:41] op_sel_hi:[1,0]
	v_pk_mul_f32 v[2:3], v[2:3], s[40:41] op_sel_hi:[1,0]
	v_pk_mul_f32 v[8:9], v[8:9], s[40:41] op_sel_hi:[1,0]
	v_pk_mul_f32 v[4:5], v[4:5], s[40:41] op_sel_hi:[1,0]
	v_rcp_f32_e32 v14, v14
	v_rcp_f32_e32 v15, v15
	v_rcp_f32_e32 v16, v10
	v_rcp_f32_e32 v17, v11
	v_rcp_f32_e32 v28, v12
	v_rcp_f32_e32 v29, v13
	v_exp_f32_e32 v6, v6
	v_exp_f32_e32 v7, v7
	v_exp_f32_e32 v2, v2
	v_exp_f32_e32 v3, v3
	v_exp_f32_e32 v8, v8
	v_exp_f32_e32 v9, v9
	v_exp_f32_e32 v4, v4
	v_exp_f32_e32 v5, v5
	s_waitcnt lgkmcnt(1)
	v_lshlrev_b32_e32 v66, 16, v54
	v_and_b32_e32 v67, 0xffff0000, v54
	v_lshlrev_b32_e32 v54, 16, v55
	v_and_b32_e32 v55, 0xffff0000, v55
	v_lshlrev_b32_e32 v68, 16, v56
	v_and_b32_e32 v69, 0xffff0000, v56
	v_lshlrev_b32_e32 v56, 16, v57
	v_and_b32_e32 v57, 0xffff0000, v57
	v_pk_mul_f32 v[12:13], v[72:73], s[42:43] op_sel_hi:[1,0]
	v_pk_mul_f32 v[10:11], v[70:71], s[42:43] op_sel_hi:[1,0]
	v_pk_mul_f32 v[30:31], v[50:51], s[42:43] op_sel_hi:[1,0]
	v_pk_mul_f32 v[32:33], v[74:75], s[42:43] op_sel_hi:[1,0]
	v_pk_fma_f32 v[10:11], v[14:15], v[10:11], v[66:67]
	v_pk_fma_f32 v[12:13], v[16:17], v[12:13], v[54:55]
	v_pk_fma_f32 v[14:15], v[26:27], v[32:33], v[68:69]
	v_pk_fma_f32 v[16:17], v[28:29], v[30:31], v[56:57]
	s_waitcnt lgkmcnt(0)
	v_lshlrev_b32_e32 v30, 16, v58
	v_and_b32_e32 v31, 0xffff0000, v58
	v_lshlrev_b32_e32 v32, 16, v59
	v_and_b32_e32 v33, 0xffff0000, v59
	v_lshlrev_b32_e32 v50, 16, v60
	v_and_b32_e32 v51, 0xffff0000, v60
	v_lshlrev_b32_e32 v54, 16, v61
	v_and_b32_e32 v55, 0xffff0000, v61
	v_cvt_pk_f32_fp8_e32 v[56:57], v52
	v_cvt_pk_f32_fp8_sdwa v[58:59], v52 src0_sel:WORD_1
	v_cvt_pk_f32_fp8_e32 v[60:61], v53
	v_cvt_pk_f32_fp8_sdwa v[52:53], v53 src0_sel:WORD_1
	v_pk_add_f32 v[6:7], v[6:7], 1.0 op_sel_hi:[1,0]
	v_pk_add_f32 v[2:3], v[2:3], 1.0 op_sel_hi:[1,0]
	v_pk_add_f32 v[8:9], v[8:9], 1.0 op_sel_hi:[1,0]
	v_pk_add_f32 v[4:5], v[4:5], 1.0 op_sel_hi:[1,0]
	v_rcp_f32_e32 v6, v6
	v_rcp_f32_e32 v7, v7
	v_rcp_f32_e32 v2, v2
	v_rcp_f32_e32 v3, v3
	v_rcp_f32_e32 v8, v8
	v_rcp_f32_e32 v9, v9
	v_rcp_f32_e32 v4, v4
	v_rcp_f32_e32 v5, v5
	s_or_b32 s70, s78, 48
	s_ashr_i32 s71, s70, 31
	s_lshl_b64 s[70:71], s[70:71], 11
	v_cvt_pk_bf16_f32 v26, v10, v11
	v_cvt_pk_bf16_f32 v27, v12, v13
	v_cvt_pk_bf16_f32 v28, v14, v15
	v_cvt_pk_bf16_f32 v29, v16, v17
	v_pk_mul_f32 v[18:19], v[58:59], s[42:43] op_sel_hi:[1,0]
	v_pk_mul_f32 v[20:21], v[56:57], s[42:43] op_sel_hi:[1,0]
	v_pk_mul_f32 v[22:23], v[52:53], s[42:43] op_sel_hi:[1,0]
	v_pk_mul_f32 v[24:25], v[60:61], s[42:43] op_sel_hi:[1,0]
	s_add_u32 s47, s56, s70
	v_pk_fma_f32 v[20:21], v[6:7], v[20:21], v[30:31]
	v_pk_fma_f32 v[18:19], v[8:9], v[18:19], v[32:33]
	v_pk_fma_f32 v[24:25], v[2:3], v[24:25], v[50:51]
	v_pk_fma_f32 v[22:23], v[4:5], v[22:23], v[54:55]
	v_cvt_pk_bf16_f32 v2, v20, v21
	v_cvt_pk_bf16_f32 v3, v18, v19
	v_cvt_pk_bf16_f32 v4, v24, v25
	s_addc_u32 s69, s57, s71
	v_cvt_pk_bf16_f32 v5, v22, v23
	ds_write_b128 v208, v[26:29]
	ds_write_b128 v208, v[2:5] offset:64
	s_add_u32 s70, s47, s76
	ds_read_b128 v[2:5], v207
	ds_read_b128 v[6:9], v207 offset:1152
	s_addc_u32 s71, s69, s77
	v_lshl_add_u64 v[26:27], s[70:71], 0, v[182:183]
	v_lshl_add_u64 v[26:27], v[26:27], 0, v[180:181]
	s_waitcnt lgkmcnt(1)
	global_store_dwordx4 v[26:27], v[2:5], off nt
	s_lshl_b32 s47, s64, 2
	s_ashr_i32 s73, s72, 31
	v_lshl_add_u64 v[2:3], s[70:71], 0, v[184:185]
	v_lshl_add_u64 v[2:3], v[2:3], 0, v[180:181]
	s_waitcnt lgkmcnt(0)
	global_store_dwordx4 v[2:3], v[6:9], off nt
	v_mov_b32_e32 v3, v175
	v_mov_b32_e32 v2, v175
	v_mov_b32_e32 v5, v175
	v_mov_b32_e32 v4, v175
	v_cvt_pk_fp8_f32 v3, v24, v25
	v_cvt_pk_fp8_f32 v2, v20, v21
	v_cvt_pk_fp8_f32 v5, v14, v15
	v_cvt_pk_fp8_f32 v4, v10, v11
	v_cvt_pk_fp8_f32 v3, v22, v23 op_sel:[0,0,1]
	v_cvt_pk_fp8_f32 v2, v18, v19 op_sel:[0,0,1]
	v_cvt_pk_fp8_f32 v5, v16, v17 op_sel:[0,0,1]
	v_cvt_pk_fp8_f32 v4, v12, v13 op_sel:[0,0,1]
	v_or_b32_e32 v6, s68, v195
	v_add_u32_e32 v6, s10, v6
	v_ashrrev_i32_e32 v7, 31, v6
	ds_write2_b64 v194, v[4:5], v[2:3] offset1:4
	ds_read_b128 v[2:5], v196
	v_lshlrev_b64 v[6:7], 10, v[6:7]
	v_lshl_add_u64 v[6:7], s[16:17], 0, v[6:7]
	v_lshl_add_u64 v[6:7], v[6:7], 0, s[74:75]
	v_lshl_add_u64 v[6:7], v[6:7], 0, v[190:191]
	s_waitcnt lgkmcnt(0)
	global_store_dwordx4 v[6:7], v[2:5], off nt
	v_mul_f32_e32 v6, v37, v37
	v_fmac_f32_e32 v6, v36, v36
	v_mul_f32_e32 v2, v15, v15
	v_mul_f32_e32 v3, v17, v17
	v_fmac_f32_e32 v2, v14, v14
	v_fmac_f32_e32 v3, v16, v16
	v_add_f32_e32 v2, v2, v3
	v_mul_f32_e32 v3, v11, v11
	v_mul_f32_e32 v4, v13, v13
	v_fmac_f32_e32 v3, v10, v10
	v_fmac_f32_e32 v4, v12, v12
	v_add_f32_e32 v3, v3, v4
	v_add_f32_e32 v2, v3, v2
	v_mul_f32_e32 v3, v25, v25
	v_mul_f32_e32 v4, v23, v23
	v_fmac_f32_e32 v3, v24, v24
	v_fmac_f32_e32 v4, v22, v22
	v_add_f32_e32 v3, v3, v4
	v_mul_f32_e32 v4, v21, v21
	v_mul_f32_e32 v5, v19, v19
	v_fmac_f32_e32 v4, v20, v20
	v_fmac_f32_e32 v5, v18, v18
	v_add_f32_e32 v4, v4, v5
	v_add_f32_e32 v3, v4, v3
	v_add_f32_e32 v2, v2, v3
	v_mul_f32_e32 v3, v47, v47
	v_mul_f32_e32 v4, v49, v49
	v_fmac_f32_e32 v3, v46, v46
	v_fmac_f32_e32 v4, v48, v48
	v_add_f32_e32 v3, v3, v4
	v_mul_f32_e32 v4, v43, v43
	v_mul_f32_e32 v5, v45, v45
	v_fmac_f32_e32 v4, v42, v42
	v_fmac_f32_e32 v5, v44, v44
	v_add_f32_e32 v4, v4, v5
	v_add_f32_e32 v3, v4, v3
	v_mul_f32_e32 v4, v39, v39
	v_mul_f32_e32 v5, v41, v41
	v_fmac_f32_e32 v4, v38, v38
	v_fmac_f32_e32 v5, v40, v40
	v_add_f32_e32 v4, v4, v5
	v_mul_f32_e32 v5, v35, v35
	v_fmac_f32_e32 v5, v34, v34
	v_add_f32_e32 v5, v5, v6
	v_add_f32_e32 v4, v5, v4
	v_add_f32_e32 v3, v3, v4
	v_mul_f32_e32 v4, v83, v83
	v_mul_f32_e32 v5, v87, v87
	v_fmac_f32_e32 v4, v82, v82
	v_fmac_f32_e32 v5, v86, v86
	v_add_f32_e32 v4, v4, v5
	v_mul_f32_e32 v5, v63, v63
	v_mul_f32_e32 v6, v65, v65
	v_fmac_f32_e32 v5, v62, v62
	v_fmac_f32_e32 v6, v64, v64
	v_add_f32_e32 v5, v5, v6
	v_add_f32_e32 v4, v5, v4
	v_mul_f32_e32 v5, v91, v91
	v_mul_f32_e32 v6, v93, v93
	v_fmac_f32_e32 v5, v90, v90
	v_fmac_f32_e32 v6, v92, v92
	v_add_f32_e32 v5, v5, v6
	v_mul_f32_e32 v6, v85, v85
	v_mul_f32_e32 v7, v89, v89
	v_fmac_f32_e32 v6, v84, v84
	v_fmac_f32_e32 v7, v88, v88
	v_add_f32_e32 v6, v6, v7
	v_add_f32_e32 v5, v6, v5
	v_add_f32_e32 v4, v4, v5
	v_mul_f32_e32 v5, v99, v99
	v_mul_f32_e32 v6, v103, v103
	v_fmac_f32_e32 v5, v98, v98
	v_fmac_f32_e32 v6, v102, v102
	v_add_f32_e32 v5, v5, v6
	v_mul_f32_e32 v6, v79, v79
	v_mul_f32_e32 v7, v81, v81
	v_fmac_f32_e32 v6, v78, v78
	v_fmac_f32_e32 v7, v80, v80
	v_add_f32_e32 v6, v6, v7
	v_add_f32_e32 v5, v6, v5
	v_mul_f32_e32 v6, v107, v107
	v_mul_f32_e32 v7, v109, v109
	v_fmac_f32_e32 v6, v106, v106
	v_fmac_f32_e32 v7, v108, v108
	v_add_f32_e32 v6, v6, v7
	v_mul_f32_e32 v7, v101, v101
	v_mul_f32_e32 v8, v105, v105
	v_fmac_f32_e32 v7, v100, v100
	v_fmac_f32_e32 v8, v104, v104
	v_add_f32_e32 v7, v7, v8
	v_add_f32_e32 v6, v7, v6
	v_add_f32_e32 v5, v5, v6
	v_mul_f32_e32 v6, v119, v119
	v_mul_f32_e32 v7, v115, v115
	v_fmac_f32_e32 v6, v118, v118
	v_fmac_f32_e32 v7, v114, v114
	v_add_f32_e32 v6, v6, v7
	v_mul_f32_e32 v7, v97, v97
	v_mul_f32_e32 v8, v95, v95
	v_fmac_f32_e32 v7, v96, v96
	v_fmac_f32_e32 v8, v94, v94
	v_add_f32_e32 v7, v7, v8
	v_add_f32_e32 v6, v7, v6
	v_mul_f32_e32 v7, v125, v125
	v_mul_f32_e32 v8, v123, v123
	v_fmac_f32_e32 v7, v124, v124
	v_fmac_f32_e32 v8, v122, v122
	v_add_f32_e32 v7, v7, v8
	v_mul_f32_e32 v8, v121, v121
	v_mul_f32_e32 v9, v117, v117
	v_fmac_f32_e32 v8, v120, v120
	v_fmac_f32_e32 v9, v116, v116
	v_add_f32_e32 v8, v8, v9
	v_add_f32_e32 v7, v8, v7
	v_add_f32_e32 v6, v6, v7
	v_mul_f32_e32 v7, v135, v135
	v_mul_f32_e32 v8, v131, v131
	v_fmac_f32_e32 v7, v134, v134
	v_fmac_f32_e32 v8, v130, v130
	v_add_f32_e32 v7, v7, v8
	v_mul_f32_e32 v8, v113, v113
	v_mul_f32_e32 v9, v111, v111
	v_fmac_f32_e32 v8, v112, v112
	v_fmac_f32_e32 v9, v110, v110
	v_add_f32_e32 v8, v8, v9
	v_add_f32_e32 v7, v8, v7
	v_mul_f32_e32 v8, v141, v141
	v_mul_f32_e32 v9, v139, v139
	v_fmac_f32_e32 v8, v140, v140
	v_fmac_f32_e32 v9, v138, v138
	v_add_f32_e32 v8, v8, v9
	v_mul_f32_e32 v9, v137, v137
	v_mul_f32_e32 v10, v133, v133
	v_fmac_f32_e32 v9, v136, v136
	v_fmac_f32_e32 v10, v132, v132
	v_add_f32_e32 v9, v9, v10
	v_add_f32_e32 v8, v9, v8
	v_add_f32_e32 v7, v7, v8
	v_mul_f32_e32 v8, v151, v151
	v_mul_f32_e32 v9, v147, v147
	v_fmac_f32_e32 v8, v150, v150
	v_fmac_f32_e32 v9, v146, v146
	v_add_f32_e32 v8, v8, v9
	v_mul_f32_e32 v9, v129, v129
	v_mul_f32_e32 v10, v127, v127
	v_fmac_f32_e32 v9, v128, v128
	v_fmac_f32_e32 v10, v126, v126
	v_add_f32_e32 v9, v9, v10
	v_add_f32_e32 v8, v9, v8
	v_mul_f32_e32 v9, v157, v157
	v_mul_f32_e32 v10, v155, v155
	v_fmac_f32_e32 v9, v156, v156
	v_fmac_f32_e32 v10, v154, v154
	v_add_f32_e32 v9, v9, v10
	v_mul_f32_e32 v10, v153, v153
	v_mul_f32_e32 v11, v149, v149
	v_fmac_f32_e32 v10, v152, v152
	v_fmac_f32_e32 v11, v148, v148
	v_add_f32_e32 v10, v10, v11
	v_add_f32_e32 v9, v10, v9
	v_add_f32_e32 v8, v8, v9
	v_mul_f32_e32 v9, v187, v187
	v_mul_f32_e32 v10, v159, v159
	v_fmac_f32_e32 v9, v186, v186
	v_fmac_f32_e32 v10, v158, v158
	v_add_f32_e32 v9, v9, v10
	v_mul_f32_e32 v10, v145, v145
	v_mul_f32_e32 v11, v143, v143
	v_fmac_f32_e32 v10, v144, v144
	v_fmac_f32_e32 v11, v142, v142
	v_add_f32_e32 v10, v10, v11
	v_add_f32_e32 v9, v10, v9
	v_mul_f32_e32 v10, v189, v189
	v_mul_f32_e32 v11, v165, v165
	v_fmac_f32_e32 v10, v188, v188
	v_fmac_f32_e32 v11, v164, v164
	v_add_f32_e32 v10, v10, v11
	v_mul_f32_e32 v11, v163, v163
	v_mul_f32_e32 v12, v161, v161
	v_fmac_f32_e32 v11, v162, v162
	v_fmac_f32_e32 v12, v160, v160
	v_add_f32_e32 v11, v11, v12
	v_add_f32_e32 v10, v11, v10
	v_add_f32_e32 v9, v9, v10
	v_lshlrev_b32_e32 v10, 2, v206
	v_lshlrev_b32_e32 v11, 4, v205
	s_or_b32 s68, s45, s47
	v_add3_u32 v10, s11, v10, v11
	ds_write2st64_b32 v10, v9, v8 offset1:1
	ds_write2st64_b32 v10, v7, v6 offset0:2 offset1:3
	ds_write2st64_b32 v10, v5, v4 offset0:4 offset1:5
	ds_write2st64_b32 v10, v3, v2 offset0:6 offset1:7
	v_add_u32_e32 v6, s11, v174
	s_ashr_i32 s69, s68, 31
	s_ashr_i32 s11, s10, 31
	s_lshl_b64 s[68:69], s[68:69], 18
	ds_read_b128 v[2:5], v6
	s_add_u32 s45, s58, s68
	s_addc_u32 s47, s59, s69
	s_lshl_b64 s[68:69], s[72:73], 2
	s_add_u32 s45, s45, s68
	s_addc_u32 s47, s47, s69
	s_lshl_b64 s[10:11], s[10:11], 2
	s_add_u32 s10, s45, s10
	s_waitcnt lgkmcnt(0)
	v_add_f32_e32 v2, v2, v3
	v_add_f32_e32 v3, v4, v5
	s_addc_u32 s11, s47, s11
	v_lshlrev_b32_e32 v7, 2, v204
	v_add_f32_e32 v2, v2, v3
	global_store_dword v7, v2, s[10:11]
	ds_read_b128 v[2:5], v6 offset:1024
	s_and_b64 vcc, exec, s[8:9]
	s_waitcnt lgkmcnt(0)
	v_add_f32_e32 v2, v2, v3
	v_add_f32_e32 v3, v4, v5
	v_add_f32_e32 v2, v2, v3
	global_store_dword v7, v2, s[10:11] offset:512
	s_mov_b64 s[10:11], -1
	s_cbranch_vccnz .LBB0_1769
	v_mov_b32_e32 v2, v0
	s_nop 0
	v_readfirstlane_b32 s8, v2
	s_and_b32 s10, s8, 0xc0
	s_lshl_b32 s8, s44, 8
	s_ashr_i32 s9, s8, 31
	s_lshl_b64 s[8:9], s[8:9], 2
	s_add_u32 s8, s12, s8
	s_addc_u32 s9, s13, s9
	s_lshl_b32 s10, s10, 2
	s_add_u32 s8, s8, s10
	v_lshlrev_b32_e32 v2, 1, v2
	s_addc_u32 s9, s9, 0
	v_and_b32_e32 v6, 0x60, v2
	global_load_dwordx4 v[10:13], v6, s[8:9] offset:16
	global_load_dwordx4 v[14:17], v6, s[8:9]
	global_load_dwordx4 v[2:5], v6, s[8:9] offset:144
	s_nop 0
	global_load_dwordx4 v[6:9], v6, s[8:9] offset:128
	s_andn2_b64 vcc, exec, s[14:15]
	s_cbranch_vccnz .LBB0_1768
	s_barrier
	s_branch .LBB0_1768

.LBB0_2286:
	s_or_b64 exec, exec, s[8:9]
	v_readlane_b32 s0, v254, 6
	s_waitcnt vmcnt(0) lgkmcnt(0)
	v_mov_b32_e32 v1, v0
	v_mov_b32_e32 v2, v0
	v_readlane_b32 s1, v254, 7
	s_barrier
	s_bitcmp1_b32 s2, 3
	s_cbranch_scc0 .Lstag_done_46961
	s_mov_b32 s4, 3
.Lstag_loop_46961:
	s_sleep 127
	s_sub_u32 s4, s4, 1
	s_cmp_lg_u32 s4, 0
	s_cbranch_scc1 .Lstag_loop_46961
.Lstag_done_46961:
	s_and_b64 vcc, exec, s[0:1]
	v_readfirstlane_b32 s18, v2
	s_cbranch_vccz .LBB0_2306
	v_lshlrev_b32_e32 v1, 4, v2
	v_add_u32_e32 v3, 0x2000, v1
	v_ashrrev_i32_e32 v4, 31, v3
	v_lshrrev_b32_e32 v4, 22, v4
	v_add_u32_e32 v4, v3, v4
	v_ashrrev_i32_e32 v4, 10, v4
	v_mul_i32_i24_e32 v5, 0x400, v4
	v_sub_u32_e32 v3, v3, v5
	v_lshrrev_b32_e32 v5, 4, v3
	v_bitop3_b32 v3, v5, v3, 32 bitop3:0x6c
	v_ashrrev_i32_e32 v5, 31, v3
	v_lshrrev_b32_e32 v5, 26, v5
	s_load_dwordx2 s[10:11], s[90:91], 0xc8
	v_add_u32_e32 v5, v3, v5
	v_lshlrev_b32_e32 v7, 3, v4
	v_ashrrev_i32_e32 v6, 6, v5
	v_and_b32_e32 v7, -16, v7
	v_and_b32_e32 v5, 0xc0, v5
	v_add_u32_e32 v7, v6, v7
	v_sub_u32_e32 v3, v3, v5
	v_mov_b32_e32 v5, 1
	v_lshlrev_b32_e32 v8, 1, v7
	v_lshrrev_b32_e32 v9, 2, v7
	v_lshlrev_b32_e32 v4, 5, v4
	v_ashrrev_i16_sdwa v3, v5, sext(v3) dst_sel:DWORD dst_unused:UNUSED_PAD src0_sel:DWORD src1_sel:BYTE_0
	v_and_b32_e32 v8, 0x3fffd8, v8
	v_and_b32_e32 v9, 4, v9
	v_and_b32_e32 v6, 3, v6
	v_and_b32_e32 v4, 32, v4
	v_bfe_i32 v3, v3, 0, 16
	s_waitcnt lgkmcnt(0)
	s_add_u32 s0, s10, 0x4fc00000
	v_or3_b32 v6, v8, v9, v6
	v_add_lshl_u32 v3, v4, v3, 1
	s_addc_u32 s1, s11, 0
	v_lshl_add_u32 v130, v6, 10, v3
	v_lshl_add_u32 v132, v7, 10, v3
	v_bfe_i32 v3, v2, 27, 1
	s_add_u32 s3, s10, 0x1e00000
	v_lshrrev_b32_e32 v3, 22, v3
	s_addc_u32 s4, s11, 0
	s_ashr_i32 s9, s18, 6
	v_add_u32_e32 v3, v1, v3
	v_readlane_b32 s6, v254, 13
	s_ashr_i32 s16, s18, 8
	s_lshl_b32 s5, s9, 10
	v_and_b32_e32 v3, 0xfffffc00, v3
	s_lshl_b32 s12, s64, 7
	v_readlane_b32 s7, v254, 14
	v_sub_u32_e32 v1, v1, v3
	s_mul_i32 s8, s64, 0x81
	s_and_b64 s[6:7], s[6:7], exec
	v_lshrrev_b32_e32 v3, 4, v1
	s_cselect_b32 s6, s8, s12
	v_readlane_b32 s7, v254, 12
	v_bitop3_b32 v1, v3, v1, 32 bitop3:0x6c
	s_add_i32 s6, s6, s7
	v_ashrrev_i32_e32 v3, 31, v1
	s_ashr_i32 s7, s6, 31
	v_lshrrev_b32_e32 v3, 26, v3
	s_lshr_b32 s7, s7, 27
	v_add_u32_e32 v4, v1, v3
	v_ashrrev_i32_e32 v3, 31, v2
	s_add_i32 s7, s6, s7
	v_lshrrev_b32_e32 v7, 26, v3
	s_ashr_i32 s8, s7, 5
	v_add_u32_e32 v7, v2, v7
	s_lshl_b32 s8, s8, 3
	v_ashrrev_i32_e32 v7, 6, v7
	s_sub_i32 s12, 0x100, s8
	v_lshlrev_b32_e32 v8, 3, v7
	s_min_i32 s12, s12, 8
	v_ashrrev_i32_e32 v6, 6, v4
	v_and_b32_e32 v8, -16, v8
	v_and_b32_e32 v4, 0xc0, v4
	s_abs_i32 s13, s12
	v_add_u32_e32 v8, v6, v8
	v_sub_u32_e32 v1, v1, v4
	v_cvt_f32_u32_e32 v4, s13
	v_lshlrev_b32_e32 v9, 1, v8
	v_lshrrev_b32_e32 v10, 2, v8
	v_lshlrev_b32_e32 v7, 5, v7
	v_ashrrev_i16_sdwa v1, v5, sext(v1) dst_sel:DWORD dst_unused:UNUSED_PAD src0_sel:DWORD src1_sel:BYTE_0
	v_and_b32_e32 v9, 0x3fffd8, v9
	v_and_b32_e32 v10, 4, v10
	v_and_b32_e32 v6, 3, v6
	v_and_b32_e32 v7, 32, v7
	v_bfe_i32 v1, v1, 0, 16
	v_or3_b32 v6, v9, v10, v6
	v_add_lshl_u32 v1, v7, v1, 1
	v_lshl_add_u32 v134, v6, 10, v1
	v_lshl_add_u32 v136, v8, 10, v1
	v_rcp_iflag_f32_e32 v1, v4
	s_sub_i32 s15, 0, s13
	s_andn2_b32 s7, s7, 31
	s_sub_i32 s6, s6, s7
	v_mul_f32_e32 v1, 0x4f7ffffe, v1
	v_cvt_u32_f32_e32 v1, v1
	s_abs_i32 s14, s6
	s_xor_b32 s7, s6, s12
	s_ashr_i32 s7, s7, 31
	v_readfirstlane_b32 s17, v1
	s_mul_i32 s15, s15, s17
	s_mul_hi_u32 s15, s17, s15
	s_add_i32 s17, s17, s15
	s_mul_hi_u32 s15, s14, s17
	s_mul_i32 s17, s15, s13
	s_sub_i32 s14, s14, s17
	s_add_i32 s17, s15, 1
	s_sub_i32 s19, s14, s13
	s_cmp_ge_u32 s14, s13
	s_cselect_b32 s15, s17, s15
	s_cselect_b32 s14, s19, s14
	s_add_i32 s17, s15, 1
	s_cmp_ge_u32 s14, s13
	s_cselect_b32 s13, s17, s15
	s_xor_b32 s13, s13, s7
	s_sub_i32 s14, s13, s7
	s_mul_i32 s7, s14, s12
	s_sub_i32 s6, s6, s7
	s_add_i32 s46, s8, s6
	s_ashr_i32 s15, s14, 31
	s_ashr_i32 s47, s46, 31
	s_lshl_b64 s[6:7], s[14:15], 18
	s_add_u32 s70, s3, s6
	s_addc_u32 s71, s4, s7
	s_add_i32 s6, s5, 0
	v_mov_b32_e32 v1, v0
	s_add_i32 m0, s6, 0x10000
	s_lshl_b64 s[12:13], s[46:47], 18
	global_load_lds_dwordx4 v134, s[70:71]
	s_add_i32 m0, s6, 0x12000
	s_add_u32 s20, s70, 0x8000
	global_load_lds_dwordx4 v130, s[70:71]
	s_addc_u32 s21, s71, 0
	s_add_i32 m0, s6, 0x14000
	v_mov_b32_e32 v139, 0
	global_load_lds_dwordx4 v134, s[20:21]
	s_add_i32 m0, s6, 0x16000
	s_add_u32 s48, s0, s12
	s_addc_u32 s49, s1, s13
	s_add_i32 s7, s6, 0x2000
	global_load_lds_dwordx4 v130, s[20:21]
	s_mov_b32 m0, s6
	s_add_u32 s12, s48, 0x20000
	global_load_lds_dwordx4 v136, s[48:49]
	s_mov_b32 m0, s7
	s_addc_u32 s13, s49, 0
	s_add_i32 s15, s6, 0x4000
	global_load_lds_dwordx4 v132, s[48:49]
	s_mov_b32 m0, s15
	s_add_i32 s33, s6, 0x6000
	global_load_lds_dwordx4 v136, s[12:13]
	s_mov_b32 m0, s33
	v_mov_b32_e32 v135, v139
	global_load_lds_dwordx4 v132, s[12:13]
	v_mov_b32_e32 v131, v139
	v_mov_b32_e32 v137, v139
	v_mov_b32_e32 v133, v139
	s_cmp_eq_u32 s16, 1
	s_mov_b32 s8, 0
	v_lshl_add_u64 v[10:11], s[70:71], 0, v[134:135]
	v_lshl_add_u64 v[8:9], s[70:71], 0, v[130:131]
	v_lshl_add_u64 v[4:5], s[48:49], 0, v[136:137]
	s_cselect_b64 s[12:13], -1, 0
	s_cmp_lg_u32 s16, 1
	v_lshl_add_u64 v[6:7], s[48:49], 0, v[132:133]
	s_cbranch_scc1 .LBB0_2289
	s_barrier

.LBB0_2302:
	v_mov_b32_e32 v186, v0
	s_lshl_b32 s46, s46, 8
	v_readfirstlane_b32 s8, v186
	s_ashr_i32 s39, s8, 6
	s_ashr_i32 s8, s8, 2
	s_andn2_b32 s8, s8, 63
	s_mul_i32 s9, s39, 0xb00
	s_and_b32 s39, s39, 3
	s_add_i32 s70, s8, s46
	s_add_i32 s9, s9, 0
	s_lshl_b32 s41, s14, 8
	s_lshl_b32 s47, s39, 6
	s_ashr_i32 s71, s70, 31
	s_add_i32 s9, s9, 0x20000
	s_or_b32 s48, s47, s41
	s_lshl_b64 s[72:73], s[70:71], 11
	s_add_u32 s41, s37, s72
	s_addc_u32 s47, s54, s73
	s_ashr_i32 s49, s48, 31
	s_lshl_b64 s[50:51], s[48:49], 1
	v_and_b32_e32 v164, 63, v186
	s_add_u32 s74, s41, s50
	v_bfe_u32 v156, v186, 3, 3
	s_addc_u32 s75, s47, s51
	v_lshlrev_b32_e32 v138, 11, v156
	v_lshlrev_b32_e32 v165, 4, v164
	v_lshl_add_u64 v[146:147], s[74:75], 0, v[138:139]
	v_and_b32_e32 v144, 0x70, v165
	v_mov_b32_e32 v145, v139
	v_lshl_add_u64 v[148:149], v[146:147], 0, v[144:145]
	v_or_b32_e32 v146, 0x4000, v138
	v_mov_b32_e32 v147, v139
	v_lshl_add_u64 v[150:151], s[74:75], 0, v[146:147]
	v_lshl_add_u64 v[152:153], v[150:151], 0, v[144:145]
	global_load_dwordx4 v[148:151], v[148:149], off
	s_nop 0
	global_load_dwordx4 v[152:155], v[152:153], off
	s_or_b32 s74, s70, 16
	s_ashr_i32 s75, s74, 31
	s_lshl_b64 s[78:79], s[74:75], 11
	s_add_u32 s41, s37, s78
	s_addc_u32 s47, s54, s79
	v_and_b32_e32 v166, 15, v186
	s_add_u32 s76, s41, s50
	v_and_b32_e32 v157, 48, v186
	v_mul_u32_u24_e32 v156, 0x90, v156
	v_mul_u32_u24_e32 v158, 0x90, v166
	s_addc_u32 s77, s47, s51
	v_add3_u32 v168, s9, v156, v144
	v_add3_u32 v169, s9, v158, v157
	v_lshl_add_u64 v[156:157], s[76:77], 0, v[138:139]
	v_lshl_add_u64 v[158:159], s[76:77], 0, v[146:147]
	v_lshl_add_u64 v[156:157], v[156:157], 0, v[144:145]
	v_lshl_add_u64 v[158:159], v[158:159], 0, v[144:145]
	v_mov_b32_e32 v174, v139
	v_mov_b32_e32 v175, v139
	s_add_u32 s41, s55, s72
	s_addc_u32 s47, s56, s73
	s_add_u32 s72, s41, s50
	s_addc_u32 s73, s47, s51
	v_bfe_u32 v167, v186, 4, 2
	s_waitcnt vmcnt(0)
	ds_write_b128 v168, v[148:151]
	ds_write_b128 v168, v[152:155] offset:1152
	ds_read_b128 v[148:151], v169
	global_load_dwordx4 v[152:155], v[156:157], off
	s_nop 0
	global_load_dwordx4 v[156:159], v[158:159], off
	ds_read_b128 v[170:173], v169 offset:64
	s_waitcnt lgkmcnt(0)
	v_lshlrev_b32_e32 v176, 16, v148
	v_and_b32_e32 v177, 0xffff0000, v148
	v_lshlrev_b32_e32 v178, 16, v150
	v_and_b32_e32 v179, 0xffff0000, v150
	v_lshlrev_b32_e32 v180, 16, v151
	v_and_b32_e32 v181, 0xffff0000, v151
	v_pk_fma_f32 v[150:151], v[118:119], s[36:37], v[176:177] op_sel_hi:[1,0,1]
	v_pk_fma_f32 v[122:123], v[122:123], s[36:37], v[178:179] op_sel_hi:[1,0,1]
	v_med3_f32 v176, v150, s69, v163
	v_med3_f32 v178, v151, s69, v163
	v_cvt_pk_fp8_f32 v174, v176, v178
	v_lshlrev_b32_e32 v148, 16, v149
	v_and_b32_e32 v149, 0xffff0000, v149
	v_lshlrev_b32_e32 v182, 16, v170
	v_and_b32_e32 v183, 0xffff0000, v170
	v_lshlrev_b32_e32 v170, 16, v171
	v_and_b32_e32 v171, 0xffff0000, v171
	v_lshlrev_b32_e32 v184, 16, v172
	v_and_b32_e32 v185, 0xffff0000, v172
	v_pk_fma_f32 v[148:149], v[120:121], s[36:37], v[148:149] op_sel_hi:[1,0,1]
	v_pk_fma_f32 v[126:127], v[126:127], s[36:37], v[182:183] op_sel_hi:[1,0,1]
	v_med3_f32 v177, v122, s69, v163
	v_med3_f32 v179, v123, s69, v163
	v_lshlrev_b32_e32 v172, 16, v173
	v_and_b32_e32 v173, 0xffff0000, v173
	v_pk_fma_f32 v[124:125], v[124:125], s[36:37], v[180:181] op_sel_hi:[1,0,1]
	v_pk_fma_f32 v[118:119], v[128:129], s[36:37], v[170:171] op_sel_hi:[1,0,1]
	v_pk_fma_f32 v[128:129], v[114:115], s[36:37], v[184:185] op_sel_hi:[1,0,1]
	v_med3_f32 v180, v148, s69, v163
	v_med3_f32 v182, v149, s69, v163
	v_cvt_pk_fp8_f32 v175, v177, v179
	v_med3_f32 v177, v126, s69, v163
	v_med3_f32 v179, v127, s69, v163
	v_mov_b32_e32 v176, v139
	v_pk_fma_f32 v[120:121], v[116:117], s[36:37], v[172:173] op_sel_hi:[1,0,1]
	v_cvt_pk_bf16_f32 v114, v150, v151
	v_cvt_pk_bf16_f32 v115, v148, v149
	v_cvt_pk_bf16_f32 v116, v122, v123
	v_cvt_pk_bf16_f32 v117, v124, v125
	v_med3_f32 v178, v128, s69, v163
	v_cvt_pk_fp8_f32 v174, v180, v182 op_sel:[0,0,1]
	v_med3_f32 v180, v129, s69, v163
	v_cvt_pk_fp8_f32 v176, v177, v179
	v_mov_b32_e32 v177, v139
	v_cvt_pk_bf16_f32 v170, v126, v127
	v_cvt_pk_bf16_f32 v171, v118, v119
	v_cvt_pk_bf16_f32 v172, v128, v129
	v_cvt_pk_bf16_f32 v173, v120, v121
	v_cvt_pk_fp8_f32 v177, v178, v180
	ds_write_b128 v169, v[114:117]
	ds_write_b128 v169, v[170:173] offset:64
	ds_read_b128 v[114:117], v168
	ds_read_b128 v[170:173], v168 offset:1152
	v_med3_f32 v181, v124, s69, v163
	v_med3_f32 v183, v125, s69, v163
	v_cvt_pk_fp8_f32 v175, v181, v183 op_sel:[0,0,1]
	v_med3_f32 v181, v118, s69, v163
	v_med3_f32 v182, v120, s69, v163
	v_med3_f32 v178, v119, s69, v163
	v_med3_f32 v179, v121, s69, v163
	v_cvt_pk_fp8_f32 v176, v181, v178 op_sel:[0,0,1]
	v_cvt_pk_fp8_f32 v177, v182, v179 op_sel:[0,0,1]
	v_lshl_add_u64 v[178:179], s[72:73], 0, v[138:139]
	v_lshl_add_u64 v[178:179], v[178:179], 0, v[144:145]
	s_waitcnt lgkmcnt(1)
	global_store_dwordx4 v[178:179], v[114:117], off nt
	s_nop 1
	v_lshl_add_u64 v[114:115], s[72:73], 0, v[146:147]
	v_lshl_add_u64 v[114:115], v[114:115], 0, v[144:145]
	s_lshl_b64 s[72:73], s[70:71], 10
	s_waitcnt lgkmcnt(0)
	global_store_dwordx4 v[114:115], v[170:173], off nt
	s_add_u32 s41, s60, s72
	v_mul_u32_u24_e32 v114, 0x50, v166
	v_lshlrev_b32_e32 v115, 3, v167
	s_addc_u32 s47, s61, s73
	v_add3_u32 v170, s9, v114, v115
	v_bfe_u32 v115, v186, 2, 4
	s_add_u32 s72, s41, s48
	v_mul_u32_u24_e32 v116, 0x50, v115
	v_and_b32_e32 v114, 48, v165
	s_addc_u32 s73, s47, s49
	v_add3_u32 v171, s9, v116, v114
	v_lshlrev_b32_e32 v116, 10, v115
	v_mov_b32_e32 v117, v139
	ds_write2_b64 v170, v[174:175], v[176:177] offset1:4
	v_lshl_add_u64 v[176:177], s[72:73], 0, v[116:117]
	s_or_b32 s72, s70, 32
	s_ashr_i32 s73, s72, 31
	ds_read_b128 v[172:175], v171
	s_lshl_b64 s[76:77], s[72:73], 11
	s_add_u32 s41, s37, s76
	s_addc_u32 s47, s54, s77
	v_mov_b32_e32 v115, v139
	s_add_u32 s80, s41, s50
	v_lshl_add_u64 v[176:177], v[176:177], 0, v[114:115]
	s_addc_u32 s81, s47, s51
	s_waitcnt lgkmcnt(0)
	global_store_dwordx4 v[176:177], v[172:175], off nt
	s_waitcnt vmcnt(4)
	ds_write_b128 v168, v[152:155]
	s_waitcnt vmcnt(3)
	ds_write_b128 v168, v[156:159] offset:1152
	v_lshl_add_u64 v[172:173], s[80:81], 0, v[138:139]
	v_lshl_add_u64 v[174:175], s[80:81], 0, v[146:147]
	v_lshl_add_u64 v[172:173], v[172:173], 0, v[144:145]
	v_lshl_add_u64 v[174:175], v[174:175], 0, v[144:145]
	ds_read_b128 v[152:155], v169
	global_load_dwordx4 v[156:159], v[172:173], off
	s_nop 0
	global_load_dwordx4 v[172:175], v[174:175], off
	ds_read_b128 v[176:179], v169 offset:64
	s_add_u32 s41, s55, s78
	s_addc_u32 s47, s56, s79
	s_waitcnt lgkmcnt(1)
	v_lshlrev_b32_e32 v180, 16, v152
	v_and_b32_e32 v181, 0xffff0000, v152
	v_lshlrev_b32_e32 v182, 16, v154
	v_and_b32_e32 v183, 0xffff0000, v154
	v_pk_fma_f32 v[110:111], v[110:111], s[36:37], v[180:181] op_sel_hi:[1,0,1]
	v_pk_fma_f32 v[106:107], v[106:107], s[36:37], v[182:183] op_sel_hi:[1,0,1]
	v_med3_f32 v181, v110, s69, v163
	v_med3_f32 v183, v111, s69, v163
	v_mov_b32_e32 v180, v139
	v_med3_f32 v182, v106, s69, v163
	v_med3_f32 v184, v107, s69, v163
	v_cvt_pk_fp8_f32 v180, v181, v183
	v_mov_b32_e32 v181, v139
	v_cvt_pk_fp8_f32 v181, v182, v184
	v_lshlrev_b32_e32 v152, 16, v153
	v_and_b32_e32 v153, 0xffff0000, v153
	v_lshlrev_b32_e32 v154, 16, v155
	v_and_b32_e32 v155, 0xffff0000, v155
	v_pk_fma_f32 v[112:113], v[112:113], s[36:37], v[152:153] op_sel_hi:[1,0,1]
	v_pk_fma_f32 v[108:109], v[108:109], s[36:37], v[154:155] op_sel_hi:[1,0,1]
	v_med3_f32 v185, v112, s69, v163
	v_med3_f32 v186, v108, s69, v163
	v_med3_f32 v182, v113, s69, v163
	v_med3_f32 v183, v109, s69, v163
	v_cvt_pk_fp8_f32 v180, v185, v182 op_sel:[0,0,1]
	v_cvt_pk_fp8_f32 v181, v186, v183 op_sel:[0,0,1]
	s_waitcnt lgkmcnt(0)
	v_lshlrev_b32_e32 v182, 16, v176
	v_and_b32_e32 v183, 0xffff0000, v176
	v_lshlrev_b32_e32 v184, 16, v178
	v_and_b32_e32 v185, 0xffff0000, v178
	v_pk_fma_f32 v[102:103], v[102:103], s[36:37], v[182:183] op_sel_hi:[1,0,1]
	v_pk_fma_f32 v[98:99], v[98:99], s[36:37], v[184:185] op_sel_hi:[1,0,1]
	v_med3_f32 v183, v102, s69, v163
	v_med3_f32 v185, v103, s69, v163
	v_mov_b32_e32 v182, v139
	v_cvt_pk_bf16_f32 v152, v110, v111
	v_cvt_pk_bf16_f32 v153, v112, v113
	v_cvt_pk_bf16_f32 v154, v106, v107
	v_cvt_pk_bf16_f32 v155, v108, v109
	v_lshlrev_b32_e32 v176, 16, v177
	v_and_b32_e32 v177, 0xffff0000, v177
	v_lshlrev_b32_e32 v178, 16, v179
	v_and_b32_e32 v179, 0xffff0000, v179
	v_med3_f32 v184, v98, s69, v163
	v_med3_f32 v186, v99, s69, v163
	v_cvt_pk_fp8_f32 v182, v183, v185
	v_mov_b32_e32 v183, v139
	v_pk_fma_f32 v[104:105], v[104:105], s[36:37], v[176:177] op_sel_hi:[1,0,1]
	v_pk_fma_f32 v[100:101], v[100:101], s[36:37], v[178:179] op_sel_hi:[1,0,1]
	v_cvt_pk_bf16_f32 v176, v102, v103
	v_cvt_pk_bf16_f32 v177, v104, v105
	v_cvt_pk_bf16_f32 v178, v98, v99
	v_cvt_pk_fp8_f32 v183, v184, v186
	v_cvt_pk_bf16_f32 v179, v100, v101
	ds_write_b128 v169, v[152:155]
	ds_write_b128 v169, v[176:179] offset:64
	ds_read_b128 v[152:155], v168
	ds_read_b128 v[176:179], v168 offset:1152
	s_add_u32 s78, s41, s50
	v_med3_f32 v187, v104, s69, v163
	v_med3_f32 v188, v100, s69, v163
	v_med3_f32 v184, v105, s69, v163
	v_med3_f32 v185, v101, s69, v163
	s_addc_u32 s79, s47, s51
	s_lshl_b64 s[74:75], s[74:75], 10
	v_cvt_pk_fp8_f32 v182, v187, v184 op_sel:[0,0,1]
	v_cvt_pk_fp8_f32 v183, v188, v185 op_sel:[0,0,1]
	v_lshl_add_u64 v[184:185], s[78:79], 0, v[138:139]
	s_add_u32 s41, s60, s74
	v_lshl_add_u64 v[184:185], v[184:185], 0, v[144:145]
	s_addc_u32 s47, s61, s75
	s_waitcnt lgkmcnt(1)
	global_store_dwordx4 v[184:185], v[152:155], off nt
	s_add_u32 s74, s41, s48
	s_addc_u32 s75, s47, s49
	v_lshl_add_u64 v[152:153], s[78:79], 0, v[146:147]
	v_lshl_add_u64 v[152:153], v[152:153], 0, v[144:145]
	s_waitcnt lgkmcnt(0)
	global_store_dwordx4 v[152:153], v[176:179], off nt
	ds_write2_b64 v170, v[180:181], v[182:183] offset1:4
	ds_read_b128 v[152:155], v171
	v_lshl_add_u64 v[176:177], s[74:75], 0, v[116:117]
	s_or_b32 s74, s70, 48
	s_ashr_i32 s75, s74, 31
	s_lshl_b64 s[78:79], s[74:75], 11
	s_add_u32 s41, s37, s78
	s_addc_u32 s47, s54, s79
	s_add_u32 s80, s41, s50
	v_lshl_add_u64 v[176:177], v[176:177], 0, v[114:115]
	s_addc_u32 s81, s47, s51
	s_waitcnt lgkmcnt(0)
	global_store_dwordx4 v[176:177], v[152:155], off nt
	v_lshl_add_u64 v[178:179], s[80:81], 0, v[146:147]
	s_waitcnt vmcnt(4)
	ds_write_b128 v168, v[156:159]
	s_waitcnt vmcnt(3)
	ds_write_b128 v168, v[172:175] offset:1152
	v_lshl_add_u64 v[152:153], s[80:81], 0, v[138:139]
	v_lshl_add_u64 v[176:177], v[152:153], 0, v[144:145]
	v_lshl_add_u64 v[172:173], v[178:179], 0, v[144:145]
	ds_read_b128 v[152:155], v169
	global_load_dwordx4 v[156:159], v[176:177], off
	s_nop 0
	global_load_dwordx4 v[172:175], v[172:173], off
	ds_read_b128 v[176:179], v169 offset:64
	s_add_u32 s41, s55, s76
	s_addc_u32 s47, s56, s77
	s_waitcnt lgkmcnt(1)
	v_lshlrev_b32_e32 v180, 16, v152
	v_and_b32_e32 v181, 0xffff0000, v152
	v_lshlrev_b32_e32 v182, 16, v154
	v_and_b32_e32 v183, 0xffff0000, v154
	v_pk_fma_f32 v[94:95], v[94:95], s[36:37], v[180:181] op_sel_hi:[1,0,1]
	v_pk_fma_f32 v[90:91], v[90:91], s[36:37], v[182:183] op_sel_hi:[1,0,1]
	v_med3_f32 v181, v94, s69, v163
	v_med3_f32 v183, v95, s69, v163
	v_mov_b32_e32 v180, v139
	v_med3_f32 v182, v90, s69, v163
	v_med3_f32 v184, v91, s69, v163
	v_cvt_pk_fp8_f32 v180, v181, v183
	v_mov_b32_e32 v181, v139
	v_cvt_pk_fp8_f32 v181, v182, v184
	v_lshlrev_b32_e32 v152, 16, v153
	v_and_b32_e32 v153, 0xffff0000, v153
	v_lshlrev_b32_e32 v154, 16, v155
	v_and_b32_e32 v155, 0xffff0000, v155
	v_pk_fma_f32 v[96:97], v[96:97], s[36:37], v[152:153] op_sel_hi:[1,0,1]
	v_pk_fma_f32 v[92:93], v[92:93], s[36:37], v[154:155] op_sel_hi:[1,0,1]
	v_med3_f32 v185, v96, s69, v163
	v_med3_f32 v186, v92, s69, v163
	v_med3_f32 v182, v97, s69, v163
	v_med3_f32 v183, v93, s69, v163
	v_cvt_pk_fp8_f32 v180, v185, v182 op_sel:[0,0,1]
	v_cvt_pk_fp8_f32 v181, v186, v183 op_sel:[0,0,1]
	s_waitcnt lgkmcnt(0)
	v_lshlrev_b32_e32 v182, 16, v176
	v_and_b32_e32 v183, 0xffff0000, v176
	v_lshlrev_b32_e32 v184, 16, v178
	v_and_b32_e32 v185, 0xffff0000, v178
	v_pk_fma_f32 v[86:87], v[86:87], s[36:37], v[182:183] op_sel_hi:[1,0,1]
	v_pk_fma_f32 v[82:83], v[82:83], s[36:37], v[184:185] op_sel_hi:[1,0,1]
	v_med3_f32 v183, v86, s69, v163
	v_med3_f32 v185, v87, s69, v163
	v_mov_b32_e32 v182, v139
	v_cvt_pk_bf16_f32 v152, v94, v95
	v_cvt_pk_bf16_f32 v153, v96, v97
	v_cvt_pk_bf16_f32 v154, v90, v91
	v_cvt_pk_bf16_f32 v155, v92, v93
	v_lshlrev_b32_e32 v176, 16, v177
	v_and_b32_e32 v177, 0xffff0000, v177
	v_lshlrev_b32_e32 v178, 16, v179
	v_and_b32_e32 v179, 0xffff0000, v179
	v_med3_f32 v184, v82, s69, v163
	v_med3_f32 v186, v83, s69, v163
	v_cvt_pk_fp8_f32 v182, v183, v185
	v_mov_b32_e32 v183, v139
	v_pk_fma_f32 v[88:89], v[88:89], s[36:37], v[176:177] op_sel_hi:[1,0,1]
	v_pk_fma_f32 v[84:85], v[84:85], s[36:37], v[178:179] op_sel_hi:[1,0,1]
	v_cvt_pk_bf16_f32 v176, v86, v87
	v_cvt_pk_bf16_f32 v177, v88, v89
	v_cvt_pk_bf16_f32 v178, v82, v83
	v_cvt_pk_fp8_f32 v183, v184, v186
	v_cvt_pk_bf16_f32 v179, v84, v85
	ds_write_b128 v169, v[152:155]
	ds_write_b128 v169, v[176:179] offset:64
	ds_read_b128 v[152:155], v168
	ds_read_b128 v[176:179], v168 offset:1152
	s_add_u32 s76, s41, s50
	v_med3_f32 v187, v88, s69, v163
	v_med3_f32 v188, v84, s69, v163
	v_med3_f32 v184, v89, s69, v163
	v_med3_f32 v185, v85, s69, v163
	s_addc_u32 s77, s47, s51
	s_lshl_b64 s[72:73], s[72:73], 10
	v_cvt_pk_fp8_f32 v182, v187, v184 op_sel:[0,0,1]
	v_cvt_pk_fp8_f32 v183, v188, v185 op_sel:[0,0,1]
	v_lshl_add_u64 v[184:185], s[76:77], 0, v[138:139]
	s_add_u32 s41, s60, s72
	v_lshl_add_u64 v[184:185], v[184:185], 0, v[144:145]
	s_addc_u32 s47, s61, s73
	s_waitcnt lgkmcnt(1)
	global_store_dwordx4 v[184:185], v[152:155], off nt
	s_add_u32 s72, s41, s48
	s_addc_u32 s73, s47, s49
	v_lshl_add_u64 v[152:153], s[76:77], 0, v[146:147]
	v_lshl_add_u64 v[152:153], v[152:153], 0, v[144:145]
	s_waitcnt lgkmcnt(0)
	global_store_dwordx4 v[152:153], v[176:179], off nt
	ds_write2_b64 v170, v[180:181], v[182:183] offset1:4
	ds_read_b128 v[152:155], v171
	v_lshl_add_u64 v[176:177], s[72:73], 0, v[116:117]
	s_add_i32 s72, s70, 0x80
	s_ashr_i32 s73, s72, 31
	s_lshl_b64 s[76:77], s[72:73], 11
	s_add_u32 s41, s37, s76
	s_addc_u32 s47, s54, s77
	s_add_u32 s80, s41, s50
	v_lshl_add_u64 v[176:177], v[176:177], 0, v[114:115]
	s_addc_u32 s81, s47, s51
	s_waitcnt lgkmcnt(0)
	global_store_dwordx4 v[176:177], v[152:155], off nt
	v_lshl_add_u64 v[178:179], s[80:81], 0, v[146:147]
	s_waitcnt vmcnt(4)
	ds_write_b128 v168, v[156:159]
	s_waitcnt vmcnt(3)
	ds_write_b128 v168, v[172:175] offset:1152
	v_lshl_add_u64 v[152:153], s[80:81], 0, v[138:139]
	v_lshl_add_u64 v[176:177], v[152:153], 0, v[144:145]
	v_lshl_add_u64 v[172:173], v[178:179], 0, v[144:145]
	ds_read_b128 v[152:155], v169
	global_load_dwordx4 v[156:159], v[176:177], off
	s_nop 0
	global_load_dwordx4 v[172:175], v[172:173], off
	ds_read_b128 v[176:179], v169 offset:64
	s_add_u32 s41, s55, s78
	s_addc_u32 s47, s56, s79
	s_waitcnt lgkmcnt(1)
	v_lshlrev_b32_e32 v180, 16, v152
	v_and_b32_e32 v181, 0xffff0000, v152
	v_lshlrev_b32_e32 v182, 16, v154
	v_and_b32_e32 v183, 0xffff0000, v154
	v_pk_fma_f32 v[78:79], v[78:79], s[36:37], v[180:181] op_sel_hi:[1,0,1]
	v_pk_fma_f32 v[74:75], v[74:75], s[36:37], v[182:183] op_sel_hi:[1,0,1]
	v_med3_f32 v181, v78, s69, v163
	v_med3_f32 v183, v79, s69, v163
	v_mov_b32_e32 v180, v139
	v_med3_f32 v182, v74, s69, v163
	v_med3_f32 v184, v75, s69, v163
	v_cvt_pk_fp8_f32 v180, v181, v183
	v_mov_b32_e32 v181, v139
	v_cvt_pk_fp8_f32 v181, v182, v184
	v_lshlrev_b32_e32 v152, 16, v153
	v_and_b32_e32 v153, 0xffff0000, v153
	v_lshlrev_b32_e32 v154, 16, v155
	v_and_b32_e32 v155, 0xffff0000, v155
	v_pk_fma_f32 v[80:81], v[80:81], s[36:37], v[152:153] op_sel_hi:[1,0,1]
	v_pk_fma_f32 v[76:77], v[76:77], s[36:37], v[154:155] op_sel_hi:[1,0,1]
	v_med3_f32 v185, v80, s69, v163
	v_med3_f32 v186, v76, s69, v163
	v_med3_f32 v182, v81, s69, v163
	v_med3_f32 v183, v77, s69, v163
	v_cvt_pk_fp8_f32 v180, v185, v182 op_sel:[0,0,1]
	v_cvt_pk_fp8_f32 v181, v186, v183 op_sel:[0,0,1]
	s_waitcnt lgkmcnt(0)
	v_lshlrev_b32_e32 v182, 16, v176
	v_and_b32_e32 v183, 0xffff0000, v176
	v_lshlrev_b32_e32 v184, 16, v178
	v_and_b32_e32 v185, 0xffff0000, v178
	v_pk_fma_f32 v[70:71], v[70:71], s[36:37], v[182:183] op_sel_hi:[1,0,1]
	v_pk_fma_f32 v[66:67], v[66:67], s[36:37], v[184:185] op_sel_hi:[1,0,1]
	v_med3_f32 v183, v70, s69, v163
	v_med3_f32 v185, v71, s69, v163
	v_mov_b32_e32 v182, v139
	v_cvt_pk_bf16_f32 v152, v78, v79
	v_cvt_pk_bf16_f32 v153, v80, v81
	v_cvt_pk_bf16_f32 v154, v74, v75
	v_cvt_pk_bf16_f32 v155, v76, v77
	v_lshlrev_b32_e32 v176, 16, v177
	v_and_b32_e32 v177, 0xffff0000, v177
	v_lshlrev_b32_e32 v178, 16, v179
	v_and_b32_e32 v179, 0xffff0000, v179
	v_med3_f32 v184, v66, s69, v163
	v_med3_f32 v186, v67, s69, v163
	v_cvt_pk_fp8_f32 v182, v183, v185
	v_mov_b32_e32 v183, v139
	v_pk_fma_f32 v[72:73], v[72:73], s[36:37], v[176:177] op_sel_hi:[1,0,1]
	v_pk_fma_f32 v[68:69], v[68:69], s[36:37], v[178:179] op_sel_hi:[1,0,1]
	v_cvt_pk_bf16_f32 v176, v70, v71
	v_cvt_pk_bf16_f32 v177, v72, v73
	v_cvt_pk_bf16_f32 v178, v66, v67
	v_cvt_pk_fp8_f32 v183, v184, v186
	v_cvt_pk_bf16_f32 v179, v68, v69
	ds_write_b128 v169, v[152:155]
	ds_write_b128 v169, v[176:179] offset:64
	ds_read_b128 v[152:155], v168
	ds_read_b128 v[176:179], v168 offset:1152
	s_add_u32 s78, s41, s50
	v_med3_f32 v187, v72, s69, v163
	v_med3_f32 v188, v68, s69, v163
	v_med3_f32 v184, v73, s69, v163
	v_med3_f32 v185, v69, s69, v163
	s_addc_u32 s79, s47, s51
	s_lshl_b64 s[74:75], s[74:75], 10
	v_cvt_pk_fp8_f32 v182, v187, v184 op_sel:[0,0,1]
	v_cvt_pk_fp8_f32 v183, v188, v185 op_sel:[0,0,1]
	v_lshl_add_u64 v[184:185], s[78:79], 0, v[138:139]
	s_add_u32 s41, s60, s74
	v_lshl_add_u64 v[184:185], v[184:185], 0, v[144:145]
	s_addc_u32 s47, s61, s75
	s_waitcnt lgkmcnt(1)
	global_store_dwordx4 v[184:185], v[152:155], off nt
	s_add_u32 s74, s41, s48
	s_addc_u32 s75, s47, s49
	v_lshl_add_u64 v[152:153], s[78:79], 0, v[146:147]
	v_lshl_add_u64 v[152:153], v[152:153], 0, v[144:145]
	s_waitcnt lgkmcnt(0)
	global_store_dwordx4 v[152:153], v[176:179], off nt
	ds_write2_b64 v170, v[180:181], v[182:183] offset1:4
	ds_read_b128 v[152:155], v171
	v_lshl_add_u64 v[176:177], s[74:75], 0, v[116:117]
	s_add_i32 s74, s70, 0x90
	s_ashr_i32 s75, s74, 31
	s_lshl_b64 s[78:79], s[74:75], 11
	s_add_u32 s41, s37, s78
	s_addc_u32 s47, s54, s79
	s_add_u32 s80, s41, s50
	v_lshl_add_u64 v[176:177], v[176:177], 0, v[114:115]
	s_addc_u32 s81, s47, s51
	s_waitcnt lgkmcnt(0)
	global_store_dwordx4 v[176:177], v[152:155], off nt
	v_lshl_add_u64 v[178:179], s[80:81], 0, v[146:147]
	s_waitcnt vmcnt(4)
	ds_write_b128 v168, v[156:159]
	s_waitcnt vmcnt(3)
	ds_write_b128 v168, v[172:175] offset:1152
	v_lshl_add_u64 v[152:153], s[80:81], 0, v[138:139]
	v_lshl_add_u64 v[176:177], v[152:153], 0, v[144:145]
	v_lshl_add_u64 v[172:173], v[178:179], 0, v[144:145]
	ds_read_b128 v[152:155], v169
	global_load_dwordx4 v[156:159], v[176:177], off
	s_nop 0
	global_load_dwordx4 v[172:175], v[172:173], off
	ds_read_b128 v[176:179], v169 offset:64
	s_add_u32 s41, s55, s76
	s_addc_u32 s47, s56, s77
	s_waitcnt lgkmcnt(1)
	v_lshlrev_b32_e32 v180, 16, v152
	v_and_b32_e32 v181, 0xffff0000, v152
	v_lshlrev_b32_e32 v182, 16, v154
	v_and_b32_e32 v183, 0xffff0000, v154
	v_pk_fma_f32 v[62:63], v[62:63], s[36:37], v[180:181] op_sel_hi:[1,0,1]
	v_pk_fma_f32 v[58:59], v[58:59], s[36:37], v[182:183] op_sel_hi:[1,0,1]
	v_med3_f32 v181, v62, s69, v163
	v_med3_f32 v183, v63, s69, v163
	v_mov_b32_e32 v180, v139
	v_med3_f32 v182, v58, s69, v163
	v_med3_f32 v184, v59, s69, v163
	v_cvt_pk_fp8_f32 v180, v181, v183
	v_mov_b32_e32 v181, v139
	v_cvt_pk_fp8_f32 v181, v182, v184
	v_lshlrev_b32_e32 v152, 16, v153
	v_and_b32_e32 v153, 0xffff0000, v153
	v_lshlrev_b32_e32 v154, 16, v155
	v_and_b32_e32 v155, 0xffff0000, v155
	v_pk_fma_f32 v[64:65], v[64:65], s[36:37], v[152:153] op_sel_hi:[1,0,1]
	v_pk_fma_f32 v[60:61], v[60:61], s[36:37], v[154:155] op_sel_hi:[1,0,1]
	v_med3_f32 v185, v64, s69, v163
	v_med3_f32 v186, v60, s69, v163
	v_med3_f32 v182, v65, s69, v163
	v_med3_f32 v183, v61, s69, v163
	v_cvt_pk_fp8_f32 v180, v185, v182 op_sel:[0,0,1]
	v_cvt_pk_fp8_f32 v181, v186, v183 op_sel:[0,0,1]
	s_waitcnt lgkmcnt(0)
	v_lshlrev_b32_e32 v182, 16, v176
	v_and_b32_e32 v183, 0xffff0000, v176
	v_lshlrev_b32_e32 v184, 16, v178
	v_and_b32_e32 v185, 0xffff0000, v178
	v_pk_fma_f32 v[54:55], v[54:55], s[36:37], v[182:183] op_sel_hi:[1,0,1]
	v_pk_fma_f32 v[50:51], v[50:51], s[36:37], v[184:185] op_sel_hi:[1,0,1]
	v_med3_f32 v183, v54, s69, v163
	v_med3_f32 v185, v55, s69, v163
	v_mov_b32_e32 v182, v139
	v_med3_f32 v184, v50, s69, v163
	v_med3_f32 v186, v51, s69, v163
	v_cvt_pk_fp8_f32 v182, v183, v185
	v_mov_b32_e32 v183, v139
	v_cvt_pk_bf16_f32 v152, v62, v63
	v_cvt_pk_bf16_f32 v153, v64, v65
	v_cvt_pk_bf16_f32 v154, v58, v59
	v_cvt_pk_bf16_f32 v155, v60, v61
	v_lshlrev_b32_e32 v176, 16, v177
	v_and_b32_e32 v177, 0xffff0000, v177
	v_lshlrev_b32_e32 v178, 16, v179
	v_and_b32_e32 v179, 0xffff0000, v179
	v_cvt_pk_fp8_f32 v183, v184, v186
	v_pk_fma_f32 v[56:57], v[56:57], s[36:37], v[176:177] op_sel_hi:[1,0,1]
	v_pk_fma_f32 v[52:53], v[52:53], s[36:37], v[178:179] op_sel_hi:[1,0,1]
	v_cvt_pk_bf16_f32 v176, v54, v55
	v_cvt_pk_bf16_f32 v177, v56, v57
	v_cvt_pk_bf16_f32 v178, v50, v51
	s_add_u32 s76, s41, s50
	v_cvt_pk_bf16_f32 v179, v52, v53
	ds_write_b128 v169, v[152:155]
	ds_write_b128 v169, v[176:179] offset:64
	ds_read_b128 v[152:155], v168
	ds_read_b128 v[176:179], v168 offset:1152
	v_med3_f32 v187, v56, s69, v163
	v_med3_f32 v188, v52, s69, v163
	v_med3_f32 v184, v57, s69, v163
	v_med3_f32 v185, v53, s69, v163
	s_addc_u32 s77, s47, s51
	s_lshl_b64 s[72:73], s[72:73], 10
	v_cvt_pk_fp8_f32 v182, v187, v184 op_sel:[0,0,1]
	v_cvt_pk_fp8_f32 v183, v188, v185 op_sel:[0,0,1]
	s_add_u32 s41, s60, s72
	v_lshl_add_u64 v[184:185], s[76:77], 0, v[138:139]
	s_addc_u32 s47, s61, s73
	v_lshl_add_u64 v[184:185], v[184:185], 0, v[144:145]
	s_add_u32 s72, s41, s48
	s_waitcnt lgkmcnt(1)
	global_store_dwordx4 v[184:185], v[152:155], off nt
	s_addc_u32 s73, s47, s49
	ds_write2_b64 v170, v[180:181], v[182:183] offset1:4
	v_lshl_add_u64 v[152:153], s[76:77], 0, v[146:147]
	s_add_i32 s76, s70, 0xa0
	v_lshl_add_u64 v[152:153], v[152:153], 0, v[144:145]
	s_ashr_i32 s77, s76, 31
	s_waitcnt lgkmcnt(1)
	global_store_dwordx4 v[152:153], v[176:179], off nt
	ds_read_b128 v[152:155], v171
	s_lshl_b64 s[80:81], s[76:77], 11
	s_add_u32 s41, s37, s80
	s_addc_u32 s47, s54, s81
	v_lshl_add_u64 v[176:177], s[72:73], 0, v[116:117]
	s_add_u32 s72, s41, s50
	v_lshl_add_u64 v[176:177], v[176:177], 0, v[114:115]
	s_addc_u32 s73, s47, s51
	s_waitcnt lgkmcnt(0)
	global_store_dwordx4 v[176:177], v[152:155], off nt
	v_lshl_add_u64 v[178:179], s[72:73], 0, v[146:147]
	s_waitcnt vmcnt(4)
	ds_write_b128 v168, v[156:159]
	s_waitcnt vmcnt(3)
	ds_write_b128 v168, v[172:175] offset:1152
	v_lshl_add_u64 v[152:153], s[72:73], 0, v[138:139]
	v_lshl_add_u64 v[176:177], v[152:153], 0, v[144:145]
	ds_read_b128 v[152:155], v169
	v_lshl_add_u64 v[156:157], v[178:179], 0, v[144:145]
	global_load_dwordx4 v[172:175], v[176:177], off
	s_nop 0
	global_load_dwordx4 v[176:179], v[156:157], off
	ds_read_b128 v[156:159], v169 offset:64
	v_mov_b32_e32 v184, v139
	s_waitcnt lgkmcnt(1)
	v_lshlrev_b32_e32 v180, 16, v152
	v_and_b32_e32 v181, 0xffff0000, v152
	v_lshlrev_b32_e32 v182, 16, v154
	v_and_b32_e32 v183, 0xffff0000, v154
	v_lshlrev_b32_e32 v152, 16, v153
	v_and_b32_e32 v153, 0xffff0000, v153
	v_lshlrev_b32_e32 v154, 16, v155
	v_and_b32_e32 v155, 0xffff0000, v155
	v_pk_fma_f32 v[46:47], v[46:47], s[36:37], v[180:181] op_sel_hi:[1,0,1]
	v_pk_fma_f32 v[42:43], v[42:43], s[36:37], v[182:183] op_sel_hi:[1,0,1]
	v_pk_fma_f32 v[48:49], v[48:49], s[36:37], v[152:153] op_sel_hi:[1,0,1]
	v_pk_fma_f32 v[44:45], v[44:45], s[36:37], v[154:155] op_sel_hi:[1,0,1]
	v_med3_f32 v152, v46, s69, v163
	v_med3_f32 v153, v42, s69, v163
	v_med3_f32 v154, v47, s69, v163
	v_med3_f32 v155, v43, s69, v163
	v_mov_b32_e32 v185, v139
	v_cvt_pk_fp8_f32 v184, v152, v154
	v_cvt_pk_fp8_f32 v185, v153, v155
	v_med3_f32 v186, v48, s69, v163
	v_med3_f32 v187, v44, s69, v163
	v_med3_f32 v152, v49, s69, v163
	v_med3_f32 v153, v45, s69, v163
	v_cvt_pk_fp8_f32 v184, v186, v152 op_sel:[0,0,1]
	v_cvt_pk_fp8_f32 v185, v187, v153 op_sel:[0,0,1]
	s_waitcnt lgkmcnt(0)
	v_lshlrev_b32_e32 v154, 16, v156
	v_and_b32_e32 v155, 0xffff0000, v156
	v_lshlrev_b32_e32 v186, 16, v158
	v_and_b32_e32 v187, 0xffff0000, v158
	v_lshlrev_b32_e32 v158, 16, v159
	v_and_b32_e32 v159, 0xffff0000, v159
	v_lshlrev_b32_e32 v152, 16, v157
	v_and_b32_e32 v153, 0xffff0000, v157
	v_pk_fma_f32 v[156:157], v[38:39], s[36:37], v[154:155] op_sel_hi:[1,0,1]
	v_pk_fma_f32 v[154:155], v[36:37], s[36:37], v[158:159] op_sel_hi:[1,0,1]
	v_pk_fma_f32 v[158:159], v[34:35], s[36:37], v[186:187] op_sel_hi:[1,0,1]
	v_pk_fma_f32 v[152:153], v[40:41], s[36:37], v[152:153] op_sel_hi:[1,0,1]
	v_med3_f32 v38, v156, s69, v163
	v_med3_f32 v39, v158, s69, v163
	v_med3_f32 v40, v157, s69, v163
	v_med3_f32 v41, v159, s69, v163
	v_mov_b32_e32 v186, v139
	v_mov_b32_e32 v187, v139
	v_cvt_pk_bf16_f32 v180, v46, v47
	v_cvt_pk_bf16_f32 v181, v48, v49
	v_cvt_pk_bf16_f32 v182, v42, v43
	v_cvt_pk_bf16_f32 v183, v44, v45
	v_cvt_pk_fp8_f32 v186, v38, v40
	v_cvt_pk_fp8_f32 v187, v39, v41
	v_cvt_pk_bf16_f32 v34, v156, v157
	v_cvt_pk_bf16_f32 v35, v152, v153
	v_cvt_pk_bf16_f32 v36, v158, v159
	v_cvt_pk_bf16_f32 v37, v154, v155
	s_add_u32 s41, s55, s78
	ds_write_b128 v169, v[180:183]
	ds_write_b128 v169, v[34:37] offset:64
	s_addc_u32 s47, s56, s79
	ds_read_b128 v[34:37], v168
	v_med3_f32 v188, v152, s69, v163
	v_med3_f32 v189, v154, s69, v163
	v_med3_f32 v38, v153, s69, v163
	v_med3_f32 v39, v155, s69, v163
	s_add_u32 s72, s41, s50
	v_cvt_pk_fp8_f32 v186, v188, v38 op_sel:[0,0,1]
	v_cvt_pk_fp8_f32 v187, v189, v39 op_sel:[0,0,1]
	s_addc_u32 s73, s47, s51
	ds_read_b128 v[38:41], v168 offset:1152
	v_lshl_add_u64 v[180:181], s[72:73], 0, v[138:139]
	v_lshl_add_u64 v[180:181], v[180:181], 0, v[144:145]
	s_waitcnt lgkmcnt(1)
	global_store_dwordx4 v[180:181], v[34:37], off nt
	ds_write2_b64 v170, v[184:185], v[186:187] offset1:4
	v_mov_b32_e32 v187, v139
	v_lshl_add_u64 v[34:35], s[72:73], 0, v[146:147]
	s_lshl_b64 s[72:73], s[74:75], 10
	v_lshl_add_u64 v[34:35], v[34:35], 0, v[144:145]
	s_add_u32 s41, s60, s72
	s_waitcnt lgkmcnt(1)
	global_store_dwordx4 v[34:35], v[38:41], off nt
	s_addc_u32 s47, s61, s73
	ds_read_b128 v[34:37], v171
	s_add_u32 s72, s41, s48
	s_addc_u32 s73, s47, s49
	v_lshl_add_u64 v[38:39], s[72:73], 0, v[116:117]
	v_lshl_add_u64 v[38:39], v[38:39], 0, v[114:115]
	s_waitcnt lgkmcnt(0)
	global_store_dwordx4 v[38:39], v[34:37], off nt
	s_addk_i32 s70, 0xb0
	s_waitcnt vmcnt(4)
	ds_write_b128 v168, v[172:175]
	s_waitcnt vmcnt(3)
	ds_write_b128 v168, v[176:179] offset:1152
	s_ashr_i32 s71, s70, 31
	ds_read_b128 v[172:175], v169
	s_lshl_b64 s[72:73], s[70:71], 11
	s_add_u32 s41, s37, s72
	s_addc_u32 s47, s54, s73
	s_add_u32 s74, s41, s50
	s_addc_u32 s75, s47, s51
	s_waitcnt lgkmcnt(0)
	v_lshlrev_b32_e32 v180, 16, v172
	v_and_b32_e32 v181, 0xffff0000, v172
	v_lshl_add_u64 v[34:35], s[74:75], 0, v[138:139]
	v_lshl_add_u64 v[36:37], s[74:75], 0, v[146:147]
	v_lshlrev_b32_e32 v172, 16, v173
	v_and_b32_e32 v173, 0xffff0000, v173
	v_lshlrev_b32_e32 v182, 16, v174
	v_and_b32_e32 v183, 0xffff0000, v174
	v_lshlrev_b32_e32 v174, 16, v175
	v_and_b32_e32 v175, 0xffff0000, v175
	v_pk_fma_f32 v[30:31], v[30:31], s[36:37], v[180:181] op_sel_hi:[1,0,1]
	v_lshl_add_u64 v[34:35], v[34:35], 0, v[144:145]
	v_lshl_add_u64 v[38:39], v[36:37], 0, v[144:145]
	v_pk_fma_f32 v[32:33], v[32:33], s[36:37], v[172:173] op_sel_hi:[1,0,1]
	v_pk_fma_f32 v[172:173], v[28:29], s[36:37], v[174:175] op_sel_hi:[1,0,1]
	v_pk_fma_f32 v[174:175], v[26:27], s[36:37], v[182:183] op_sel_hi:[1,0,1]
	v_med3_f32 v181, v30, s69, v163
	v_med3_f32 v183, v31, s69, v163
	v_mov_b32_e32 v180, v139
	global_load_dwordx4 v[34:37], v[34:35], off
	s_nop 0
	global_load_dwordx4 v[38:41], v[38:39], off
	ds_read_b128 v[176:179], v169 offset:64
	v_med3_f32 v182, v174, s69, v163
	v_med3_f32 v184, v175, s69, v163
	v_cvt_pk_fp8_f32 v180, v181, v183
	v_mov_b32_e32 v181, v139
	v_cvt_pk_fp8_f32 v181, v182, v184
	v_med3_f32 v185, v32, s69, v163
	v_med3_f32 v186, v172, s69, v163
	v_med3_f32 v182, v33, s69, v163
	v_med3_f32 v183, v173, s69, v163
	v_cvt_pk_fp8_f32 v180, v185, v182 op_sel:[0,0,1]
	v_cvt_pk_fp8_f32 v181, v186, v183 op_sel:[0,0,1]
	s_waitcnt lgkmcnt(0)
	v_lshlrev_b32_e32 v182, 16, v176
	v_and_b32_e32 v183, 0xffff0000, v176
	v_lshlrev_b32_e32 v184, 16, v178
	v_and_b32_e32 v185, 0xffff0000, v178
	v_lshlrev_b32_e32 v176, 16, v177
	v_and_b32_e32 v177, 0xffff0000, v177
	v_pk_fma_f32 v[182:183], v[22:23], s[36:37], v[182:183] op_sel_hi:[1,0,1]
	v_pk_fma_f32 v[184:185], v[18:19], s[36:37], v[184:185] op_sel_hi:[1,0,1]
	v_pk_fma_f32 v[176:177], v[24:25], s[36:37], v[176:177] op_sel_hi:[1,0,1]
	v_med3_f32 v22, v182, s69, v163
	v_med3_f32 v23, v184, s69, v163
	v_med3_f32 v24, v183, s69, v163
	v_med3_f32 v25, v185, s69, v163
	v_mov_b32_e32 v186, v139
	v_cvt_pk_bf16_f32 v26, v30, v31
	v_cvt_pk_bf16_f32 v27, v32, v33
	v_cvt_pk_bf16_f32 v28, v174, v175
	v_cvt_pk_bf16_f32 v29, v172, v173
	v_lshlrev_b32_e32 v178, 16, v179
	v_and_b32_e32 v179, 0xffff0000, v179
	v_cvt_pk_fp8_f32 v186, v22, v24
	v_cvt_pk_fp8_f32 v187, v23, v25
	v_pk_fma_f32 v[178:179], v[20:21], s[36:37], v[178:179] op_sel_hi:[1,0,1]
	v_cvt_pk_bf16_f32 v18, v182, v183
	v_cvt_pk_bf16_f32 v19, v176, v177
	v_cvt_pk_bf16_f32 v20, v184, v185
	s_add_u32 s41, s55, s80
	v_cvt_pk_bf16_f32 v21, v178, v179
	ds_write_b128 v169, v[26:29]
	ds_write_b128 v169, v[18:21] offset:64
	s_addc_u32 s47, s56, s81
	ds_read_b128 v[18:21], v168
	v_med3_f32 v188, v176, s69, v163
	v_med3_f32 v189, v178, s69, v163
	v_med3_f32 v22, v177, s69, v163
	v_med3_f32 v23, v179, s69, v163
	s_add_u32 s74, s41, s50
	v_cvt_pk_fp8_f32 v186, v188, v22 op_sel:[0,0,1]
	v_cvt_pk_fp8_f32 v187, v189, v23 op_sel:[0,0,1]
	s_addc_u32 s75, s47, s51
	ds_read_b128 v[22:25], v168 offset:1152
	v_lshl_add_u64 v[26:27], s[74:75], 0, v[138:139]
	v_lshl_add_u64 v[26:27], v[26:27], 0, v[144:145]
	s_waitcnt lgkmcnt(1)
	global_store_dwordx4 v[26:27], v[18:21], off nt
	ds_write2_b64 v170, v[180:181], v[186:187] offset1:4
	s_nop 0
	v_lshl_add_u64 v[18:19], s[74:75], 0, v[146:147]
	s_lshl_b64 s[74:75], s[76:77], 10
	v_lshl_add_u64 v[18:19], v[18:19], 0, v[144:145]
	s_add_u32 s41, s60, s74
	s_waitcnt lgkmcnt(1)
	global_store_dwordx4 v[18:19], v[22:25], off nt
	s_addc_u32 s47, s61, s75
	ds_read_b128 v[18:21], v171
	s_add_u32 s74, s41, s48
	s_addc_u32 s75, s47, s49
	v_lshl_add_u64 v[22:23], s[74:75], 0, v[116:117]
	v_lshl_add_u64 v[22:23], v[22:23], 0, v[114:115]
	s_waitcnt lgkmcnt(0)
	global_store_dwordx4 v[22:23], v[18:21], off nt
	s_waitcnt vmcnt(4)
	ds_write_b128 v168, v[34:37]
	s_waitcnt vmcnt(3)
	ds_write_b128 v168, v[38:41] offset:1152
	v_mul_f32_e32 v18, v31, v31
	v_mul_f32_e32 v19, v33, v33
	v_fmac_f32_e32 v18, v30, v30
	v_fmac_f32_e32 v19, v32, v32
	v_add_f32_e32 v18, v18, v19
	v_mul_f32_e32 v19, v175, v175
	v_mul_f32_e32 v20, v173, v173
	v_fmac_f32_e32 v19, v174, v174
	v_fmac_f32_e32 v20, v172, v172
	v_add_f32_e32 v19, v19, v20
	v_add_f32_e32 v18, v18, v19
	v_mul_f32_e32 v19, v183, v183
	v_mul_f32_e32 v20, v177, v177
	v_fmac_f32_e32 v19, v182, v182
	v_fmac_f32_e32 v20, v176, v176
	v_add_f32_e32 v19, v19, v20
	v_mul_f32_e32 v20, v185, v185
	v_mul_f32_e32 v21, v179, v179
	v_fmac_f32_e32 v20, v184, v184
	v_fmac_f32_e32 v21, v178, v178
	v_add_f32_e32 v20, v20, v21
	v_add_f32_e32 v19, v19, v20
	v_add_f32_e32 v30, v18, v19
	v_mul_f32_e32 v18, v47, v47
	v_mul_f32_e32 v19, v49, v49
	v_fmac_f32_e32 v18, v46, v46
	v_fmac_f32_e32 v19, v48, v48
	v_add_f32_e32 v18, v18, v19
	v_mul_f32_e32 v19, v43, v43
	v_mul_f32_e32 v20, v45, v45
	v_fmac_f32_e32 v19, v42, v42
	v_fmac_f32_e32 v20, v44, v44
	v_add_f32_e32 v19, v19, v20
	v_add_f32_e32 v18, v18, v19
	v_mul_f32_e32 v19, v157, v157
	v_mul_f32_e32 v20, v153, v153
	v_fmac_f32_e32 v19, v156, v156
	v_fmac_f32_e32 v20, v152, v152
	v_add_f32_e32 v19, v19, v20
	v_mul_f32_e32 v20, v159, v159
	v_mul_f32_e32 v21, v155, v155
	v_fmac_f32_e32 v20, v158, v158
	v_fmac_f32_e32 v21, v154, v154
	v_add_f32_e32 v20, v20, v21
	v_add_f32_e32 v19, v19, v20
	v_add_f32_e32 v31, v18, v19
	v_mul_f32_e32 v18, v63, v63
	v_mul_f32_e32 v19, v65, v65
	v_fmac_f32_e32 v18, v62, v62
	v_fmac_f32_e32 v19, v64, v64
	v_add_f32_e32 v18, v18, v19
	v_mul_f32_e32 v19, v59, v59
	v_mul_f32_e32 v20, v61, v61
	v_fmac_f32_e32 v19, v58, v58
	v_fmac_f32_e32 v20, v60, v60
	v_add_f32_e32 v19, v19, v20
	v_add_f32_e32 v18, v18, v19
	v_mul_f32_e32 v19, v55, v55
	v_mul_f32_e32 v20, v57, v57
	v_fmac_f32_e32 v19, v54, v54
	v_fmac_f32_e32 v20, v56, v56
	v_add_f32_e32 v19, v19, v20
	v_mul_f32_e32 v20, v51, v51
	v_mul_f32_e32 v21, v53, v53
	v_fmac_f32_e32 v20, v50, v50
	v_fmac_f32_e32 v21, v52, v52
	v_add_f32_e32 v20, v20, v21
	v_add_f32_e32 v19, v19, v20
	v_add_f32_e32 v32, v18, v19
	v_mul_f32_e32 v18, v79, v79
	v_mul_f32_e32 v19, v81, v81
	v_fmac_f32_e32 v18, v78, v78
	v_fmac_f32_e32 v19, v80, v80
	v_add_f32_e32 v18, v18, v19
	v_mul_f32_e32 v19, v75, v75
	v_mul_f32_e32 v20, v77, v77
	v_fmac_f32_e32 v19, v74, v74
	v_fmac_f32_e32 v20, v76, v76
	v_add_f32_e32 v19, v19, v20
	v_add_f32_e32 v18, v18, v19
	v_mul_f32_e32 v19, v71, v71
	v_mul_f32_e32 v20, v73, v73
	v_fmac_f32_e32 v19, v70, v70
	v_fmac_f32_e32 v20, v72, v72
	v_add_f32_e32 v19, v19, v20
	v_mul_f32_e32 v20, v67, v67
	v_mul_f32_e32 v21, v69, v69
	v_fmac_f32_e32 v20, v66, v66
	v_fmac_f32_e32 v21, v68, v68
	v_add_f32_e32 v20, v20, v21
	v_add_f32_e32 v19, v19, v20
	v_add_f32_e32 v33, v18, v19
	v_mul_f32_e32 v18, v95, v95
	v_mul_f32_e32 v19, v97, v97
	v_fmac_f32_e32 v18, v94, v94
	v_fmac_f32_e32 v19, v96, v96
	v_add_f32_e32 v18, v18, v19
	v_mul_f32_e32 v19, v91, v91
	v_mul_f32_e32 v20, v93, v93
	v_fmac_f32_e32 v19, v90, v90
	v_fmac_f32_e32 v20, v92, v92
	v_add_f32_e32 v19, v19, v20
	v_add_f32_e32 v18, v18, v19
	v_mul_f32_e32 v19, v87, v87
	v_mul_f32_e32 v20, v89, v89
	v_fmac_f32_e32 v19, v86, v86
	v_fmac_f32_e32 v20, v88, v88
	v_add_f32_e32 v19, v19, v20
	v_mul_f32_e32 v20, v83, v83
	v_mul_f32_e32 v21, v85, v85
	v_fmac_f32_e32 v20, v82, v82
	v_fmac_f32_e32 v21, v84, v84
	v_add_f32_e32 v20, v20, v21
	v_add_f32_e32 v19, v19, v20
	v_add_f32_e32 v42, v18, v19
	v_mul_f32_e32 v18, v111, v111
	v_mul_f32_e32 v19, v113, v113
	v_fmac_f32_e32 v18, v110, v110
	v_fmac_f32_e32 v19, v112, v112
	v_add_f32_e32 v18, v18, v19
	v_mul_f32_e32 v19, v107, v107
	v_mul_f32_e32 v20, v109, v109
	v_fmac_f32_e32 v19, v106, v106
	v_fmac_f32_e32 v20, v108, v108
	v_add_f32_e32 v19, v19, v20
	v_add_f32_e32 v18, v18, v19
	v_mul_f32_e32 v19, v103, v103
	v_mul_f32_e32 v20, v105, v105
	v_fmac_f32_e32 v19, v102, v102
	v_fmac_f32_e32 v20, v104, v104
	v_add_f32_e32 v19, v19, v20
	v_mul_f32_e32 v20, v99, v99
	v_mul_f32_e32 v21, v101, v101
	v_fmac_f32_e32 v20, v98, v98
	v_fmac_f32_e32 v21, v100, v100
	v_add_f32_e32 v20, v20, v21
	v_add_f32_e32 v19, v19, v20
	v_add_f32_e32 v43, v18, v19
	v_mul_f32_e32 v18, v151, v151
	v_mul_f32_e32 v19, v149, v149
	v_fmac_f32_e32 v18, v150, v150
	v_fmac_f32_e32 v19, v148, v148
	v_add_f32_e32 v18, v18, v19
	v_mul_f32_e32 v19, v123, v123
	v_mul_f32_e32 v20, v125, v125
	v_fmac_f32_e32 v19, v122, v122
	v_fmac_f32_e32 v20, v124, v124
	v_add_f32_e32 v19, v19, v20
	v_add_f32_e32 v22, v18, v19
	v_mul_f32_e32 v18, v127, v127
	v_mul_f32_e32 v19, v119, v119
	v_fmac_f32_e32 v18, v126, v126
	v_fmac_f32_e32 v19, v118, v118
	v_add_f32_e32 v23, v18, v19
	ds_read_b128 v[18:21], v169
	v_mul_f32_e32 v24, v129, v129
	v_mul_f32_e32 v25, v121, v121
	v_fmac_f32_e32 v24, v128, v128
	v_fmac_f32_e32 v25, v120, v120
	v_add_f32_e32 v24, v24, v25
	v_add_f32_e32 v23, v23, v24
	v_add_f32_e32 v34, v22, v23
	ds_read_b128 v[22:25], v169 offset:64
	s_waitcnt lgkmcnt(1)
	v_lshlrev_b32_e32 v26, 16, v18
	v_and_b32_e32 v27, 0xffff0000, v18
	v_lshlrev_b32_e32 v18, 16, v19
	v_and_b32_e32 v19, 0xffff0000, v19
	v_lshlrev_b32_e32 v28, 16, v20
	v_and_b32_e32 v29, 0xffff0000, v20
	v_lshlrev_b32_e32 v20, 16, v21
	v_and_b32_e32 v21, 0xffff0000, v21
	v_pk_fma_f32 v[16:17], v[16:17], s[36:37], v[18:19] op_sel_hi:[1,0,1]
	v_pk_fma_f32 v[14:15], v[14:15], s[36:37], v[26:27] op_sel_hi:[1,0,1]
	v_pk_fma_f32 v[18:19], v[12:13], s[36:37], v[20:21] op_sel_hi:[1,0,1]
	v_pk_fma_f32 v[20:21], v[10:11], s[36:37], v[28:29] op_sel_hi:[1,0,1]
	v_mul_f32_e32 v10, v15, v15
	v_mul_f32_e32 v11, v17, v17
	v_fmac_f32_e32 v10, v14, v14
	v_fmac_f32_e32 v11, v16, v16
	v_add_f32_e32 v10, v10, v11
	v_mul_f32_e32 v11, v21, v21
	v_mul_f32_e32 v12, v19, v19
	v_fmac_f32_e32 v11, v20, v20
	v_fmac_f32_e32 v12, v18, v18
	v_add_f32_e32 v11, v11, v12
	v_add_f32_e32 v26, v10, v11
	v_cvt_pk_bf16_f32 v10, v14, v15
	v_med3_f32 v27, v14, s69, v163
	v_med3_f32 v15, v15, s69, v163
	v_mov_b32_e32 v14, v139
	v_cvt_pk_bf16_f32 v11, v16, v17
	v_cvt_pk_bf16_f32 v12, v20, v21
	v_med3_f32 v20, v20, s69, v163
	v_med3_f32 v21, v21, s69, v163
	v_cvt_pk_fp8_f32 v14, v27, v15
	v_mov_b32_e32 v15, v139
	v_cvt_pk_fp8_f32 v15, v20, v21
	v_cvt_pk_bf16_f32 v13, v18, v19
	v_med3_f32 v16, v16, s69, v163
	v_med3_f32 v18, v18, s69, v163
	v_med3_f32 v17, v17, s69, v163
	v_med3_f32 v19, v19, s69, v163
	v_cvt_pk_fp8_f32 v14, v16, v17 op_sel:[0,0,1]
	v_cvt_pk_fp8_f32 v15, v18, v19 op_sel:[0,0,1]
	s_waitcnt lgkmcnt(0)
	v_lshlrev_b32_e32 v16, 16, v22
	v_and_b32_e32 v17, 0xffff0000, v22
	v_lshlrev_b32_e32 v18, 16, v23
	v_and_b32_e32 v19, 0xffff0000, v23
	v_lshlrev_b32_e32 v20, 16, v24
	v_and_b32_e32 v21, 0xffff0000, v24
	v_pk_fma_f32 v[8:9], v[8:9], s[36:37], v[18:19] op_sel_hi:[1,0,1]
	v_pk_fma_f32 v[6:7], v[6:7], s[36:37], v[16:17] op_sel_hi:[1,0,1]
	v_lshlrev_b32_e32 v22, 16, v25
	v_and_b32_e32 v23, 0xffff0000, v25
	v_pk_fma_f32 v[18:19], v[2:3], s[36:37], v[20:21] op_sel_hi:[1,0,1]
	v_mul_f32_e32 v2, v7, v7
	v_mul_f32_e32 v3, v9, v9
	v_pk_fma_f32 v[16:17], v[4:5], s[36:37], v[22:23] op_sel_hi:[1,0,1]
	v_fmac_f32_e32 v2, v6, v6
	v_fmac_f32_e32 v3, v8, v8
	v_add_f32_e32 v2, v2, v3
	v_mul_f32_e32 v3, v19, v19
	v_mul_f32_e32 v4, v17, v17
	v_fmac_f32_e32 v3, v18, v18
	v_fmac_f32_e32 v4, v16, v16
	v_add_f32_e32 v3, v3, v4
	v_add_f32_e32 v2, v2, v3
	v_add_f32_e32 v20, v26, v2
	v_cvt_pk_bf16_f32 v2, v6, v7
	v_cvt_pk_bf16_f32 v3, v8, v9
	v_cvt_pk_bf16_f32 v4, v18, v19
	v_med3_f32 v6, v6, s69, v163
	v_med3_f32 v21, v18, s69, v163
	v_med3_f32 v7, v7, s69, v163
	v_med3_f32 v22, v19, s69, v163
	v_mov_b32_e32 v18, v139
	v_mov_b32_e32 v19, v139
	v_cvt_pk_fp8_f32 v18, v6, v7
	v_cvt_pk_fp8_f32 v19, v21, v22
	v_cvt_pk_bf16_f32 v5, v16, v17
	s_add_u32 s41, s55, s72
	ds_write_b128 v169, v[10:13]
	ds_write_b128 v169, v[2:5] offset:64
	s_addc_u32 s47, s56, s73
	ds_read_b128 v[2:5], v168
	v_med3_f32 v8, v8, s69, v163
	v_med3_f32 v16, v16, s69, v163
	v_med3_f32 v6, v9, s69, v163
	v_med3_f32 v7, v17, s69, v163
	s_add_u32 s50, s41, s50
	v_cvt_pk_fp8_f32 v18, v8, v6 op_sel:[0,0,1]
	v_cvt_pk_fp8_f32 v19, v16, v7 op_sel:[0,0,1]
	s_addc_u32 s51, s47, s51
	ds_read_b128 v[6:9], v168 offset:1152
	v_lshl_add_u64 v[10:11], s[50:51], 0, v[138:139]
	v_lshl_add_u64 v[10:11], v[10:11], 0, v[144:145]
	s_waitcnt lgkmcnt(1)
	global_store_dwordx4 v[10:11], v[2:5], off nt
	ds_write2_b64 v170, v[14:15], v[18:19] offset1:4
	v_lshlrev_b32_e32 v10, 2, v164
	v_lshl_add_u64 v[2:3], s[50:51], 0, v[146:147]
	s_lshl_b64 s[50:51], s[70:71], 10
	v_lshl_add_u64 v[2:3], v[2:3], 0, v[144:145]
	s_add_u32 s41, s60, s50
	s_waitcnt lgkmcnt(1)
	global_store_dwordx4 v[2:3], v[6:9], off nt
	s_addc_u32 s47, s61, s51
	ds_read_b128 v[2:5], v171
	s_add_u32 s48, s41, s48
	s_addc_u32 s49, s47, s49
	v_lshl_add_u64 v[6:7], s[48:49], 0, v[116:117]
	v_lshl_add_u64 v[6:7], v[6:7], 0, v[114:115]
	s_waitcnt lgkmcnt(0)
	global_store_dwordx4 v[6:7], v[2:5], off nt
	s_lshl_b32 s14, s14, 2
	s_or_b32 s48, s39, s14
	v_lshlrev_b32_e32 v2, 2, v167
	v_lshlrev_b32_e32 v3, 4, v166
	v_add3_u32 v2, s9, v2, v3
	ds_write2st64_b32 v2, v34, v43 offset1:1
	ds_write2st64_b32 v2, v42, v33 offset0:2 offset1:3
	ds_write2st64_b32 v2, v32, v31 offset0:4 offset1:5
	ds_write2st64_b32 v2, v30, v20 offset0:6 offset1:7
	v_add_u32_e32 v6, s9, v165
	s_ashr_i32 s49, s48, 31
	s_ashr_i32 s47, s46, 31
	s_ashr_i32 s9, s8, 31
	s_lshl_b64 s[48:49], s[48:49], 18
	ds_read_b128 v[2:5], v6
	s_add_u32 s14, s58, s48
	s_addc_u32 s39, s59, s49
	s_lshl_b64 s[46:47], s[46:47], 2
	ds_read_b128 v[6:9], v6 offset:1024
	s_add_u32 s14, s14, s46
	s_addc_u32 s39, s39, s47
	s_lshl_b64 s[8:9], s[8:9], 2
	s_add_u32 s8, s14, s8
	s_waitcnt lgkmcnt(1)
	v_add_f32_e32 v2, v2, v3
	v_add_f32_e32 v3, v4, v5
	s_addc_u32 s9, s39, s9
	v_add_f32_e32 v2, v2, v3
	global_store_dword v10, v2, s[8:9]
	s_waitcnt lgkmcnt(0)
	v_add_f32_e32 v2, v6, v7
	v_add_f32_e32 v3, v8, v9
	v_add_f32_e32 v2, v2, v3
	global_store_dword v10, v2, s[8:9] offset:512
	s_and_b64 vcc, exec, s[10:11]
	s_mov_b64 s[8:9], -1
	s_cbranch_vccnz .LBB0_2291
	v_mov_b32_e32 v2, v0
	s_andn2_b64 vcc, exec, s[12:13]
	s_cbranch_vccnz .LBB0_2290
	s_barrier
	s_branch .LBB0_2290

.LBB0_3582:
	v_mov_b32_e32 v178, v0
	s_lshl_b32 s41, s70, 8
	v_readfirstlane_b32 s8, v178
	s_ashr_i32 s39, s8, 6
	s_mul_i32 s9, s39, 0xb00
	s_and_b32 s39, s39, 3
	s_lshl_b32 s47, s39, 6
	s_ashr_i32 s8, s8, 8
	s_or_b32 s48, s47, s41
	s_lshl_b32 s41, s46, 2
	s_add_i32 s50, s41, s70
	s_lshl_b32 s41, s8, 2
	s_or_b32 s58, s41, s39
	s_add_i32 s9, s9, 0
	s_ashr_i32 s51, s50, 31
	s_ashr_i32 s59, s58, 31
	s_add_i32 s9, s9, 0x20000
	s_lshl_b64 s[50:51], s[50:51], 16
	s_lshl_b64 s[58:59], s[58:59], 13
	s_add_u32 s41, s56, s50
	s_addc_u32 s47, s57, s51
	s_add_u32 s58, s41, s58
	s_addc_u32 s59, s47, s59
	s_lshl_b32 s46, s46, 8
	s_lshl_b32 s8, s8, 6
	s_add_i32 s50, s8, s46
	s_ashr_i32 s51, s50, 31
	s_ashr_i32 s49, s48, 31
	s_lshl_b64 s[60:61], s[50:51], 11
	s_add_u32 s41, s64, s60
	s_addc_u32 s47, s65, s61
	s_lshl_b64 s[48:49], s[48:49], 1
	v_and_b32_e32 v177, 63, v178
	s_add_u32 s62, s41, s48
	v_bfe_u32 v180, v178, 3, 3
	v_lshlrev_b32_e32 v154, 4, v177
	s_addc_u32 s63, s47, s49
	v_lshlrev_b32_e32 v166, 11, v180
	v_mov_b32_e32 v167, v155
	v_lshl_add_u64 v[160:161], s[62:63], 0, v[166:167]
	v_and_b32_e32 v164, 0x70, v154
	v_mov_b32_e32 v165, v155
	v_or_b32_e32 v168, 0x4000, v166
	v_mov_b32_e32 v169, v155
	v_lshl_add_u64 v[160:161], v[160:161], 0, v[164:165]
	v_lshl_add_u64 v[162:163], s[62:63], 0, v[168:169]
	global_load_dwordx4 v[170:173], v154, s[58:59]
	v_lshl_add_u64 v[174:175], v[162:163], 0, v[164:165]
	global_load_dwordx4 v[160:163], v[160:161], off
	s_nop 0
	global_load_dwordx4 v[182:185], v[174:175], off
	s_or_b32 s62, s50, 16
	v_pk_fma_f32 v[142:143], v[142:143], s[30:31], v[14:15] op_sel_hi:[1,0,1]
	s_ashr_i32 s63, s62, 31
	v_pk_mul_f32 v[142:143], v[142:143], s[34:35] op_sel_hi:[1,0]
	s_lshl_b64 s[62:63], s[62:63], 11
	v_pk_fma_f32 v[138:139], v[138:139], s[30:31], v[10:11] op_sel_hi:[1,0,1]
	v_exp_f32_e32 v142, v142
	v_exp_f32_e32 v143, v143
	s_add_u32 s41, s64, s62
	v_pk_mul_f32 v[138:139], v[138:139], s[34:35] op_sel_hi:[1,0]
	s_addc_u32 s47, s65, s63
	v_pk_fma_f32 v[144:145], v[144:145], s[30:31], v[16:17] op_sel_hi:[1,0,1]
	v_pk_fma_f32 v[140:141], v[140:141], s[30:31], v[12:13] op_sel_hi:[1,0,1]
	v_exp_f32_e32 v138, v138
	v_exp_f32_e32 v139, v139
	s_add_u32 s80, s41, s48
	v_pk_mul_f32 v[144:145], v[144:145], s[34:35] op_sel_hi:[1,0]
	v_pk_mul_f32 v[140:141], v[140:141], s[34:35] op_sel_hi:[1,0]
	v_and_b32_e32 v179, 15, v178
	s_addc_u32 s81, s47, s49
	v_and_b32_e32 v174, 48, v178
	v_exp_f32_e32 v194, v144
	v_exp_f32_e32 v195, v145
	v_exp_f32_e32 v196, v140
	v_exp_f32_e32 v197, v141
	v_mul_u32_u24_e32 v144, 0x90, v180
	v_mul_u32_u24_e32 v145, 0x90, v179
	v_pk_add_f32 v[140:141], v[142:143], 1.0 op_sel_hi:[1,0]
	v_lshl_add_u64 v[142:143], s[80:81], 0, v[166:167]
	v_add3_u32 v180, s9, v144, v164
	v_add3_u32 v181, s9, v145, v174
	v_lshl_add_u64 v[144:145], s[80:81], 0, v[168:169]
	v_lshl_add_u64 v[142:143], v[142:143], 0, v[164:165]
	v_pk_add_f32 v[198:199], v[138:139], 1.0 op_sel_hi:[1,0]
	v_rcp_f32_e32 v200, v140
	v_rcp_f32_e32 v201, v141
	global_load_dwordx4 v[138:141], v154, s[58:59] offset:1024
	v_lshl_add_u64 v[144:145], v[144:145], 0, v[164:165]
	global_load_dwordx4 v[186:189], v[142:143], off
	global_load_dwordx4 v[190:193], v[144:145], off
	v_pk_fma_f32 v[134:135], v[134:135], s[30:31], v[2:3] op_sel_hi:[1,0,1]
	s_waitcnt vmcnt(0)
	v_pk_fma_f32 v[130:131], v[130:131], s[30:31], v[6:7] op_sel_hi:[1,0,1]
	v_pk_mul_f32 v[134:135], v[134:135], s[34:35] op_sel_hi:[1,0]
	v_pk_fma_f32 v[132:133], v[132:133], s[30:31], v[8:9] op_sel_hi:[1,0,1]
	v_pk_fma_f32 v[136:137], v[136:137], s[30:31], v[4:5] op_sel_hi:[1,0,1]
	v_pk_mul_f32 v[130:131], v[130:131], s[34:35] op_sel_hi:[1,0]
	v_exp_f32_e32 v134, v134
	v_exp_f32_e32 v135, v135
	v_pk_mul_f32 v[132:133], v[132:133], s[34:35] op_sel_hi:[1,0]
	v_pk_mul_f32 v[136:137], v[136:137], s[34:35] op_sel_hi:[1,0]
	v_rcp_f32_e32 v198, v198
	v_rcp_f32_e32 v199, v199
	v_exp_f32_e32 v130, v130
	v_exp_f32_e32 v131, v131
	s_waitcnt vmcnt(0)
	ds_write_b128 v180, v[160:163]
	ds_write_b128 v180, v[182:185] offset:1152
	ds_read_b128 v[142:145], v181
	ds_read_b128 v[182:185], v181 offset:64
	v_cvt_pk_f32_fp8_e32 v[202:203], v170
	v_cvt_pk_f32_fp8_sdwa v[160:161], v170 src0_sel:WORD_1
	v_cvt_pk_f32_fp8_e32 v[162:163], v171
	s_waitcnt lgkmcnt(0)
	v_lshlrev_b32_e32 v206, 16, v144
	v_and_b32_e32 v207, 0xffff0000, v144
	v_lshlrev_b32_e32 v208, 16, v145
	v_and_b32_e32 v209, 0xffff0000, v145
	v_pk_add_f32 v[144:145], v[194:195], 1.0 op_sel_hi:[1,0]
	v_cvt_pk_f32_fp8_sdwa v[170:171], v171 src0_sel:WORD_1
	v_pk_add_f32 v[194:195], v[196:197], 1.0 op_sel_hi:[1,0]
	v_rcp_f32_e32 v144, v144
	v_rcp_f32_e32 v145, v145
	v_exp_f32_e32 v132, v132
	v_exp_f32_e32 v133, v133
	v_exp_f32_e32 v136, v136
	v_exp_f32_e32 v137, v137
	v_rcp_f32_e32 v194, v194
	v_rcp_f32_e32 v195, v195
	v_lshlrev_b32_e32 v204, 16, v142
	v_and_b32_e32 v205, 0xffff0000, v142
	v_lshlrev_b32_e32 v142, 16, v143
	v_and_b32_e32 v143, 0xffff0000, v143
	v_pk_mul_f32 v[196:197], v[202:203], s[36:37] op_sel_hi:[1,0]
	v_pk_mul_f32 v[160:161], v[160:161], s[36:37] op_sel_hi:[1,0]
	v_pk_mul_f32 v[162:163], v[162:163], s[36:37] op_sel_hi:[1,0]
	v_pk_add_f32 v[134:135], v[134:135], 1.0 op_sel_hi:[1,0]
	v_pk_mul_f32 v[170:171], v[170:171], s[36:37] op_sel_hi:[1,0]
	v_pk_fma_f32 v[142:143], v[144:145], v[160:161], v[142:143]
	v_pk_fma_f32 v[144:145], v[200:201], v[196:197], v[204:205]
	v_pk_fma_f32 v[162:163], v[198:199], v[162:163], v[206:207]
	v_cvt_pk_f32_fp8_e32 v[200:201], v172
	v_cvt_pk_f32_fp8_sdwa v[202:203], v172 src0_sel:WORD_1
	v_cvt_pk_f32_fp8_e32 v[204:205], v173
	v_cvt_pk_f32_fp8_sdwa v[172:173], v173 src0_sel:WORD_1
	v_pk_add_f32 v[130:131], v[130:131], 1.0 op_sel_hi:[1,0]
	v_rcp_f32_e32 v206, v134
	v_rcp_f32_e32 v207, v135
	v_pk_add_f32 v[132:133], v[132:133], 1.0 op_sel_hi:[1,0]
	v_pk_add_f32 v[134:135], v[136:137], 1.0 op_sel_hi:[1,0]
	v_pk_fma_f32 v[160:161], v[194:195], v[170:171], v[208:209]
	v_rcp_f32_e32 v130, v130
	v_rcp_f32_e32 v131, v131
	v_rcp_f32_e32 v132, v132
	v_rcp_f32_e32 v133, v133
	v_rcp_f32_e32 v208, v134
	v_rcp_f32_e32 v209, v135
	v_cvt_pk_bf16_f32 v194, v144, v145
	v_cvt_pk_bf16_f32 v195, v142, v143
	v_cvt_pk_bf16_f32 v196, v162, v163
	v_cvt_pk_bf16_f32 v197, v160, v161
	v_lshlrev_b32_e32 v170, 16, v182
	v_and_b32_e32 v171, 0xffff0000, v182
	v_lshlrev_b32_e32 v182, 16, v183
	v_and_b32_e32 v183, 0xffff0000, v183
	v_lshlrev_b32_e32 v198, 16, v184
	v_and_b32_e32 v199, 0xffff0000, v184
	v_lshlrev_b32_e32 v184, 16, v185
	v_and_b32_e32 v185, 0xffff0000, v185
	v_pk_mul_f32 v[136:137], v[200:201], s[36:37] op_sel_hi:[1,0]
	v_pk_mul_f32 v[134:135], v[202:203], s[36:37] op_sel_hi:[1,0]
	v_pk_mul_f32 v[200:201], v[204:205], s[36:37] op_sel_hi:[1,0]
	v_pk_mul_f32 v[172:173], v[172:173], s[36:37] op_sel_hi:[1,0]
	v_pk_fma_f32 v[134:135], v[132:133], v[134:135], v[182:183]
	v_pk_fma_f32 v[136:137], v[130:131], v[136:137], v[170:171]
	v_pk_fma_f32 v[170:171], v[208:209], v[172:173], v[184:185]
	v_pk_fma_f32 v[172:173], v[206:207], v[200:201], v[198:199]
	v_cvt_pk_bf16_f32 v130, v136, v137
	v_cvt_pk_bf16_f32 v131, v134, v135
	s_add_u32 s41, s66, s60
	v_cvt_pk_bf16_f32 v132, v172, v173
	v_cvt_pk_bf16_f32 v133, v170, v171
	ds_write_b128 v181, v[194:197]
	ds_write_b128 v181, v[130:133] offset:64
	s_addc_u32 s47, s67, s61
	ds_read_b128 v[130:133], v180
	ds_read_b128 v[182:185], v180 offset:1152
	s_add_u32 s60, s41, s48
	s_addc_u32 s61, s47, s49
	v_lshl_add_u64 v[194:195], s[60:61], 0, v[166:167]
	v_lshl_add_u64 v[194:195], v[194:195], 0, v[164:165]
	s_waitcnt lgkmcnt(1)
	global_store_dwordx4 v[194:195], v[130:133], off nt
	v_pk_fma_f32 v[122:123], v[122:123], s[30:31], v[14:15] op_sel_hi:[1,0,1]
	v_pk_fma_f32 v[126:127], v[126:127], s[30:31], v[10:11] op_sel_hi:[1,0,1]
	v_lshl_add_u64 v[130:131], s[60:61], 0, v[168:169]
	s_or_b32 s60, s50, 32
	s_ashr_i32 s61, s60, 31
	s_lshl_b64 s[60:61], s[60:61], 11
	s_add_u32 s41, s64, s60
	s_addc_u32 s47, s65, s61
	v_lshl_add_u64 v[130:131], v[130:131], 0, v[164:165]
	s_add_u32 s80, s41, s48
	s_waitcnt lgkmcnt(0)
	global_store_dwordx4 v[130:131], v[182:185], off nt
	s_addc_u32 s81, s47, s49
	v_lshl_add_u64 v[196:197], s[80:81], 0, v[168:169]
	v_lshl_add_u64 v[182:183], s[80:81], 0, v[166:167]
	global_load_dwordx4 v[130:133], v154, s[58:59] offset:2048
	v_lshl_add_u64 v[194:195], v[182:183], 0, v[164:165]
	ds_write_b128 v180, v[186:189]
	ds_write_b128 v180, v[190:193] offset:1152
	v_lshl_add_u64 v[190:191], v[196:197], 0, v[164:165]
	ds_read_b128 v[182:185], v181
	global_load_dwordx4 v[186:189], v[194:195], off
	s_nop 0
	global_load_dwordx4 v[190:193], v[190:191], off
	v_pk_mul_f32 v[122:123], v[122:123], s[34:35] op_sel_hi:[1,0]
	v_pk_fma_f32 v[124:125], v[124:125], s[30:31], v[16:17] op_sel_hi:[1,0,1]
	v_exp_f32_e32 v122, v122
	v_exp_f32_e32 v123, v123
	v_pk_mul_f32 v[126:127], v[126:127], s[34:35] op_sel_hi:[1,0]
	v_pk_fma_f32 v[128:129], v[128:129], s[30:31], v[12:13] op_sel_hi:[1,0,1]
	v_exp_f32_e32 v126, v126
	v_pk_add_f32 v[122:123], v[122:123], 1.0 op_sel_hi:[1,0]
	v_exp_f32_e32 v127, v127
	v_rcp_f32_e32 v208, v122
	v_rcp_f32_e32 v209, v123
	v_pk_mul_f32 v[122:123], v[124:125], s[34:35] op_sel_hi:[1,0]
	v_pk_mul_f32 v[124:125], v[128:129], s[34:35] op_sel_hi:[1,0]
	v_exp_f32_e32 v122, v122
	v_exp_f32_e32 v123, v123
	v_pk_fma_f32 v[118:119], v[118:119], s[30:31], v[2:3] op_sel_hi:[1,0,1]
	v_exp_f32_e32 v124, v124
	v_exp_f32_e32 v125, v125
	v_pk_fma_f32 v[114:115], v[114:115], s[30:31], v[6:7] op_sel_hi:[1,0,1]
	v_pk_mul_f32 v[118:119], v[118:119], s[34:35] op_sel_hi:[1,0]
	v_pk_fma_f32 v[116:117], v[116:117], s[30:31], v[8:9] op_sel_hi:[1,0,1]
	v_pk_fma_f32 v[120:121], v[120:121], s[30:31], v[4:5] op_sel_hi:[1,0,1]
	v_cvt_pk_f32_fp8_e32 v[202:203], v138
	v_cvt_pk_f32_fp8_sdwa v[204:205], v138 src0_sel:WORD_1
	v_cvt_pk_f32_fp8_e32 v[206:207], v139
	v_pk_add_f32 v[126:127], v[126:127], 1.0 op_sel_hi:[1,0]
	v_pk_add_f32 v[122:123], v[122:123], 1.0 op_sel_hi:[1,0]
	v_pk_mul_f32 v[114:115], v[114:115], s[34:35] op_sel_hi:[1,0]
	v_exp_f32_e32 v118, v118
	v_exp_f32_e32 v119, v119
	v_pk_mul_f32 v[116:117], v[116:117], s[34:35] op_sel_hi:[1,0]
	v_pk_mul_f32 v[120:121], v[120:121], s[34:35] op_sel_hi:[1,0]
	v_rcp_f32_e32 v128, v126
	v_rcp_f32_e32 v129, v127
	v_rcp_f32_e32 v122, v122
	v_rcp_f32_e32 v123, v123
	v_exp_f32_e32 v114, v114
	v_exp_f32_e32 v115, v115
	v_exp_f32_e32 v116, v116
	v_exp_f32_e32 v117, v117
	v_exp_f32_e32 v120, v120
	v_exp_f32_e32 v121, v121
	v_pk_add_f32 v[124:125], v[124:125], 1.0 op_sel_hi:[1,0]
	ds_read_b128 v[194:197], v181 offset:64
	s_waitcnt lgkmcnt(1)
	v_lshlrev_b32_e32 v198, 16, v182
	v_and_b32_e32 v199, 0xffff0000, v182
	v_lshlrev_b32_e32 v182, 16, v183
	v_and_b32_e32 v183, 0xffff0000, v183
	v_lshlrev_b32_e32 v200, 16, v184
	v_and_b32_e32 v201, 0xffff0000, v184
	v_cvt_pk_f32_fp8_sdwa v[138:139], v139 src0_sel:WORD_1
	v_rcp_f32_e32 v126, v124
	v_rcp_f32_e32 v127, v125
	v_pk_mul_f32 v[124:125], v[202:203], s[36:37] op_sel_hi:[1,0]
	v_pk_mul_f32 v[202:203], v[204:205], s[36:37] op_sel_hi:[1,0]
	v_pk_mul_f32 v[204:205], v[206:207], s[36:37] op_sel_hi:[1,0]
	v_pk_add_f32 v[118:119], v[118:119], 1.0 op_sel_hi:[1,0]
	v_pk_fma_f32 v[122:123], v[122:123], v[202:203], v[182:183]
	v_pk_fma_f32 v[128:129], v[128:129], v[204:205], v[200:201]
	v_cvt_pk_f32_fp8_e32 v[200:201], v140
	v_cvt_pk_f32_fp8_sdwa v[202:203], v140 src0_sel:WORD_1
	v_cvt_pk_f32_fp8_e32 v[204:205], v141
	v_cvt_pk_f32_fp8_sdwa v[140:141], v141 src0_sel:WORD_1
	v_pk_add_f32 v[114:115], v[114:115], 1.0 op_sel_hi:[1,0]
	v_rcp_f32_e32 v206, v118
	v_rcp_f32_e32 v207, v119
	v_pk_add_f32 v[116:117], v[116:117], 1.0 op_sel_hi:[1,0]
	v_pk_add_f32 v[118:119], v[120:121], 1.0 op_sel_hi:[1,0]
	v_pk_fma_f32 v[124:125], v[208:209], v[124:125], v[198:199]
	v_rcp_f32_e32 v114, v114
	v_rcp_f32_e32 v115, v115
	v_rcp_f32_e32 v116, v116
	v_rcp_f32_e32 v117, v117
	v_rcp_f32_e32 v208, v118
	v_rcp_f32_e32 v209, v119
	v_lshlrev_b32_e32 v184, 16, v185
	v_and_b32_e32 v185, 0xffff0000, v185
	v_pk_mul_f32 v[138:139], v[138:139], s[36:37] op_sel_hi:[1,0]
	v_cvt_pk_bf16_f32 v182, v124, v125
	v_cvt_pk_bf16_f32 v183, v122, v123
	s_waitcnt lgkmcnt(0)
	v_lshlrev_b32_e32 v198, 16, v196
	v_pk_fma_f32 v[126:127], v[126:127], v[138:139], v[184:185]
	v_cvt_pk_bf16_f32 v184, v128, v129
	v_lshlrev_b32_e32 v138, 16, v194
	v_cvt_pk_bf16_f32 v185, v126, v127
	v_and_b32_e32 v139, 0xffff0000, v194
	v_lshlrev_b32_e32 v194, 16, v195
	v_and_b32_e32 v195, 0xffff0000, v195
	v_and_b32_e32 v199, 0xffff0000, v196
	v_lshlrev_b32_e32 v196, 16, v197
	v_and_b32_e32 v197, 0xffff0000, v197
	v_pk_mul_f32 v[120:121], v[200:201], s[36:37] op_sel_hi:[1,0]
	v_pk_mul_f32 v[118:119], v[202:203], s[36:37] op_sel_hi:[1,0]
	v_pk_mul_f32 v[200:201], v[204:205], s[36:37] op_sel_hi:[1,0]
	v_pk_mul_f32 v[140:141], v[140:141], s[36:37] op_sel_hi:[1,0]
	v_pk_fma_f32 v[118:119], v[116:117], v[118:119], v[194:195]
	v_pk_fma_f32 v[120:121], v[114:115], v[120:121], v[138:139]
	v_pk_fma_f32 v[138:139], v[208:209], v[140:141], v[196:197]
	v_pk_fma_f32 v[140:141], v[206:207], v[200:201], v[198:199]
	v_cvt_pk_bf16_f32 v114, v120, v121
	v_cvt_pk_bf16_f32 v115, v118, v119
	s_add_u32 s41, s66, s62
	v_cvt_pk_bf16_f32 v116, v140, v141
	v_cvt_pk_bf16_f32 v117, v138, v139
	ds_write_b128 v181, v[182:185]
	ds_write_b128 v181, v[114:117] offset:64
	s_addc_u32 s47, s67, s63
	ds_read_b128 v[114:117], v180
	ds_read_b128 v[182:185], v180 offset:1152
	s_add_u32 s62, s41, s48
	s_addc_u32 s63, s47, s49
	v_lshl_add_u64 v[194:195], s[62:63], 0, v[166:167]
	v_lshl_add_u64 v[194:195], v[194:195], 0, v[164:165]
	s_waitcnt lgkmcnt(1)
	global_store_dwordx4 v[194:195], v[114:117], off nt
	v_lshl_add_u64 v[174:175], s[58:59], 0, v[154:155]
	v_pk_fma_f32 v[106:107], v[106:107], s[30:31], v[14:15] op_sel_hi:[1,0,1]
	v_lshl_add_u64 v[114:115], s[62:63], 0, v[168:169]
	v_lshl_add_u64 v[114:115], v[114:115], 0, v[164:165]
	s_waitcnt lgkmcnt(0)
	global_store_dwordx4 v[114:115], v[182:185], off nt
	global_load_dwordx4 v[114:117], v154, s[58:59] offset:3072
	s_or_b32 s58, s50, 48
	s_ashr_i32 s59, s58, 31
	s_lshl_b64 s[58:59], s[58:59], 11
	s_add_u32 s41, s64, s58
	s_addc_u32 s47, s65, s59
	s_add_u32 s62, s41, s48
	s_addc_u32 s63, s47, s49
	v_lshl_add_u64 v[182:183], s[62:63], 0, v[166:167]
	v_lshl_add_u64 v[196:197], s[62:63], 0, v[168:169]
	v_lshl_add_u64 v[194:195], v[182:183], 0, v[164:165]
	s_waitcnt vmcnt(4)
	ds_write_b128 v180, v[186:189]
	s_waitcnt vmcnt(3)
	ds_write_b128 v180, v[190:193] offset:1152
	v_lshl_add_u64 v[190:191], v[196:197], 0, v[164:165]
	ds_read_b128 v[182:185], v181
	global_load_dwordx4 v[186:189], v[194:195], off
	s_nop 0
	global_load_dwordx4 v[190:193], v[190:191], off
	v_pk_mul_f32 v[106:107], v[106:107], s[34:35] op_sel_hi:[1,0]
	v_pk_fma_f32 v[110:111], v[110:111], s[30:31], v[10:11] op_sel_hi:[1,0,1]
	v_exp_f32_e32 v106, v106
	v_exp_f32_e32 v107, v107
	v_pk_fma_f32 v[108:109], v[108:109], s[30:31], v[16:17] op_sel_hi:[1,0,1]
	v_pk_mul_f32 v[110:111], v[110:111], s[34:35] op_sel_hi:[1,0]
	v_pk_fma_f32 v[112:113], v[112:113], s[30:31], v[12:13] op_sel_hi:[1,0,1]
	v_pk_add_f32 v[106:107], v[106:107], 1.0 op_sel_hi:[1,0]
	v_exp_f32_e32 v110, v110
	v_rcp_f32_e32 v208, v106
	v_rcp_f32_e32 v209, v107
	v_pk_mul_f32 v[106:107], v[108:109], s[34:35] op_sel_hi:[1,0]
	v_exp_f32_e32 v111, v111
	v_exp_f32_e32 v106, v106
	v_exp_f32_e32 v107, v107
	v_pk_mul_f32 v[108:109], v[112:113], s[34:35] op_sel_hi:[1,0]
	v_pk_fma_f32 v[102:103], v[102:103], s[30:31], v[2:3] op_sel_hi:[1,0,1]
	v_exp_f32_e32 v108, v108
	v_exp_f32_e32 v109, v109
	v_pk_fma_f32 v[98:99], v[98:99], s[30:31], v[6:7] op_sel_hi:[1,0,1]
	v_pk_mul_f32 v[102:103], v[102:103], s[34:35] op_sel_hi:[1,0]
	v_pk_fma_f32 v[100:101], v[100:101], s[30:31], v[8:9] op_sel_hi:[1,0,1]
	v_pk_fma_f32 v[104:105], v[104:105], s[30:31], v[4:5] op_sel_hi:[1,0,1]
	v_cvt_pk_f32_fp8_e32 v[202:203], v130
	v_cvt_pk_f32_fp8_sdwa v[204:205], v130 src0_sel:WORD_1
	v_cvt_pk_f32_fp8_e32 v[206:207], v131
	v_pk_add_f32 v[110:111], v[110:111], 1.0 op_sel_hi:[1,0]
	v_pk_add_f32 v[106:107], v[106:107], 1.0 op_sel_hi:[1,0]
	v_pk_mul_f32 v[98:99], v[98:99], s[34:35] op_sel_hi:[1,0]
	v_exp_f32_e32 v102, v102
	v_exp_f32_e32 v103, v103
	v_pk_mul_f32 v[100:101], v[100:101], s[34:35] op_sel_hi:[1,0]
	v_pk_mul_f32 v[104:105], v[104:105], s[34:35] op_sel_hi:[1,0]
	v_rcp_f32_e32 v112, v110
	v_rcp_f32_e32 v113, v111
	v_rcp_f32_e32 v106, v106
	v_rcp_f32_e32 v107, v107
	v_exp_f32_e32 v98, v98
	v_exp_f32_e32 v99, v99
	v_exp_f32_e32 v100, v100
	v_exp_f32_e32 v101, v101
	v_exp_f32_e32 v104, v104
	v_exp_f32_e32 v105, v105
	v_pk_add_f32 v[108:109], v[108:109], 1.0 op_sel_hi:[1,0]
	ds_read_b128 v[194:197], v181 offset:64
	s_waitcnt lgkmcnt(1)
	v_lshlrev_b32_e32 v198, 16, v182
	v_and_b32_e32 v199, 0xffff0000, v182
	v_lshlrev_b32_e32 v182, 16, v183
	v_and_b32_e32 v183, 0xffff0000, v183
	v_lshlrev_b32_e32 v200, 16, v184
	v_and_b32_e32 v201, 0xffff0000, v184
	v_cvt_pk_f32_fp8_sdwa v[130:131], v131 src0_sel:WORD_1
	v_rcp_f32_e32 v110, v108
	v_rcp_f32_e32 v111, v109
	v_pk_mul_f32 v[108:109], v[202:203], s[36:37] op_sel_hi:[1,0]
	v_pk_mul_f32 v[202:203], v[204:205], s[36:37] op_sel_hi:[1,0]
	v_pk_mul_f32 v[204:205], v[206:207], s[36:37] op_sel_hi:[1,0]
	v_pk_add_f32 v[102:103], v[102:103], 1.0 op_sel_hi:[1,0]
	v_pk_fma_f32 v[106:107], v[106:107], v[202:203], v[182:183]
	v_pk_fma_f32 v[112:113], v[112:113], v[204:205], v[200:201]
	v_cvt_pk_f32_fp8_e32 v[200:201], v132
	v_cvt_pk_f32_fp8_sdwa v[202:203], v132 src0_sel:WORD_1
	v_cvt_pk_f32_fp8_e32 v[204:205], v133
	v_cvt_pk_f32_fp8_sdwa v[132:133], v133 src0_sel:WORD_1
	v_pk_add_f32 v[98:99], v[98:99], 1.0 op_sel_hi:[1,0]
	v_rcp_f32_e32 v206, v102
	v_rcp_f32_e32 v207, v103
	v_pk_add_f32 v[100:101], v[100:101], 1.0 op_sel_hi:[1,0]
	v_pk_add_f32 v[102:103], v[104:105], 1.0 op_sel_hi:[1,0]
	v_pk_fma_f32 v[108:109], v[208:209], v[108:109], v[198:199]
	v_rcp_f32_e32 v98, v98
	v_rcp_f32_e32 v99, v99
	v_rcp_f32_e32 v100, v100
	v_rcp_f32_e32 v101, v101
	v_rcp_f32_e32 v208, v102
	v_rcp_f32_e32 v209, v103
	v_lshlrev_b32_e32 v184, 16, v185
	v_and_b32_e32 v185, 0xffff0000, v185
	v_pk_mul_f32 v[130:131], v[130:131], s[36:37] op_sel_hi:[1,0]
	v_cvt_pk_bf16_f32 v182, v108, v109
	v_cvt_pk_bf16_f32 v183, v106, v107
	s_waitcnt lgkmcnt(0)
	v_lshlrev_b32_e32 v198, 16, v196
	v_pk_fma_f32 v[110:111], v[110:111], v[130:131], v[184:185]
	v_cvt_pk_bf16_f32 v184, v112, v113
	v_lshlrev_b32_e32 v130, 16, v194
	v_cvt_pk_bf16_f32 v185, v110, v111
	v_and_b32_e32 v131, 0xffff0000, v194
	v_lshlrev_b32_e32 v194, 16, v195
	v_and_b32_e32 v195, 0xffff0000, v195
	v_and_b32_e32 v199, 0xffff0000, v196
	v_lshlrev_b32_e32 v196, 16, v197
	v_and_b32_e32 v197, 0xffff0000, v197
	v_pk_mul_f32 v[104:105], v[200:201], s[36:37] op_sel_hi:[1,0]
	v_pk_mul_f32 v[102:103], v[202:203], s[36:37] op_sel_hi:[1,0]
	v_pk_mul_f32 v[200:201], v[204:205], s[36:37] op_sel_hi:[1,0]
	v_pk_mul_f32 v[132:133], v[132:133], s[36:37] op_sel_hi:[1,0]
	v_pk_fma_f32 v[102:103], v[100:101], v[102:103], v[194:195]
	v_pk_fma_f32 v[104:105], v[98:99], v[104:105], v[130:131]
	v_pk_fma_f32 v[130:131], v[208:209], v[132:133], v[196:197]
	v_pk_fma_f32 v[132:133], v[206:207], v[200:201], v[198:199]
	v_cvt_pk_bf16_f32 v98, v104, v105
	v_cvt_pk_bf16_f32 v99, v102, v103
	s_add_u32 s41, s66, s60
	v_cvt_pk_bf16_f32 v100, v132, v133
	v_cvt_pk_bf16_f32 v101, v130, v131
	ds_write_b128 v181, v[182:185]
	ds_write_b128 v181, v[98:101] offset:64
	s_addc_u32 s47, s67, s61
	ds_read_b128 v[98:101], v180
	ds_read_b128 v[182:185], v180 offset:1152
	s_add_u32 s60, s41, s48
	s_addc_u32 s61, s47, s49
	v_lshl_add_u64 v[194:195], s[60:61], 0, v[166:167]
	v_lshl_add_u64 v[194:195], v[194:195], 0, v[164:165]
	s_waitcnt lgkmcnt(1)
	global_store_dwordx4 v[194:195], v[98:101], off nt
	v_add_co_u32_e32 v174, vcc, s78, v174
	s_nop 0
	v_lshl_add_u64 v[98:99], s[60:61], 0, v[168:169]
	s_add_i32 s60, s50, 0x80
	s_ashr_i32 s61, s60, 31
	s_lshl_b64 s[60:61], s[60:61], 11
	s_add_u32 s41, s64, s60
	s_addc_u32 s47, s65, s61
	s_add_u32 s62, s41, s48
	v_lshl_add_u64 v[98:99], v[98:99], 0, v[164:165]
	s_addc_u32 s63, s47, s49
	s_waitcnt lgkmcnt(0)
	global_store_dwordx4 v[98:99], v[182:185], off nt
	v_lshl_add_u64 v[98:99], s[62:63], 0, v[166:167]
	v_addc_co_u32_e32 v175, vcc, 0, v175, vcc
	v_lshl_add_u64 v[182:183], v[98:99], 0, v[164:165]
	global_load_dwordx4 v[98:101], v[174:175], off
	s_nop 0
	global_load_dwordx4 v[182:185], v[182:183], off
	s_waitcnt vmcnt(5)
	ds_write_b128 v180, v[186:189]
	s_waitcnt vmcnt(4)
	ds_write_b128 v180, v[190:193] offset:1152
	v_lshl_add_u64 v[190:191], s[62:63], 0, v[168:169]
	v_lshl_add_u64 v[190:191], v[190:191], 0, v[164:165]
	global_load_dwordx4 v[190:193], v[190:191], off
	v_pk_fma_f32 v[90:91], v[90:91], s[30:31], v[14:15] op_sel_hi:[1,0,1]
	v_pk_fma_f32 v[94:95], v[94:95], s[30:31], v[10:11] op_sel_hi:[1,0,1]
	v_pk_mul_f32 v[90:91], v[90:91], s[34:35] op_sel_hi:[1,0]
	v_pk_fma_f32 v[92:93], v[92:93], s[30:31], v[16:17] op_sel_hi:[1,0,1]
	v_exp_f32_e32 v90, v90
	v_exp_f32_e32 v91, v91
	v_pk_mul_f32 v[94:95], v[94:95], s[34:35] op_sel_hi:[1,0]
	v_pk_fma_f32 v[96:97], v[96:97], s[30:31], v[12:13] op_sel_hi:[1,0,1]
	v_exp_f32_e32 v94, v94
	v_pk_add_f32 v[90:91], v[90:91], 1.0 op_sel_hi:[1,0]
	v_exp_f32_e32 v95, v95
	v_rcp_f32_e32 v208, v90
	v_rcp_f32_e32 v209, v91
	v_pk_mul_f32 v[90:91], v[92:93], s[34:35] op_sel_hi:[1,0]
	v_pk_mul_f32 v[92:93], v[96:97], s[34:35] op_sel_hi:[1,0]
	v_exp_f32_e32 v90, v90
	v_exp_f32_e32 v91, v91
	v_pk_fma_f32 v[86:87], v[86:87], s[30:31], v[2:3] op_sel_hi:[1,0,1]
	ds_read_b128 v[186:189], v181
	ds_read_b128 v[194:197], v181 offset:64
	v_exp_f32_e32 v92, v92
	v_exp_f32_e32 v93, v93
	v_pk_fma_f32 v[82:83], v[82:83], s[30:31], v[6:7] op_sel_hi:[1,0,1]
	v_pk_mul_f32 v[86:87], v[86:87], s[34:35] op_sel_hi:[1,0]
	v_pk_fma_f32 v[84:85], v[84:85], s[30:31], v[8:9] op_sel_hi:[1,0,1]
	v_pk_fma_f32 v[88:89], v[88:89], s[30:31], v[4:5] op_sel_hi:[1,0,1]
	v_cvt_pk_f32_fp8_e32 v[202:203], v114
	v_cvt_pk_f32_fp8_sdwa v[204:205], v114 src0_sel:WORD_1
	v_cvt_pk_f32_fp8_e32 v[206:207], v115
	v_pk_add_f32 v[94:95], v[94:95], 1.0 op_sel_hi:[1,0]
	v_pk_add_f32 v[90:91], v[90:91], 1.0 op_sel_hi:[1,0]
	v_pk_mul_f32 v[82:83], v[82:83], s[34:35] op_sel_hi:[1,0]
	v_exp_f32_e32 v86, v86
	v_exp_f32_e32 v87, v87
	v_pk_mul_f32 v[84:85], v[84:85], s[34:35] op_sel_hi:[1,0]
	v_pk_mul_f32 v[88:89], v[88:89], s[34:35] op_sel_hi:[1,0]
	v_rcp_f32_e32 v96, v94
	v_rcp_f32_e32 v97, v95
	v_rcp_f32_e32 v90, v90
	v_rcp_f32_e32 v91, v91
	v_exp_f32_e32 v82, v82
	v_exp_f32_e32 v83, v83
	v_exp_f32_e32 v84, v84
	v_exp_f32_e32 v85, v85
	v_exp_f32_e32 v88, v88
	v_exp_f32_e32 v89, v89
	v_pk_add_f32 v[92:93], v[92:93], 1.0 op_sel_hi:[1,0]
	s_waitcnt lgkmcnt(1)
	v_lshlrev_b32_e32 v198, 16, v186
	v_and_b32_e32 v199, 0xffff0000, v186
	v_lshlrev_b32_e32 v186, 16, v187
	v_and_b32_e32 v187, 0xffff0000, v187
	v_lshlrev_b32_e32 v200, 16, v188
	v_and_b32_e32 v201, 0xffff0000, v188
	v_cvt_pk_f32_fp8_sdwa v[114:115], v115 src0_sel:WORD_1
	v_rcp_f32_e32 v94, v92
	v_rcp_f32_e32 v95, v93
	v_pk_mul_f32 v[92:93], v[202:203], s[36:37] op_sel_hi:[1,0]
	v_pk_mul_f32 v[202:203], v[204:205], s[36:37] op_sel_hi:[1,0]
	v_pk_mul_f32 v[204:205], v[206:207], s[36:37] op_sel_hi:[1,0]
	v_pk_add_f32 v[86:87], v[86:87], 1.0 op_sel_hi:[1,0]
	v_pk_fma_f32 v[90:91], v[90:91], v[202:203], v[186:187]
	v_pk_fma_f32 v[96:97], v[96:97], v[204:205], v[200:201]
	v_cvt_pk_f32_fp8_e32 v[200:201], v116
	v_cvt_pk_f32_fp8_sdwa v[202:203], v116 src0_sel:WORD_1
	v_cvt_pk_f32_fp8_e32 v[204:205], v117
	v_cvt_pk_f32_fp8_sdwa v[116:117], v117 src0_sel:WORD_1
	v_pk_add_f32 v[82:83], v[82:83], 1.0 op_sel_hi:[1,0]
	v_rcp_f32_e32 v206, v86
	v_rcp_f32_e32 v207, v87
	v_pk_add_f32 v[84:85], v[84:85], 1.0 op_sel_hi:[1,0]
	v_pk_add_f32 v[86:87], v[88:89], 1.0 op_sel_hi:[1,0]
	v_pk_fma_f32 v[92:93], v[208:209], v[92:93], v[198:199]
	v_rcp_f32_e32 v82, v82
	v_rcp_f32_e32 v83, v83
	v_rcp_f32_e32 v84, v84
	v_rcp_f32_e32 v85, v85
	v_rcp_f32_e32 v208, v86
	v_rcp_f32_e32 v209, v87
	v_lshlrev_b32_e32 v188, 16, v189
	v_and_b32_e32 v189, 0xffff0000, v189
	v_pk_mul_f32 v[114:115], v[114:115], s[36:37] op_sel_hi:[1,0]
	v_cvt_pk_bf16_f32 v186, v92, v93
	v_cvt_pk_bf16_f32 v187, v90, v91
	s_waitcnt lgkmcnt(0)
	v_lshlrev_b32_e32 v198, 16, v196
	v_pk_fma_f32 v[94:95], v[94:95], v[114:115], v[188:189]
	v_cvt_pk_bf16_f32 v188, v96, v97
	v_lshlrev_b32_e32 v114, 16, v194
	v_cvt_pk_bf16_f32 v189, v94, v95
	v_and_b32_e32 v115, 0xffff0000, v194
	v_lshlrev_b32_e32 v194, 16, v195
	v_and_b32_e32 v195, 0xffff0000, v195
	v_and_b32_e32 v199, 0xffff0000, v196
	v_lshlrev_b32_e32 v196, 16, v197
	v_and_b32_e32 v197, 0xffff0000, v197
	v_pk_mul_f32 v[88:89], v[200:201], s[36:37] op_sel_hi:[1,0]
	v_pk_mul_f32 v[86:87], v[202:203], s[36:37] op_sel_hi:[1,0]
	v_pk_mul_f32 v[200:201], v[204:205], s[36:37] op_sel_hi:[1,0]
	v_pk_mul_f32 v[116:117], v[116:117], s[36:37] op_sel_hi:[1,0]
	v_pk_fma_f32 v[86:87], v[84:85], v[86:87], v[194:195]
	v_pk_fma_f32 v[88:89], v[82:83], v[88:89], v[114:115]
	v_pk_fma_f32 v[114:115], v[208:209], v[116:117], v[196:197]
	v_pk_fma_f32 v[116:117], v[206:207], v[200:201], v[198:199]
	v_cvt_pk_bf16_f32 v82, v88, v89
	v_cvt_pk_bf16_f32 v83, v86, v87
	s_add_u32 s41, s66, s58
	v_cvt_pk_bf16_f32 v84, v116, v117
	v_cvt_pk_bf16_f32 v85, v114, v115
	ds_write_b128 v181, v[186:189]
	ds_write_b128 v181, v[82:85] offset:64
	s_addc_u32 s47, s67, s59
	ds_read_b128 v[82:85], v180
	ds_read_b128 v[186:189], v180 offset:1152
	s_add_u32 s58, s41, s48
	s_addc_u32 s59, s47, s49
	v_lshl_add_u64 v[194:195], s[58:59], 0, v[166:167]
	v_lshl_add_u64 v[194:195], v[194:195], 0, v[164:165]
	s_waitcnt lgkmcnt(1)
	global_store_dwordx4 v[194:195], v[82:85], off nt
	v_pk_fma_f32 v[74:75], v[74:75], s[30:31], v[14:15] op_sel_hi:[1,0,1]
	v_pk_fma_f32 v[78:79], v[78:79], s[30:31], v[10:11] op_sel_hi:[1,0,1]
	v_lshl_add_u64 v[82:83], s[58:59], 0, v[168:169]
	s_add_i32 s58, s50, 0x90
	s_ashr_i32 s59, s58, 31
	s_lshl_b64 s[58:59], s[58:59], 11
	s_add_u32 s41, s64, s58
	s_addc_u32 s47, s65, s59
	s_add_u32 s62, s41, s48
	v_lshl_add_u64 v[82:83], v[82:83], 0, v[164:165]
	s_addc_u32 s63, s47, s49
	s_waitcnt lgkmcnt(0)
	global_store_dwordx4 v[82:83], v[186:189], off nt
	v_lshl_add_u64 v[82:83], s[62:63], 0, v[166:167]
	v_pk_fma_f32 v[76:77], v[76:77], s[30:31], v[16:17] op_sel_hi:[1,0,1]
	v_lshl_add_u64 v[186:187], v[82:83], 0, v[164:165]
	global_load_dwordx4 v[82:85], v[174:175], off offset:1024
	s_nop 0
	global_load_dwordx4 v[186:189], v[186:187], off
	s_waitcnt vmcnt(5)
	ds_write_b128 v180, v[182:185]
	s_waitcnt vmcnt(4)
	ds_write_b128 v180, v[190:193] offset:1152
	v_lshl_add_u64 v[190:191], s[62:63], 0, v[168:169]
	v_lshl_add_u64 v[190:191], v[190:191], 0, v[164:165]
	global_load_dwordx4 v[190:193], v[190:191], off
	v_pk_mul_f32 v[74:75], v[74:75], s[34:35] op_sel_hi:[1,0]
	v_pk_mul_f32 v[78:79], v[78:79], s[34:35] op_sel_hi:[1,0]
	v_pk_mul_f32 v[76:77], v[76:77], s[34:35] op_sel_hi:[1,0]
	v_exp_f32_e32 v74, v74
	v_exp_f32_e32 v75, v75
	v_exp_f32_e32 v78, v78
	v_exp_f32_e32 v79, v79
	v_exp_f32_e32 v76, v76
	v_exp_f32_e32 v77, v77
	v_pk_fma_f32 v[80:81], v[80:81], s[30:31], v[12:13] op_sel_hi:[1,0,1]
	v_pk_fma_f32 v[70:71], v[70:71], s[30:31], v[2:3] op_sel_hi:[1,0,1]
	ds_read_b128 v[182:185], v181
	ds_read_b128 v[194:197], v181 offset:64
	v_pk_mul_f32 v[80:81], v[80:81], s[34:35] op_sel_hi:[1,0]
	v_pk_fma_f32 v[66:67], v[66:67], s[30:31], v[6:7] op_sel_hi:[1,0,1]
	v_pk_mul_f32 v[70:71], v[70:71], s[34:35] op_sel_hi:[1,0]
	v_pk_fma_f32 v[68:69], v[68:69], s[30:31], v[8:9] op_sel_hi:[1,0,1]
	v_pk_fma_f32 v[72:73], v[72:73], s[30:31], v[4:5] op_sel_hi:[1,0,1]
	v_cvt_pk_f32_fp8_e32 v[202:203], v98
	v_cvt_pk_f32_fp8_sdwa v[204:205], v98 src0_sel:WORD_1
	v_cvt_pk_f32_fp8_e32 v[206:207], v99
	v_pk_add_f32 v[74:75], v[74:75], 1.0 op_sel_hi:[1,0]
	v_pk_add_f32 v[78:79], v[78:79], 1.0 op_sel_hi:[1,0]
	v_exp_f32_e32 v80, v80
	v_exp_f32_e32 v81, v81
	v_pk_add_f32 v[76:77], v[76:77], 1.0 op_sel_hi:[1,0]
	v_pk_mul_f32 v[66:67], v[66:67], s[34:35] op_sel_hi:[1,0]
	v_exp_f32_e32 v70, v70
	v_exp_f32_e32 v71, v71
	v_pk_mul_f32 v[68:69], v[68:69], s[34:35] op_sel_hi:[1,0]
	v_pk_mul_f32 v[72:73], v[72:73], s[34:35] op_sel_hi:[1,0]
	v_rcp_f32_e32 v74, v74
	v_rcp_f32_e32 v75, v75
	v_rcp_f32_e32 v78, v78
	v_rcp_f32_e32 v79, v79
	v_rcp_f32_e32 v76, v76
	v_rcp_f32_e32 v77, v77
	v_exp_f32_e32 v66, v66
	v_exp_f32_e32 v67, v67
	v_exp_f32_e32 v68, v68
	v_exp_f32_e32 v69, v69
	v_exp_f32_e32 v72, v72
	v_exp_f32_e32 v73, v73
	s_waitcnt lgkmcnt(1)
	v_lshlrev_b32_e32 v198, 16, v182
	v_and_b32_e32 v199, 0xffff0000, v182
	v_lshlrev_b32_e32 v182, 16, v183
	v_and_b32_e32 v183, 0xffff0000, v183
	v_lshlrev_b32_e32 v200, 16, v184
	v_and_b32_e32 v201, 0xffff0000, v184
	v_cvt_pk_f32_fp8_sdwa v[98:99], v99 src0_sel:WORD_1
	v_pk_add_f32 v[80:81], v[80:81], 1.0 op_sel_hi:[1,0]
	v_pk_mul_f32 v[204:205], v[204:205], s[36:37] op_sel_hi:[1,0]
	v_pk_mul_f32 v[202:203], v[202:203], s[36:37] op_sel_hi:[1,0]
	v_pk_mul_f32 v[206:207], v[206:207], s[36:37] op_sel_hi:[1,0]
	v_pk_add_f32 v[70:71], v[70:71], 1.0 op_sel_hi:[1,0]
	v_rcp_f32_e32 v80, v80
	v_rcp_f32_e32 v81, v81
	v_pk_fma_f32 v[74:75], v[74:75], v[202:203], v[198:199]
	v_pk_fma_f32 v[76:77], v[76:77], v[204:205], v[182:183]
	v_pk_fma_f32 v[78:79], v[78:79], v[206:207], v[200:201]
	v_cvt_pk_f32_fp8_e32 v[200:201], v100
	v_cvt_pk_f32_fp8_sdwa v[202:203], v100 src0_sel:WORD_1
	v_cvt_pk_f32_fp8_e32 v[204:205], v101
	v_cvt_pk_f32_fp8_sdwa v[100:101], v101 src0_sel:WORD_1
	v_pk_add_f32 v[66:67], v[66:67], 1.0 op_sel_hi:[1,0]
	v_rcp_f32_e32 v206, v70
	v_rcp_f32_e32 v207, v71
	v_pk_add_f32 v[68:69], v[68:69], 1.0 op_sel_hi:[1,0]
	v_pk_add_f32 v[70:71], v[72:73], 1.0 op_sel_hi:[1,0]
	v_rcp_f32_e32 v66, v66
	v_rcp_f32_e32 v67, v67
	v_rcp_f32_e32 v68, v68
	v_rcp_f32_e32 v69, v69
	v_rcp_f32_e32 v208, v70
	v_rcp_f32_e32 v209, v71
	v_lshlrev_b32_e32 v184, 16, v185
	v_and_b32_e32 v185, 0xffff0000, v185
	v_pk_mul_f32 v[98:99], v[98:99], s[36:37] op_sel_hi:[1,0]
	v_cvt_pk_bf16_f32 v182, v74, v75
	v_cvt_pk_bf16_f32 v183, v76, v77
	s_waitcnt lgkmcnt(0)
	v_lshlrev_b32_e32 v198, 16, v196
	v_pk_fma_f32 v[80:81], v[80:81], v[98:99], v[184:185]
	v_cvt_pk_bf16_f32 v184, v78, v79
	v_lshlrev_b32_e32 v98, 16, v194
	v_cvt_pk_bf16_f32 v185, v80, v81
	v_and_b32_e32 v99, 0xffff0000, v194
	v_lshlrev_b32_e32 v194, 16, v195
	v_and_b32_e32 v195, 0xffff0000, v195
	v_and_b32_e32 v199, 0xffff0000, v196
	v_lshlrev_b32_e32 v196, 16, v197
	v_and_b32_e32 v197, 0xffff0000, v197
	v_pk_mul_f32 v[72:73], v[202:203], s[36:37] op_sel_hi:[1,0]
	v_pk_mul_f32 v[70:71], v[200:201], s[36:37] op_sel_hi:[1,0]
	v_pk_mul_f32 v[100:101], v[100:101], s[36:37] op_sel_hi:[1,0]
	v_pk_mul_f32 v[200:201], v[204:205], s[36:37] op_sel_hi:[1,0]
	v_pk_fma_f32 v[70:71], v[66:67], v[70:71], v[98:99]
	v_pk_fma_f32 v[72:73], v[68:69], v[72:73], v[194:195]
	v_pk_fma_f32 v[98:99], v[206:207], v[200:201], v[198:199]
	v_pk_fma_f32 v[100:101], v[208:209], v[100:101], v[196:197]
	v_cvt_pk_bf16_f32 v66, v70, v71
	v_cvt_pk_bf16_f32 v67, v72, v73
	v_cvt_pk_bf16_f32 v68, v98, v99
	s_add_u32 s41, s66, s60
	v_cvt_pk_bf16_f32 v69, v100, v101
	ds_write_b128 v181, v[182:185]
	ds_write_b128 v181, v[66:69] offset:64
	s_addc_u32 s47, s67, s61
	ds_read_b128 v[66:69], v180
	ds_read_b128 v[182:185], v180 offset:1152
	s_add_u32 s60, s41, s48
	s_addc_u32 s61, s47, s49
	v_lshl_add_u64 v[194:195], s[60:61], 0, v[166:167]
	v_lshl_add_u64 v[194:195], v[194:195], 0, v[164:165]
	s_waitcnt lgkmcnt(1)
	global_store_dwordx4 v[194:195], v[66:69], off nt
	v_pk_fma_f32 v[58:59], v[58:59], s[30:31], v[14:15] op_sel_hi:[1,0,1]
	v_pk_fma_f32 v[62:63], v[62:63], s[30:31], v[10:11] op_sel_hi:[1,0,1]
	v_lshl_add_u64 v[66:67], s[60:61], 0, v[168:169]
	s_add_i32 s60, s50, 0xa0
	s_ashr_i32 s61, s60, 31
	s_lshl_b64 s[60:61], s[60:61], 11
	s_add_u32 s41, s64, s60
	s_addc_u32 s47, s65, s61
	s_add_u32 s62, s41, s48
	v_lshl_add_u64 v[66:67], v[66:67], 0, v[164:165]
	s_addc_u32 s63, s47, s49
	s_waitcnt lgkmcnt(0)
	global_store_dwordx4 v[66:67], v[182:185], off nt
	v_lshl_add_u64 v[66:67], s[62:63], 0, v[166:167]
	v_pk_fma_f32 v[60:61], v[60:61], s[30:31], v[16:17] op_sel_hi:[1,0,1]
	v_lshl_add_u64 v[182:183], v[66:67], 0, v[164:165]
	global_load_dwordx4 v[66:69], v[174:175], off offset:2048
	s_nop 0
	global_load_dwordx4 v[182:185], v[182:183], off
	s_waitcnt vmcnt(5)
	ds_write_b128 v180, v[186:189]
	s_waitcnt vmcnt(4)
	ds_write_b128 v180, v[190:193] offset:1152
	v_lshl_add_u64 v[190:191], s[62:63], 0, v[168:169]
	v_lshl_add_u64 v[190:191], v[190:191], 0, v[164:165]
	global_load_dwordx4 v[190:193], v[190:191], off
	v_pk_mul_f32 v[58:59], v[58:59], s[34:35] op_sel_hi:[1,0]
	v_pk_mul_f32 v[62:63], v[62:63], s[34:35] op_sel_hi:[1,0]
	v_pk_mul_f32 v[60:61], v[60:61], s[34:35] op_sel_hi:[1,0]
	v_exp_f32_e32 v58, v58
	v_exp_f32_e32 v59, v59
	v_exp_f32_e32 v62, v62
	v_exp_f32_e32 v63, v63
	v_exp_f32_e32 v60, v60
	v_exp_f32_e32 v61, v61
	v_pk_fma_f32 v[64:65], v[64:65], s[30:31], v[12:13] op_sel_hi:[1,0,1]
	v_pk_fma_f32 v[54:55], v[54:55], s[30:31], v[2:3] op_sel_hi:[1,0,1]
	ds_read_b128 v[186:189], v181
	ds_read_b128 v[194:197], v181 offset:64
	v_pk_mul_f32 v[64:65], v[64:65], s[34:35] op_sel_hi:[1,0]
	v_pk_fma_f32 v[50:51], v[50:51], s[30:31], v[6:7] op_sel_hi:[1,0,1]
	v_pk_mul_f32 v[54:55], v[54:55], s[34:35] op_sel_hi:[1,0]
	v_pk_fma_f32 v[52:53], v[52:53], s[30:31], v[8:9] op_sel_hi:[1,0,1]
	v_pk_fma_f32 v[56:57], v[56:57], s[30:31], v[4:5] op_sel_hi:[1,0,1]
	v_cvt_pk_f32_fp8_e32 v[202:203], v82
	v_cvt_pk_f32_fp8_sdwa v[204:205], v82 src0_sel:WORD_1
	v_cvt_pk_f32_fp8_e32 v[206:207], v83
	v_pk_add_f32 v[58:59], v[58:59], 1.0 op_sel_hi:[1,0]
	v_pk_add_f32 v[62:63], v[62:63], 1.0 op_sel_hi:[1,0]
	v_exp_f32_e32 v64, v64
	v_exp_f32_e32 v65, v65
	v_pk_add_f32 v[60:61], v[60:61], 1.0 op_sel_hi:[1,0]
	v_pk_mul_f32 v[50:51], v[50:51], s[34:35] op_sel_hi:[1,0]
	v_exp_f32_e32 v54, v54
	v_exp_f32_e32 v55, v55
	v_pk_mul_f32 v[52:53], v[52:53], s[34:35] op_sel_hi:[1,0]
	v_pk_mul_f32 v[56:57], v[56:57], s[34:35] op_sel_hi:[1,0]
	v_rcp_f32_e32 v58, v58
	v_rcp_f32_e32 v59, v59
	v_rcp_f32_e32 v62, v62
	v_rcp_f32_e32 v63, v63
	v_rcp_f32_e32 v60, v60
	v_rcp_f32_e32 v61, v61
	v_exp_f32_e32 v50, v50
	v_exp_f32_e32 v51, v51
	v_exp_f32_e32 v52, v52
	v_exp_f32_e32 v53, v53
	v_exp_f32_e32 v56, v56
	v_exp_f32_e32 v57, v57
	s_waitcnt lgkmcnt(1)
	v_lshlrev_b32_e32 v198, 16, v186
	v_and_b32_e32 v199, 0xffff0000, v186
	v_lshlrev_b32_e32 v186, 16, v187
	v_and_b32_e32 v187, 0xffff0000, v187
	v_lshlrev_b32_e32 v200, 16, v188
	v_and_b32_e32 v201, 0xffff0000, v188
	v_cvt_pk_f32_fp8_sdwa v[82:83], v83 src0_sel:WORD_1
	v_pk_add_f32 v[64:65], v[64:65], 1.0 op_sel_hi:[1,0]
	v_pk_mul_f32 v[204:205], v[204:205], s[36:37] op_sel_hi:[1,0]
	v_pk_mul_f32 v[202:203], v[202:203], s[36:37] op_sel_hi:[1,0]
	v_pk_mul_f32 v[206:207], v[206:207], s[36:37] op_sel_hi:[1,0]
	v_pk_add_f32 v[54:55], v[54:55], 1.0 op_sel_hi:[1,0]
	v_rcp_f32_e32 v64, v64
	v_rcp_f32_e32 v65, v65
	v_pk_fma_f32 v[58:59], v[58:59], v[202:203], v[198:199]
	v_pk_fma_f32 v[60:61], v[60:61], v[204:205], v[186:187]
	v_pk_fma_f32 v[62:63], v[62:63], v[206:207], v[200:201]
	v_cvt_pk_f32_fp8_e32 v[200:201], v84
	v_cvt_pk_f32_fp8_sdwa v[202:203], v84 src0_sel:WORD_1
	v_cvt_pk_f32_fp8_e32 v[204:205], v85
	v_cvt_pk_f32_fp8_sdwa v[84:85], v85 src0_sel:WORD_1
	v_pk_add_f32 v[50:51], v[50:51], 1.0 op_sel_hi:[1,0]
	v_rcp_f32_e32 v206, v54
	v_rcp_f32_e32 v207, v55
	v_pk_add_f32 v[52:53], v[52:53], 1.0 op_sel_hi:[1,0]
	v_pk_add_f32 v[54:55], v[56:57], 1.0 op_sel_hi:[1,0]
	v_rcp_f32_e32 v50, v50
	v_rcp_f32_e32 v51, v51
	v_rcp_f32_e32 v52, v52
	v_rcp_f32_e32 v53, v53
	v_rcp_f32_e32 v208, v54
	v_rcp_f32_e32 v209, v55
	v_lshlrev_b32_e32 v188, 16, v189
	v_and_b32_e32 v189, 0xffff0000, v189
	v_pk_mul_f32 v[82:83], v[82:83], s[36:37] op_sel_hi:[1,0]
	s_add_u32 s41, s66, s58
	v_pk_fma_f32 v[64:65], v[64:65], v[82:83], v[188:189]
	v_cvt_pk_bf16_f32 v186, v58, v59
	v_cvt_pk_bf16_f32 v187, v60, v61
	v_cvt_pk_bf16_f32 v188, v62, v63
	s_waitcnt lgkmcnt(0)
	v_lshlrev_b32_e32 v82, 16, v194
	v_cvt_pk_bf16_f32 v189, v64, v65
	v_and_b32_e32 v83, 0xffff0000, v194
	v_lshlrev_b32_e32 v194, 16, v195
	v_and_b32_e32 v195, 0xffff0000, v195
	v_lshlrev_b32_e32 v198, 16, v196
	v_and_b32_e32 v199, 0xffff0000, v196
	v_lshlrev_b32_e32 v196, 16, v197
	v_and_b32_e32 v197, 0xffff0000, v197
	v_pk_mul_f32 v[56:57], v[202:203], s[36:37] op_sel_hi:[1,0]
	v_pk_mul_f32 v[54:55], v[200:201], s[36:37] op_sel_hi:[1,0]
	v_pk_mul_f32 v[84:85], v[84:85], s[36:37] op_sel_hi:[1,0]
	v_pk_mul_f32 v[200:201], v[204:205], s[36:37] op_sel_hi:[1,0]
	s_addc_u32 s47, s67, s59
	v_pk_fma_f32 v[54:55], v[50:51], v[54:55], v[82:83]
	v_pk_fma_f32 v[56:57], v[52:53], v[56:57], v[194:195]
	v_pk_fma_f32 v[82:83], v[206:207], v[200:201], v[198:199]
	v_pk_fma_f32 v[84:85], v[208:209], v[84:85], v[196:197]
	v_cvt_pk_bf16_f32 v50, v54, v55
	v_cvt_pk_bf16_f32 v51, v56, v57
	v_cvt_pk_bf16_f32 v52, v82, v83
	s_add_u32 s58, s41, s48
	v_cvt_pk_bf16_f32 v53, v84, v85
	ds_write_b128 v181, v[186:189]
	ds_write_b128 v181, v[50:53] offset:64
	ds_read_b128 v[50:53], v180
	ds_read_b128 v[186:189], v180 offset:1152
	s_addc_u32 s59, s47, s49
	s_addk_i32 s50, 0xb0
	s_ashr_i32 s51, s50, 31
	s_lshl_b64 s[50:51], s[50:51], 11
	v_lshl_add_u64 v[194:195], s[58:59], 0, v[166:167]
	s_add_u32 s41, s64, s50
	v_lshl_add_u64 v[194:195], v[194:195], 0, v[164:165]
	s_addc_u32 s47, s65, s51
	s_waitcnt lgkmcnt(1)
	global_store_dwordx4 v[194:195], v[50:53], off nt
	v_pk_fma_f32 v[42:43], v[42:43], s[30:31], v[14:15] op_sel_hi:[1,0,1]
	v_pk_fma_f32 v[46:47], v[46:47], s[30:31], v[10:11] op_sel_hi:[1,0,1]
	v_lshl_add_u64 v[50:51], s[58:59], 0, v[168:169]
	s_add_u32 s58, s41, s48
	v_lshl_add_u64 v[50:51], v[50:51], 0, v[164:165]
	s_addc_u32 s59, s47, s49
	s_waitcnt lgkmcnt(0)
	global_store_dwordx4 v[50:51], v[186:189], off nt
	v_lshl_add_u64 v[50:51], s[58:59], 0, v[166:167]
	v_pk_fma_f32 v[44:45], v[44:45], s[30:31], v[16:17] op_sel_hi:[1,0,1]
	v_lshl_add_u64 v[186:187], v[50:51], 0, v[164:165]
	global_load_dwordx4 v[50:53], v[174:175], off offset:3072
	s_nop 0
	global_load_dwordx4 v[186:189], v[186:187], off
	v_lshl_add_u64 v[174:175], s[58:59], 0, v[168:169]
	s_waitcnt vmcnt(5)
	ds_write_b128 v180, v[182:185]
	s_waitcnt vmcnt(4)
	ds_write_b128 v180, v[190:193] offset:1152
	v_lshl_add_u64 v[174:175], v[174:175], 0, v[164:165]
	global_load_dwordx4 v[190:193], v[174:175], off
	v_pk_mul_f32 v[42:43], v[42:43], s[34:35] op_sel_hi:[1,0]
	v_pk_mul_f32 v[46:47], v[46:47], s[34:35] op_sel_hi:[1,0]
	v_pk_mul_f32 v[44:45], v[44:45], s[34:35] op_sel_hi:[1,0]
	v_exp_f32_e32 v42, v42
	v_exp_f32_e32 v43, v43
	v_exp_f32_e32 v46, v46
	v_exp_f32_e32 v47, v47
	v_exp_f32_e32 v44, v44
	v_exp_f32_e32 v45, v45
	v_pk_fma_f32 v[48:49], v[48:49], s[30:31], v[12:13] op_sel_hi:[1,0,1]
	ds_read_b128 v[182:185], v181
	ds_read_b128 v[194:197], v181 offset:64
	v_pk_mul_f32 v[48:49], v[48:49], s[34:35] op_sel_hi:[1,0]
	v_pk_fma_f32 v[34:35], v[34:35], s[30:31], v[6:7] op_sel_hi:[1,0,1]
	v_pk_fma_f32 v[38:39], v[38:39], s[30:31], v[2:3] op_sel_hi:[1,0,1]
	v_pk_fma_f32 v[36:37], v[36:37], s[30:31], v[8:9] op_sel_hi:[1,0,1]
	v_pk_fma_f32 v[40:41], v[40:41], s[30:31], v[4:5] op_sel_hi:[1,0,1]
	v_cvt_pk_f32_fp8_e32 v[200:201], v66
	v_cvt_pk_f32_fp8_sdwa v[202:203], v66 src0_sel:WORD_1
	v_cvt_pk_f32_fp8_e32 v[204:205], v67
	v_pk_add_f32 v[42:43], v[42:43], 1.0 op_sel_hi:[1,0]
	v_pk_add_f32 v[46:47], v[46:47], 1.0 op_sel_hi:[1,0]
	v_exp_f32_e32 v48, v48
	v_exp_f32_e32 v49, v49
	v_pk_add_f32 v[44:45], v[44:45], 1.0 op_sel_hi:[1,0]
	v_pk_mul_f32 v[34:35], v[34:35], s[34:35] op_sel_hi:[1,0]
	v_pk_mul_f32 v[38:39], v[38:39], s[34:35] op_sel_hi:[1,0]
	v_pk_mul_f32 v[36:37], v[36:37], s[34:35] op_sel_hi:[1,0]
	v_pk_mul_f32 v[40:41], v[40:41], s[34:35] op_sel_hi:[1,0]
	v_rcp_f32_e32 v42, v42
	v_rcp_f32_e32 v43, v43
	v_rcp_f32_e32 v46, v46
	v_rcp_f32_e32 v47, v47
	v_rcp_f32_e32 v44, v44
	v_rcp_f32_e32 v45, v45
	v_exp_f32_e32 v34, v34
	v_exp_f32_e32 v35, v35
	v_exp_f32_e32 v38, v38
	v_exp_f32_e32 v39, v39
	v_exp_f32_e32 v36, v36
	v_exp_f32_e32 v37, v37
	v_exp_f32_e32 v40, v40
	v_exp_f32_e32 v41, v41
	s_waitcnt lgkmcnt(1)
	v_lshlrev_b32_e32 v174, 16, v182
	v_and_b32_e32 v175, 0xffff0000, v182
	v_lshlrev_b32_e32 v182, 16, v183
	v_and_b32_e32 v183, 0xffff0000, v183
	v_lshlrev_b32_e32 v198, 16, v184
	v_and_b32_e32 v199, 0xffff0000, v184
	v_cvt_pk_f32_fp8_sdwa v[66:67], v67 src0_sel:WORD_1
	v_pk_add_f32 v[48:49], v[48:49], 1.0 op_sel_hi:[1,0]
	v_pk_mul_f32 v[202:203], v[202:203], s[36:37] op_sel_hi:[1,0]
	v_pk_mul_f32 v[200:201], v[200:201], s[36:37] op_sel_hi:[1,0]
	v_pk_mul_f32 v[204:205], v[204:205], s[36:37] op_sel_hi:[1,0]
	v_rcp_f32_e32 v48, v48
	v_rcp_f32_e32 v49, v49
	v_pk_fma_f32 v[42:43], v[42:43], v[200:201], v[174:175]
	v_pk_fma_f32 v[44:45], v[44:45], v[202:203], v[182:183]
	v_pk_fma_f32 v[46:47], v[46:47], v[204:205], v[198:199]
	v_cvt_pk_f32_fp8_e32 v[198:199], v68
	v_cvt_pk_f32_fp8_sdwa v[200:201], v68 src0_sel:WORD_1
	v_cvt_pk_f32_fp8_e32 v[202:203], v69
	v_cvt_pk_f32_fp8_sdwa v[68:69], v69 src0_sel:WORD_1
	v_pk_add_f32 v[34:35], v[34:35], 1.0 op_sel_hi:[1,0]
	v_pk_add_f32 v[38:39], v[38:39], 1.0 op_sel_hi:[1,0]
	v_pk_add_f32 v[36:37], v[36:37], 1.0 op_sel_hi:[1,0]
	v_pk_add_f32 v[40:41], v[40:41], 1.0 op_sel_hi:[1,0]
	v_rcp_f32_e32 v34, v34
	v_rcp_f32_e32 v35, v35
	v_rcp_f32_e32 v38, v38
	v_rcp_f32_e32 v39, v39
	v_rcp_f32_e32 v36, v36
	v_rcp_f32_e32 v37, v37
	v_rcp_f32_e32 v40, v40
	v_rcp_f32_e32 v41, v41
	v_lshlrev_b32_e32 v184, 16, v185
	v_and_b32_e32 v185, 0xffff0000, v185
	v_pk_mul_f32 v[66:67], v[66:67], s[36:37] op_sel_hi:[1,0]
	v_cvt_pk_bf16_f32 v182, v42, v43
	v_cvt_pk_bf16_f32 v183, v44, v45
	s_waitcnt lgkmcnt(0)
	v_lshlrev_b32_e32 v174, 16, v195
	v_pk_fma_f32 v[48:49], v[48:49], v[66:67], v[184:185]
	v_cvt_pk_bf16_f32 v184, v46, v47
	v_lshlrev_b32_e32 v66, 16, v194
	v_cvt_pk_bf16_f32 v185, v48, v49
	v_and_b32_e32 v67, 0xffff0000, v194
	v_and_b32_e32 v175, 0xffff0000, v195
	v_lshlrev_b32_e32 v194, 16, v196
	v_and_b32_e32 v195, 0xffff0000, v196
	v_lshlrev_b32_e32 v196, 16, v197
	v_and_b32_e32 v197, 0xffff0000, v197
	v_pk_mul_f32 v[200:201], v[200:201], s[36:37] op_sel_hi:[1,0]
	v_pk_mul_f32 v[198:199], v[198:199], s[36:37] op_sel_hi:[1,0]
	v_pk_mul_f32 v[68:69], v[68:69], s[36:37] op_sel_hi:[1,0]
	v_pk_mul_f32 v[202:203], v[202:203], s[36:37] op_sel_hi:[1,0]
	v_pk_fma_f32 v[34:35], v[34:35], v[198:199], v[66:67]
	v_pk_fma_f32 v[36:37], v[36:37], v[200:201], v[174:175]
	v_pk_fma_f32 v[38:39], v[38:39], v[202:203], v[194:195]
	v_pk_fma_f32 v[40:41], v[40:41], v[68:69], v[196:197]
	v_cvt_pk_bf16_f32 v66, v34, v35
	v_cvt_pk_bf16_f32 v67, v36, v37
	v_cvt_pk_bf16_f32 v68, v38, v39
	s_add_u32 s41, s66, s60
	v_cvt_pk_bf16_f32 v69, v40, v41
	ds_write_b128 v181, v[182:185]
	ds_write_b128 v181, v[66:69] offset:64
	s_addc_u32 s47, s67, s61
	ds_read_b128 v[66:69], v180
	ds_read_b128 v[182:185], v180 offset:1152
	s_add_u32 s58, s41, s48
	s_addc_u32 s59, s47, s49
	v_lshl_add_u64 v[174:175], s[58:59], 0, v[166:167]
	v_pk_fma_f32 v[14:15], v[26:27], s[30:31], v[14:15] op_sel_hi:[1,0,1]
	v_pk_fma_f32 v[10:11], v[30:31], s[30:31], v[10:11] op_sel_hi:[1,0,1]
	v_pk_fma_f32 v[16:17], v[28:29], s[30:31], v[16:17] op_sel_hi:[1,0,1]
	v_pk_fma_f32 v[12:13], v[32:33], s[30:31], v[12:13] op_sel_hi:[1,0,1]
	v_lshl_add_u64 v[174:175], v[174:175], 0, v[164:165]
	v_pk_mul_f32 v[14:15], v[14:15], s[34:35] op_sel_hi:[1,0]
	v_pk_mul_f32 v[10:11], v[10:11], s[34:35] op_sel_hi:[1,0]
	v_pk_mul_f32 v[16:17], v[16:17], s[34:35] op_sel_hi:[1,0]
	v_pk_mul_f32 v[12:13], v[12:13], s[34:35] op_sel_hi:[1,0]
	s_waitcnt lgkmcnt(1)
	global_store_dwordx4 v[174:175], v[66:69], off nt
	v_exp_f32_e32 v14, v14
	v_exp_f32_e32 v15, v15
	v_lshl_add_u64 v[66:67], s[58:59], 0, v[168:169]
	v_exp_f32_e32 v10, v10
	v_exp_f32_e32 v11, v11
	v_exp_f32_e32 v16, v16
	v_exp_f32_e32 v17, v17
	v_exp_f32_e32 v12, v12
	v_exp_f32_e32 v13, v13
	v_lshl_add_u64 v[66:67], v[66:67], 0, v[164:165]
	s_waitcnt lgkmcnt(0)
	global_store_dwordx4 v[66:67], v[182:185], off nt
	s_waitcnt vmcnt(3)
	ds_write_b128 v180, v[186:189]
	s_waitcnt vmcnt(2)
	ds_write_b128 v180, v[190:193] offset:1152
	v_pk_fma_f32 v[6:7], v[18:19], s[30:31], v[6:7] op_sel_hi:[1,0,1]
	v_pk_fma_f32 v[2:3], v[22:23], s[30:31], v[2:3] op_sel_hi:[1,0,1]
	v_pk_fma_f32 v[8:9], v[20:21], s[30:31], v[8:9] op_sel_hi:[1,0,1]
	v_pk_fma_f32 v[4:5], v[24:25], s[30:31], v[4:5] op_sel_hi:[1,0,1]
	ds_read_b128 v[66:69], v181
	ds_read_b128 v[182:185], v181 offset:64
	v_cvt_pk_f32_fp8_e32 v[188:189], v50
	v_cvt_pk_f32_fp8_sdwa v[190:191], v50 src0_sel:WORD_1
	v_cvt_pk_f32_fp8_e32 v[192:193], v51
	v_cvt_pk_f32_fp8_sdwa v[50:51], v51 src0_sel:WORD_1
	v_pk_add_f32 v[14:15], v[14:15], 1.0 op_sel_hi:[1,0]
	v_pk_add_f32 v[10:11], v[10:11], 1.0 op_sel_hi:[1,0]
	v_pk_add_f32 v[16:17], v[16:17], 1.0 op_sel_hi:[1,0]
	v_pk_add_f32 v[12:13], v[12:13], 1.0 op_sel_hi:[1,0]
	v_pk_mul_f32 v[6:7], v[6:7], s[34:35] op_sel_hi:[1,0]
	v_pk_mul_f32 v[2:3], v[2:3], s[34:35] op_sel_hi:[1,0]
	v_pk_mul_f32 v[8:9], v[8:9], s[34:35] op_sel_hi:[1,0]
	v_pk_mul_f32 v[4:5], v[4:5], s[34:35] op_sel_hi:[1,0]
	v_rcp_f32_e32 v14, v14
	v_rcp_f32_e32 v15, v15
	v_rcp_f32_e32 v10, v10
	v_rcp_f32_e32 v11, v11
	v_rcp_f32_e32 v16, v16
	v_rcp_f32_e32 v17, v17
	v_rcp_f32_e32 v12, v12
	v_rcp_f32_e32 v13, v13
	v_exp_f32_e32 v6, v6
	v_exp_f32_e32 v7, v7
	v_exp_f32_e32 v2, v2
	v_exp_f32_e32 v3, v3
	v_exp_f32_e32 v8, v8
	v_exp_f32_e32 v9, v9
	v_exp_f32_e32 v4, v4
	v_exp_f32_e32 v5, v5
	s_waitcnt lgkmcnt(1)
	v_lshlrev_b32_e32 v174, 16, v66
	v_and_b32_e32 v175, 0xffff0000, v66
	v_lshlrev_b32_e32 v66, 16, v67
	v_and_b32_e32 v67, 0xffff0000, v67
	v_lshlrev_b32_e32 v186, 16, v68
	v_and_b32_e32 v187, 0xffff0000, v68
	v_lshlrev_b32_e32 v68, 16, v69
	v_and_b32_e32 v69, 0xffff0000, v69
	v_pk_mul_f32 v[26:27], v[190:191], s[36:37] op_sel_hi:[1,0]
	v_pk_mul_f32 v[28:29], v[188:189], s[36:37] op_sel_hi:[1,0]
	v_pk_mul_f32 v[30:31], v[50:51], s[36:37] op_sel_hi:[1,0]
	v_pk_mul_f32 v[32:33], v[192:193], s[36:37] op_sel_hi:[1,0]
	v_pk_fma_f32 v[14:15], v[14:15], v[28:29], v[174:175]
	v_pk_fma_f32 v[16:17], v[16:17], v[26:27], v[66:67]
	v_pk_fma_f32 v[26:27], v[10:11], v[32:33], v[186:187]
	v_pk_fma_f32 v[28:29], v[12:13], v[30:31], v[68:69]
	s_waitcnt lgkmcnt(0)
	v_lshlrev_b32_e32 v30, 16, v182
	v_and_b32_e32 v31, 0xffff0000, v182
	v_lshlrev_b32_e32 v32, 16, v183
	v_and_b32_e32 v33, 0xffff0000, v183
	v_cvt_pk_f32_fp8_e32 v[68:69], v52
	v_cvt_pk_f32_fp8_sdwa v[174:175], v52 src0_sel:WORD_1
	v_cvt_pk_f32_fp8_e32 v[182:183], v53
	v_cvt_pk_f32_fp8_sdwa v[52:53], v53 src0_sel:WORD_1
	v_pk_add_f32 v[6:7], v[6:7], 1.0 op_sel_hi:[1,0]
	v_pk_add_f32 v[2:3], v[2:3], 1.0 op_sel_hi:[1,0]
	v_pk_add_f32 v[8:9], v[8:9], 1.0 op_sel_hi:[1,0]
	v_pk_add_f32 v[4:5], v[4:5], 1.0 op_sel_hi:[1,0]
	v_rcp_f32_e32 v6, v6
	v_rcp_f32_e32 v7, v7
	v_rcp_f32_e32 v2, v2
	v_rcp_f32_e32 v3, v3
	v_rcp_f32_e32 v8, v8
	v_rcp_f32_e32 v9, v9
	v_rcp_f32_e32 v4, v4
	v_rcp_f32_e32 v5, v5
	v_cvt_pk_bf16_f32 v10, v14, v15
	v_cvt_pk_bf16_f32 v11, v16, v17
	v_cvt_pk_bf16_f32 v12, v26, v27
	v_cvt_pk_bf16_f32 v13, v28, v29
	v_lshlrev_b32_e32 v50, 16, v184
	v_and_b32_e32 v51, 0xffff0000, v184
	v_lshlrev_b32_e32 v66, 16, v185
	v_and_b32_e32 v67, 0xffff0000, v185
	v_pk_mul_f32 v[18:19], v[174:175], s[36:37] op_sel_hi:[1,0]
	v_pk_mul_f32 v[20:21], v[68:69], s[36:37] op_sel_hi:[1,0]
	v_pk_mul_f32 v[22:23], v[52:53], s[36:37] op_sel_hi:[1,0]
	v_pk_mul_f32 v[24:25], v[182:183], s[36:37] op_sel_hi:[1,0]
	v_pk_fma_f32 v[20:21], v[6:7], v[20:21], v[30:31]
	v_pk_fma_f32 v[18:19], v[8:9], v[18:19], v[32:33]
	v_pk_fma_f32 v[24:25], v[2:3], v[24:25], v[50:51]
	v_pk_fma_f32 v[22:23], v[4:5], v[22:23], v[66:67]
	v_cvt_pk_bf16_f32 v2, v20, v21
	v_cvt_pk_bf16_f32 v3, v18, v19
	v_cvt_pk_bf16_f32 v4, v24, v25
	s_add_u32 s41, s66, s50
	v_cvt_pk_bf16_f32 v5, v22, v23
	ds_write_b128 v181, v[10:13]
	ds_write_b128 v181, v[2:5] offset:64
	s_addc_u32 s47, s67, s51
	ds_read_b128 v[2:5], v180
	ds_read_b128 v[6:9], v180 offset:1152
	s_add_u32 s48, s41, s48
	s_addc_u32 s49, s47, s49
	v_lshl_add_u64 v[10:11], s[48:49], 0, v[166:167]
	v_lshl_add_u64 v[10:11], v[10:11], 0, v[164:165]
	s_waitcnt lgkmcnt(1)
	global_store_dwordx4 v[10:11], v[2:5], off nt
	v_mul_f32_e32 v10, v103, v103
	v_fmac_f32_e32 v10, v102, v102
	v_lshl_add_u64 v[2:3], s[48:49], 0, v[168:169]
	v_lshl_add_u64 v[2:3], v[2:3], 0, v[164:165]
	s_waitcnt lgkmcnt(0)
	global_store_dwordx4 v[2:3], v[6:9], off nt
	v_mul_f32_e32 v2, v27, v27
	v_mul_f32_e32 v3, v29, v29
	v_fmac_f32_e32 v2, v26, v26
	v_fmac_f32_e32 v3, v28, v28
	v_add_f32_e32 v2, v2, v3
	v_mul_f32_e32 v3, v15, v15
	v_mul_f32_e32 v4, v17, v17
	v_fmac_f32_e32 v3, v14, v14
	v_fmac_f32_e32 v4, v16, v16
	v_add_f32_e32 v3, v3, v4
	v_add_f32_e32 v2, v3, v2
	v_mul_f32_e32 v3, v25, v25
	v_mul_f32_e32 v4, v23, v23
	v_fmac_f32_e32 v3, v24, v24
	v_fmac_f32_e32 v4, v22, v22
	v_add_f32_e32 v3, v3, v4
	v_mul_f32_e32 v4, v21, v21
	v_mul_f32_e32 v5, v19, v19
	v_fmac_f32_e32 v4, v20, v20
	v_fmac_f32_e32 v5, v18, v18
	v_add_f32_e32 v4, v4, v5
	v_add_f32_e32 v3, v4, v3
	v_add_f32_e32 v2, v2, v3
	v_mul_f32_e32 v3, v47, v47
	v_mul_f32_e32 v4, v49, v49
	v_fmac_f32_e32 v3, v46, v46
	v_fmac_f32_e32 v4, v48, v48
	v_add_f32_e32 v3, v3, v4
	v_mul_f32_e32 v4, v43, v43
	v_mul_f32_e32 v5, v45, v45
	v_fmac_f32_e32 v4, v42, v42
	v_fmac_f32_e32 v5, v44, v44
	v_add_f32_e32 v4, v4, v5
	v_add_f32_e32 v3, v4, v3
	v_mul_f32_e32 v4, v39, v39
	v_mul_f32_e32 v5, v41, v41
	v_fmac_f32_e32 v4, v38, v38
	v_fmac_f32_e32 v5, v40, v40
	v_add_f32_e32 v4, v4, v5
	v_mul_f32_e32 v5, v35, v35
	v_mul_f32_e32 v6, v37, v37
	v_fmac_f32_e32 v5, v34, v34
	v_fmac_f32_e32 v6, v36, v36
	v_add_f32_e32 v5, v5, v6
	v_add_f32_e32 v4, v5, v4
	v_add_f32_e32 v3, v3, v4
	v_mul_f32_e32 v4, v63, v63
	v_mul_f32_e32 v5, v65, v65
	v_fmac_f32_e32 v4, v62, v62
	v_fmac_f32_e32 v5, v64, v64
	v_add_f32_e32 v4, v4, v5
	v_mul_f32_e32 v5, v59, v59
	v_mul_f32_e32 v6, v61, v61
	v_fmac_f32_e32 v5, v58, v58
	v_fmac_f32_e32 v6, v60, v60
	v_add_f32_e32 v5, v5, v6
	v_add_f32_e32 v4, v5, v4
	v_mul_f32_e32 v5, v83, v83
	v_mul_f32_e32 v6, v85, v85
	v_fmac_f32_e32 v5, v82, v82
	v_fmac_f32_e32 v6, v84, v84
	v_add_f32_e32 v5, v5, v6
	v_mul_f32_e32 v6, v55, v55
	v_mul_f32_e32 v7, v57, v57
	v_fmac_f32_e32 v6, v54, v54
	v_fmac_f32_e32 v7, v56, v56
	v_add_f32_e32 v6, v6, v7
	v_add_f32_e32 v5, v6, v5
	v_add_f32_e32 v4, v4, v5
	v_mul_f32_e32 v5, v79, v79
	v_mul_f32_e32 v6, v81, v81
	v_fmac_f32_e32 v5, v78, v78
	v_fmac_f32_e32 v6, v80, v80
	v_add_f32_e32 v5, v5, v6
	v_mul_f32_e32 v6, v75, v75
	v_mul_f32_e32 v7, v77, v77
	v_fmac_f32_e32 v6, v74, v74
	v_fmac_f32_e32 v7, v76, v76
	v_add_f32_e32 v6, v6, v7
	v_add_f32_e32 v5, v6, v5
	v_mul_f32_e32 v6, v99, v99
	v_mul_f32_e32 v7, v101, v101
	v_fmac_f32_e32 v6, v98, v98
	v_fmac_f32_e32 v7, v100, v100
	v_add_f32_e32 v6, v6, v7
	v_mul_f32_e32 v7, v71, v71
	v_mul_f32_e32 v8, v73, v73
	v_fmac_f32_e32 v7, v70, v70
	v_fmac_f32_e32 v8, v72, v72
	v_add_f32_e32 v7, v7, v8
	v_add_f32_e32 v6, v7, v6
	v_add_f32_e32 v5, v5, v6
	v_mul_f32_e32 v6, v97, v97
	v_mul_f32_e32 v7, v95, v95
	v_fmac_f32_e32 v6, v96, v96
	v_fmac_f32_e32 v7, v94, v94
	v_add_f32_e32 v6, v6, v7
	v_mul_f32_e32 v7, v93, v93
	v_mul_f32_e32 v8, v91, v91
	v_fmac_f32_e32 v7, v92, v92
	v_fmac_f32_e32 v8, v90, v90
	v_add_f32_e32 v7, v7, v8
	v_add_f32_e32 v6, v7, v6
	v_mul_f32_e32 v7, v117, v117
	v_mul_f32_e32 v8, v115, v115
	v_fmac_f32_e32 v7, v116, v116
	v_fmac_f32_e32 v8, v114, v114
	v_add_f32_e32 v7, v7, v8
	v_mul_f32_e32 v8, v89, v89
	v_mul_f32_e32 v9, v87, v87
	v_fmac_f32_e32 v8, v88, v88
	v_fmac_f32_e32 v9, v86, v86
	v_add_f32_e32 v8, v8, v9
	v_add_f32_e32 v7, v8, v7
	v_add_f32_e32 v6, v6, v7
	v_mul_f32_e32 v7, v113, v113
	v_mul_f32_e32 v8, v111, v111
	v_fmac_f32_e32 v7, v112, v112
	v_fmac_f32_e32 v8, v110, v110
	v_add_f32_e32 v7, v7, v8
	v_mul_f32_e32 v8, v109, v109
	v_mul_f32_e32 v9, v107, v107
	v_fmac_f32_e32 v8, v108, v108
	v_fmac_f32_e32 v9, v106, v106
	v_add_f32_e32 v8, v8, v9
	v_add_f32_e32 v7, v8, v7
	v_mul_f32_e32 v8, v133, v133
	v_mul_f32_e32 v9, v131, v131
	v_fmac_f32_e32 v8, v132, v132
	v_fmac_f32_e32 v9, v130, v130
	v_add_f32_e32 v8, v8, v9
	v_mul_f32_e32 v9, v105, v105
	v_fmac_f32_e32 v9, v104, v104
	v_add_f32_e32 v9, v9, v10
	v_add_f32_e32 v8, v9, v8
	v_add_f32_e32 v7, v7, v8
	v_mul_f32_e32 v8, v129, v129
	v_mul_f32_e32 v9, v127, v127
	v_fmac_f32_e32 v8, v128, v128
	v_fmac_f32_e32 v9, v126, v126
	v_add_f32_e32 v8, v8, v9
	v_mul_f32_e32 v9, v125, v125
	v_mul_f32_e32 v10, v123, v123
	v_fmac_f32_e32 v9, v124, v124
	v_fmac_f32_e32 v10, v122, v122
	v_add_f32_e32 v9, v9, v10
	v_add_f32_e32 v8, v9, v8
	v_mul_f32_e32 v9, v141, v141
	v_mul_f32_e32 v10, v139, v139
	v_fmac_f32_e32 v9, v140, v140
	v_fmac_f32_e32 v10, v138, v138
	v_add_f32_e32 v9, v9, v10
	v_mul_f32_e32 v10, v121, v121
	v_mul_f32_e32 v11, v119, v119
	v_fmac_f32_e32 v10, v120, v120
	v_fmac_f32_e32 v11, v118, v118
	v_add_f32_e32 v10, v10, v11
	v_add_f32_e32 v9, v10, v9
	v_add_f32_e32 v8, v8, v9
	v_mul_f32_e32 v9, v163, v163
	v_mul_f32_e32 v10, v161, v161
	v_fmac_f32_e32 v9, v162, v162
	v_fmac_f32_e32 v10, v160, v160
	v_add_f32_e32 v9, v9, v10
	v_mul_f32_e32 v10, v145, v145
	v_mul_f32_e32 v11, v143, v143
	v_fmac_f32_e32 v10, v144, v144
	v_fmac_f32_e32 v11, v142, v142
	v_add_f32_e32 v10, v10, v11
	v_add_f32_e32 v9, v10, v9
	v_mul_f32_e32 v10, v173, v173
	v_mul_f32_e32 v11, v171, v171
	v_fmac_f32_e32 v10, v172, v172
	v_fmac_f32_e32 v11, v170, v170
	v_add_f32_e32 v10, v10, v11
	v_mul_f32_e32 v11, v137, v137
	v_mul_f32_e32 v12, v135, v135
	v_fmac_f32_e32 v11, v136, v136
	v_fmac_f32_e32 v12, v134, v134
	v_add_f32_e32 v11, v11, v12
	v_add_f32_e32 v10, v11, v10
	v_add_f32_e32 v9, v9, v10
	v_lshrrev_b32_e32 v10, 2, v178
	s_lshl_b32 s41, s70, 2
	v_and_b32_e32 v10, 12, v10
	v_lshlrev_b32_e32 v11, 4, v179
	s_or_b32 s48, s39, s41
	v_add3_u32 v10, s9, v10, v11
	ds_write2st64_b32 v10, v9, v8 offset1:1
	ds_write2st64_b32 v10, v7, v6 offset0:2 offset1:3
	ds_write2st64_b32 v10, v5, v4 offset0:4 offset1:5
	ds_write2st64_b32 v10, v3, v2 offset0:6 offset1:7
	v_add_u32_e32 v6, s9, v154
	s_ashr_i32 s49, s48, 31
	s_ashr_i32 s47, s46, 31
	s_ashr_i32 s9, s8, 31
	s_lshl_b64 s[48:49], s[48:49], 18
	ds_read_b128 v[2:5], v6
	s_add_u32 s39, s68, s48
	s_addc_u32 s41, s69, s49
	s_lshl_b64 s[46:47], s[46:47], 2
	ds_read_b128 v[6:9], v6 offset:1024
	s_add_u32 s39, s39, s46
	s_addc_u32 s41, s41, s47
	s_lshl_b64 s[8:9], s[8:9], 2
	s_add_u32 s8, s39, s8
	s_waitcnt lgkmcnt(1)
	v_add_f32_e32 v2, v2, v3
	v_add_f32_e32 v3, v4, v5
	s_addc_u32 s9, s41, s9
	v_lshlrev_b32_e32 v10, 2, v177
	v_add_f32_e32 v2, v2, v3
	global_store_dword v10, v2, s[8:9]
	s_waitcnt lgkmcnt(0)
	v_add_f32_e32 v2, v6, v7
	v_add_f32_e32 v3, v8, v9
	v_add_f32_e32 v2, v2, v3
	s_and_b64 vcc, exec, s[6:7]
	s_mov_b64 s[6:7], -1
	global_store_dword v10, v2, s[8:9] offset:512
	s_cbranch_vccnz .LBB0_3571
	v_mov_b32_e32 v2, v0
	s_nop 0
	v_readfirstlane_b32 s6, v2
	s_and_b32 s8, s6, 0xc0
	s_lshl_b32 s6, s38, 8
	s_ashr_i32 s7, s6, 31
	s_lshl_b64 s[6:7], s[6:7], 2
	s_add_u32 s6, s5, s6
	s_addc_u32 s7, s31, s7
	s_lshl_b32 s8, s8, 2
	s_add_u32 s6, s6, s8
	v_lshlrev_b32_e32 v2, 1, v2
	s_addc_u32 s7, s7, 0
	v_and_b32_e32 v6, 0x60, v2
	global_load_dwordx4 v[10:13], v6, s[6:7] offset:16
	global_load_dwordx4 v[14:17], v6, s[6:7]
	global_load_dwordx4 v[2:5], v6, s[6:7] offset:144
	s_nop 0
	global_load_dwordx4 v[6:9], v6, s[6:7] offset:128
	s_andn2_b64 vcc, exec, s[12:13]
	s_cbranch_vccnz .LBB0_3570
	s_barrier
	s_branch .LBB0_3570
